# GEMM epilogue stores carry the nt (streaming) hint so fewer dirty lines wait in L2 for the grid barrier's writeback
# baseline (speedup 1.0000x reference)
.LBB0_181:
	v_lshl_or_b32 v150, s45, 8, v154
	v_lshl_add_u32 v159, s22, 8, v152
	v_ashrrev_i32_e32 v151, 31, v150
	v_mov_b64_e32 v[148:149], s[8:9]
	v_mad_i64_i32 v[160:161], s[24:25], v159, s44, v[148:149]
	v_lshlrev_b64 v[150:151], 1, v[150:151]
	v_lshl_add_u64 v[160:161], v[160:161], 0, v[150:151]
	v_cvt_pk_bf16_f32 v126, v126, v127
	v_cvt_pk_bf16_f32 v127, v128, v129
	v_cvt_pk_bf16_f32 v128, v122, v123
	v_cvt_pk_bf16_f32 v129, v124, v125
	global_store_dwordx4 v[160:161], v[126:129], off nt
	v_cvt_pk_bf16_f32 v114, v114, v115
	v_cvt_pk_bf16_f32 v115, v116, v117
	v_cvt_pk_bf16_f32 v116, v106, v107
	v_or_b32_e32 v106, 16, v159
	v_mad_i64_i32 v[106:107], s[24:25], v106, s44, v[148:149]
	v_cvt_pk_bf16_f32 v117, v108, v109
	global_store_dwordx4 v[160:161], v[114:117], off offset:256 nt
	s_andn2_b64 vcc, exec, s[4:5]
	s_mov_b64 s[4:5], -1
	v_lshl_add_u64 v[114:115], v[106:107], 0, v[150:151]
	v_cvt_pk_bf16_f32 v106, v118, v119
	v_cvt_pk_bf16_f32 v107, v120, v121
	v_cvt_pk_bf16_f32 v108, v110, v111
	v_cvt_pk_bf16_f32 v109, v112, v113
	global_store_dwordx4 v[114:115], v[106:109], off nt
	v_cvt_pk_bf16_f32 v98, v98, v99
	v_cvt_pk_bf16_f32 v99, v100, v101
	v_cvt_pk_bf16_f32 v100, v90, v91
	v_or_b32_e32 v90, 32, v159
	v_mad_i64_i32 v[90:91], s[24:25], v90, s44, v[148:149]
	v_cvt_pk_bf16_f32 v101, v92, v93
	global_store_dwordx4 v[114:115], v[98:101], off offset:256 nt
	s_nop 1
	v_lshl_add_u64 v[98:99], v[90:91], 0, v[150:151]
	v_cvt_pk_bf16_f32 v90, v102, v103
	v_cvt_pk_bf16_f32 v91, v104, v105
	v_cvt_pk_bf16_f32 v92, v94, v95
	v_cvt_pk_bf16_f32 v93, v96, v97
	global_store_dwordx4 v[98:99], v[90:93], off nt
	v_cvt_pk_bf16_f32 v82, v82, v83
	v_cvt_pk_bf16_f32 v83, v84, v85
	v_cvt_pk_bf16_f32 v84, v74, v75
	v_or_b32_e32 v74, 48, v159
	v_mad_i64_i32 v[74:75], s[24:25], v74, s44, v[148:149]
	v_cvt_pk_bf16_f32 v85, v76, v77
	global_store_dwordx4 v[98:99], v[82:85], off offset:256 nt
	s_nop 1
	v_lshl_add_u64 v[82:83], v[74:75], 0, v[150:151]
	v_cvt_pk_bf16_f32 v74, v86, v87
	v_cvt_pk_bf16_f32 v75, v88, v89
	v_cvt_pk_bf16_f32 v76, v78, v79
	v_cvt_pk_bf16_f32 v77, v80, v81
	global_store_dwordx4 v[82:83], v[74:77], off nt
	v_cvt_pk_bf16_f32 v70, v70, v71
	v_cvt_pk_bf16_f32 v71, v72, v73
	v_cvt_pk_bf16_f32 v72, v66, v67
	v_add_u32_e32 v66, 0x80, v159
	v_mad_i64_i32 v[66:67], s[24:25], v66, s44, v[148:149]
	v_lshl_add_u64 v[66:67], v[66:67], 0, v[150:151]
	v_cvt_pk_bf16_f32 v73, v68, v69
	global_store_dwordx4 v[82:83], v[70:73], off offset:256 nt
	v_cvt_pk_bf16_f32 v62, v62, v63
	v_cvt_pk_bf16_f32 v63, v64, v65
	v_cvt_pk_bf16_f32 v64, v58, v59
	v_cvt_pk_bf16_f32 v65, v60, v61
	global_store_dwordx4 v[66:67], v[62:65], off nt
	v_cvt_pk_bf16_f32 v50, v50, v51
	v_cvt_pk_bf16_f32 v51, v52, v53
	v_cvt_pk_bf16_f32 v52, v42, v43
	v_add_u32_e32 v42, 0x90, v159
	v_mad_i64_i32 v[42:43], s[24:25], v42, s44, v[148:149]
	v_cvt_pk_bf16_f32 v53, v44, v45
	global_store_dwordx4 v[66:67], v[50:53], off offset:256 nt
	s_nop 1
	v_lshl_add_u64 v[50:51], v[42:43], 0, v[150:151]
	v_cvt_pk_bf16_f32 v42, v54, v55
	v_cvt_pk_bf16_f32 v43, v56, v57
	v_cvt_pk_bf16_f32 v44, v46, v47
	v_cvt_pk_bf16_f32 v45, v48, v49
	global_store_dwordx4 v[50:51], v[42:45], off nt
	v_cvt_pk_bf16_f32 v34, v34, v35
	v_cvt_pk_bf16_f32 v35, v36, v37
	v_cvt_pk_bf16_f32 v36, v26, v27
	v_add_u32_e32 v26, 0xa0, v159
	v_mad_i64_i32 v[26:27], s[24:25], v26, s44, v[148:149]
	v_cvt_pk_bf16_f32 v37, v28, v29
	global_store_dwordx4 v[50:51], v[34:37], off offset:256 nt
	s_nop 1
	v_lshl_add_u64 v[34:35], v[26:27], 0, v[150:151]
	v_cvt_pk_bf16_f32 v26, v38, v39
	v_cvt_pk_bf16_f32 v27, v40, v41
	v_cvt_pk_bf16_f32 v28, v30, v31
	v_cvt_pk_bf16_f32 v29, v32, v33
	global_store_dwordx4 v[34:35], v[26:29], off nt
	v_cvt_pk_bf16_f32 v18, v18, v19
	v_cvt_pk_bf16_f32 v19, v20, v21
	v_cvt_pk_bf16_f32 v20, v10, v11
	v_add_u32_e32 v10, 0xb0, v159
	v_mad_i64_i32 v[10:11], s[24:25], v10, s44, v[148:149]
	v_cvt_pk_bf16_f32 v21, v12, v13
	global_store_dwordx4 v[34:35], v[18:21], off offset:256 nt
	s_nop 1
	v_lshl_add_u64 v[18:19], v[10:11], 0, v[150:151]
	v_cvt_pk_bf16_f32 v10, v22, v23
	v_cvt_pk_bf16_f32 v11, v24, v25
	v_cvt_pk_bf16_f32 v12, v14, v15
	v_cvt_pk_bf16_f32 v13, v16, v17
	global_store_dwordx4 v[18:19], v[10:13], off nt
	v_cvt_pk_bf16_f32 v6, v6, v7
	v_cvt_pk_bf16_f32 v7, v8, v9
	v_cvt_pk_bf16_f32 v8, v2, v3
	v_cvt_pk_bf16_f32 v9, v4, v5
	global_store_dwordx4 v[18:19], v[6:9], off offset:256 nt
	s_cbranch_vccnz .LBB0_174
	s_andn2_b64 vcc, exec, s[6:7]
	s_cbranch_vccnz .LBB0_173
	s_barrier
	s_branch .LBB0_173

.LBB0_387:
	v_lshl_add_u32 v150, s24, 8, v152
	v_lshl_or_b32 v148, s26, 8, v154
	v_ashrrev_i32_e32 v151, 31, v150
	v_ashrrev_i32_e32 v149, 31, v148
	v_lshlrev_b64 v[160:161], 11, v[150:151]
	v_lshl_add_u64 v[168:169], v[160:161], 0, v[148:149]
	v_lshl_add_u64 v[170:171], v[168:169], 2, s[48:49]
	v_mov_b32_e32 v222, v170
	v_mov_b32_e32 v223, v171
	v_mov_b32_e32 v240, 0x20000
	v_mov_b32_e32 v241, 0
	global_load_dwordx4 v[174:177], v[222:223], off
	global_load_dwordx4 v[178:181], v[222:223], off offset:16
	global_load_dwordx4 v[182:185], v[222:223], off offset:512
	global_load_dwordx4 v[190:193], v[222:223], off offset:528
	v_lshl_add_u64 v[222:223], v[240:241], 0, v[222:223]
	global_load_dwordx4 v[194:197], v[222:223], off
	global_load_dwordx4 v[198:201], v[222:223], off offset:16
	global_load_dwordx4 v[202:205], v[222:223], off offset:512
	global_load_dwordx4 v[206:209], v[222:223], off offset:528
	v_lshl_add_u64 v[222:223], v[240:241], 0, v[222:223]
	global_load_dwordx4 v[210:213], v[222:223], off
	global_load_dwordx4 v[214:217], v[222:223], off offset:16
	global_load_dwordx4 v[218:221], v[222:223], off offset:512
	global_load_dwordx4 v[228:231], v[222:223], off offset:528
	s_nop 0
	s_nop 0
	v_lshl_add_u64 v[168:169], v[168:169], 1, s[50:51]
	s_waitcnt vmcnt(8)
	s_nop 1
	v_pk_mov_b32 v[160:161], v[174:175], v[174:175] op_sel:[0,1]
	v_pk_mov_b32 v[162:163], v[176:177], v[176:177] op_sel:[0,1]
	v_pk_mov_b32 v[164:165], v[178:179], v[178:179] op_sel:[0,1]
	v_pk_mov_b32 v[166:167], v[180:181], v[180:181] op_sel:[0,1]
	v_pk_add_f32 v[128:129], v[128:129], v[162:163]
	v_pk_add_f32 v[172:173], v[126:127], v[160:161]
	v_pk_add_f32 v[166:167], v[124:125], v[166:167]
	v_pk_add_f32 v[164:165], v[122:123], v[164:165]
	v_cvt_pk_bf16_f32 v122, v172, v173
	v_cvt_pk_bf16_f32 v123, v128, v129
	v_mul_f32_e32 v129, v129, v129
	v_cvt_pk_bf16_f32 v124, v164, v165
	v_cvt_pk_bf16_f32 v125, v166, v167
	global_store_dwordx4 v[168:169], v[122:125], off nt
	s_nop 0
	s_nop 0
	s_nop 0
	v_and_b32_e32 v123, 64, v159
	v_mul_f32_e32 v170, v173, v173
	v_mul_f32_e32 v165, v165, v165
	v_mul_f32_e32 v167, v167, v167
	v_xor_b32_e32 v122, 16, v159
	v_add_u32_e32 v123, 64, v123
	v_fmac_f32_e32 v170, v172, v172
	v_fmac_f32_e32 v129, v128, v128
	v_fmac_f32_e32 v165, v164, v164
	v_fmac_f32_e32 v167, v166, v166
	v_cmp_lt_i32_e32 vcc, v122, v123
	v_add_f32_e32 v128, v170, v129
	v_add_f32_e32 v129, v165, v167
	v_cndmask_b32_e32 v122, v159, v122, vcc
	v_add_f32_e32 v128, v128, v129
	v_lshlrev_b32_e32 v122, 2, v122
	s_nop 1
	v_pk_mov_b32 v[124:125], v[182:183], v[182:183] op_sel:[0,1]
	v_pk_mov_b32 v[126:127], v[184:185], v[184:185] op_sel:[0,1]
	v_pk_add_f32 v[120:121], v[120:121], v[126:127]
	v_pk_add_f32 v[118:119], v[118:119], v[124:125]
	s_nop 1
	v_pk_mov_b32 v[160:161], v[190:191], v[190:191] op_sel:[0,1]
	v_pk_mov_b32 v[162:163], v[192:193], v[192:193] op_sel:[0,1]
	v_lshl_add_u64 v[222:223], v[240:241], 0, v[222:223]
	global_load_dwordx4 v[174:177], v[222:223], off
	global_load_dwordx4 v[178:181], v[222:223], off offset:16
	global_load_dwordx4 v[182:185], v[222:223], off offset:512
	global_load_dwordx4 v[190:193], v[222:223], off offset:528
	v_pk_add_f32 v[124:125], v[116:117], v[162:163]
	v_pk_add_f32 v[126:127], v[114:115], v[160:161]
	v_mul_f32_e32 v114, v119, v119
	v_mul_f32_e32 v115, v121, v121
	v_mul_f32_e32 v116, v127, v127
	v_mul_f32_e32 v117, v125, v125
	v_fmac_f32_e32 v114, v118, v118
	v_fmac_f32_e32 v115, v120, v120
	v_fmac_f32_e32 v116, v126, v126
	v_fmac_f32_e32 v117, v124, v124
	v_add_f32_e32 v114, v114, v115
	v_add_f32_e32 v115, v116, v117
	v_add_f32_e32 v114, v114, v115
	v_add_f32_e32 v114, v128, v114
	ds_bpermute_b32 v115, v122, v114
	v_xor_b32_e32 v116, 32, v159
	v_cmp_lt_i32_e32 vcc, v116, v123
	v_cvt_pk_bf16_f32 v118, v118, v119
	v_cvt_pk_bf16_f32 v119, v120, v121
	s_waitcnt lgkmcnt(0)
	v_add_f32_e32 v114, v114, v115
	v_cvt_pk_bf16_f32 v120, v126, v127
	v_cvt_pk_bf16_f32 v121, v124, v125
	v_cndmask_b32_e32 v116, v159, v116, vcc
	v_lshlrev_b32_e32 v116, 2, v116
	ds_bpermute_b32 v115, v116, v114
	global_store_dwordx4 v[168:169], v[118:121], off offset:256 nt
	s_and_saveexec_b64 s[24:25], s[4:5]
	s_cbranch_execz .LBB0_389
	s_waitcnt lgkmcnt(0)
	v_add_f32_e32 v114, v114, v115
	v_fma_f32 v114, v114, s55, 0.5
	v_trunc_f32_e32 v114, v114
	v_mul_f32_e32 v115, 0x2f800000, v114
	v_floor_f32_e32 v115, v115
	v_fmac_f32_e32 v114, 0xcf800000, v115
	v_cvt_u32_f32_e32 v114, v114
	v_cvt_u32_f32_e32 v115, v115
	v_lshl_add_u64 v[118:119], v[150:151], 3, s[10:11]
	global_atomic_add_x2 v[118:119], v[114:115], off
.LBB0_389:
	s_or_b64 exec, exec, s[24:25]
	v_or_b32_e32 v114, 16, v150
	s_waitcnt lgkmcnt(0)
	v_ashrrev_i32_e32 v115, 31, v114
	v_lshlrev_b64 v[118:119], 11, v[114:115]
	v_lshl_add_u64 v[128:129], v[118:119], 0, v[148:149]
	v_lshl_add_u64 v[160:161], v[128:129], 2, s[48:49]
	s_nop 0
	s_nop 0
	v_lshl_add_u64 v[128:129], v[128:129], 1, s[50:51]
	s_waitcnt vmcnt(10)
	s_nop 1
	v_pk_mov_b32 v[118:119], v[194:195], v[194:195] op_sel:[0,1]
	v_pk_mov_b32 v[120:121], v[196:197], v[196:197] op_sel:[0,1]
	v_pk_add_f32 v[120:121], v[112:113], v[120:121]
	v_pk_add_f32 v[118:119], v[110:111], v[118:119]
	s_nop 1
	v_pk_mov_b32 v[124:125], v[198:199], v[198:199] op_sel:[0,1]
	v_pk_mov_b32 v[126:127], v[200:201], v[200:201] op_sel:[0,1]
	v_pk_add_f32 v[126:127], v[108:109], v[126:127]
	v_pk_add_f32 v[124:125], v[106:107], v[124:125]
	v_cvt_pk_bf16_f32 v106, v118, v119
	v_cvt_pk_bf16_f32 v107, v120, v121
	v_mul_f32_e32 v117, v119, v119
	v_cvt_pk_bf16_f32 v108, v124, v125
	v_cvt_pk_bf16_f32 v109, v126, v127
	global_store_dwordx4 v[128:129], v[106:109], off nt
	s_nop 0
	s_nop 0
	s_nop 0
	v_mul_f32_e32 v119, v121, v121
	v_mul_f32_e32 v121, v125, v125
	v_mul_f32_e32 v123, v127, v127
	v_fmac_f32_e32 v117, v118, v118
	v_fmac_f32_e32 v119, v120, v120
	v_fmac_f32_e32 v121, v124, v124
	v_fmac_f32_e32 v123, v126, v126
	v_add_f32_e32 v117, v117, v119
	v_add_f32_e32 v118, v121, v123
	v_add_f32_e32 v117, v117, v118
	s_nop 1
	v_pk_mov_b32 v[106:107], v[202:203], v[202:203] op_sel:[0,1]
	v_pk_mov_b32 v[108:109], v[204:205], v[204:205] op_sel:[0,1]
	v_pk_add_f32 v[104:105], v[104:105], v[108:109]
	v_pk_add_f32 v[102:103], v[102:103], v[106:107]
	s_nop 1
	v_pk_mov_b32 v[110:111], v[206:207], v[206:207] op_sel:[0,1]
	v_pk_mov_b32 v[112:113], v[208:209], v[208:209] op_sel:[0,1]
	v_lshl_add_u64 v[222:223], v[240:241], 2, v[222:223]
	v_lshl_add_u64 v[222:223], v[240:241], 0, v[222:223]
	global_load_dwordx4 v[194:197], v[222:223], off
	global_load_dwordx4 v[198:201], v[222:223], off offset:16
	global_load_dwordx4 v[202:205], v[222:223], off offset:512
	global_load_dwordx4 v[206:209], v[222:223], off offset:528
	v_pk_add_f32 v[106:107], v[100:101], v[112:113]
	v_pk_add_f32 v[108:109], v[98:99], v[110:111]
	v_mul_f32_e32 v98, v103, v103
	v_mul_f32_e32 v99, v105, v105
	v_mul_f32_e32 v100, v109, v109
	v_mul_f32_e32 v101, v107, v107
	v_fmac_f32_e32 v98, v102, v102
	v_fmac_f32_e32 v99, v104, v104
	v_fmac_f32_e32 v100, v108, v108
	v_fmac_f32_e32 v101, v106, v106
	v_add_f32_e32 v98, v98, v99
	v_add_f32_e32 v99, v100, v101
	v_add_f32_e32 v98, v98, v99
	v_add_f32_e32 v98, v117, v98
	ds_bpermute_b32 v99, v122, v98
	v_cvt_pk_bf16_f32 v100, v102, v103
	v_cvt_pk_bf16_f32 v101, v104, v105
	v_cvt_pk_bf16_f32 v102, v108, v109
	v_cvt_pk_bf16_f32 v103, v106, v107
	s_waitcnt lgkmcnt(0)
	v_add_f32_e32 v98, v98, v99
	ds_bpermute_b32 v99, v116, v98
	global_store_dwordx4 v[128:129], v[100:103], off offset:256 nt
	s_and_saveexec_b64 s[24:25], s[4:5]
	s_cbranch_execz .LBB0_391
	s_waitcnt lgkmcnt(0)
	v_add_f32_e32 v98, v98, v99
	v_fma_f32 v98, v98, s55, 0.5
	v_trunc_f32_e32 v98, v98
	v_mul_f32_e32 v99, 0x2f800000, v98
	v_floor_f32_e32 v99, v99
	v_fmac_f32_e32 v98, 0xcf800000, v99
	v_cvt_u32_f32_e32 v98, v98
	v_cvt_u32_f32_e32 v99, v99
	v_lshl_add_u64 v[100:101], v[114:115], 3, s[10:11]
	global_atomic_add_x2 v[100:101], v[98:99], off
.LBB0_391:
	s_or_b64 exec, exec, s[24:25]
	v_or_b32_e32 v98, 32, v150
	s_waitcnt lgkmcnt(0)
	v_ashrrev_i32_e32 v99, 31, v98
	v_lshlrev_b64 v[100:101], 11, v[98:99]
	v_lshl_add_u64 v[108:109], v[100:101], 0, v[148:149]
	v_lshl_add_u64 v[110:111], v[108:109], 2, s[48:49]
	s_nop 0
	s_nop 0
	v_lshl_add_u64 v[108:109], v[108:109], 1, s[50:51]
	s_waitcnt vmcnt(12)
	s_nop 1
	v_pk_mov_b32 v[100:101], v[210:211], v[210:211] op_sel:[0,1]
	v_pk_mov_b32 v[102:103], v[212:213], v[212:213] op_sel:[0,1]
	v_pk_add_f32 v[102:103], v[96:97], v[102:103]
	v_pk_add_f32 v[100:101], v[94:95], v[100:101]
	s_nop 1
	v_pk_mov_b32 v[104:105], v[214:215], v[214:215] op_sel:[0,1]
	v_pk_mov_b32 v[106:107], v[216:217], v[216:217] op_sel:[0,1]
	v_pk_add_f32 v[106:107], v[92:93], v[106:107]
	v_pk_add_f32 v[104:105], v[90:91], v[104:105]
	v_cvt_pk_bf16_f32 v90, v100, v101
	v_cvt_pk_bf16_f32 v91, v102, v103
	v_mul_f32_e32 v101, v101, v101
	v_cvt_pk_bf16_f32 v92, v104, v105
	v_cvt_pk_bf16_f32 v93, v106, v107
	global_store_dwordx4 v[108:109], v[90:93], off nt
	s_nop 0
	s_nop 0
	s_nop 0
	v_mul_f32_e32 v103, v103, v103
	v_mul_f32_e32 v105, v105, v105
	v_mul_f32_e32 v107, v107, v107
	v_fmac_f32_e32 v101, v100, v100
	v_fmac_f32_e32 v103, v102, v102
	v_fmac_f32_e32 v105, v104, v104
	v_fmac_f32_e32 v107, v106, v106
	v_add_f32_e32 v100, v101, v103
	v_add_f32_e32 v101, v105, v107
	v_add_f32_e32 v100, v100, v101
	s_nop 1
	v_pk_mov_b32 v[90:91], v[218:219], v[218:219] op_sel:[0,1]
	v_pk_mov_b32 v[92:93], v[220:221], v[220:221] op_sel:[0,1]
	v_pk_add_f32 v[88:89], v[88:89], v[92:93]
	v_pk_add_f32 v[86:87], v[86:87], v[90:91]
	s_nop 1
	v_pk_mov_b32 v[94:95], v[228:229], v[228:229] op_sel:[0,1]
	v_pk_mov_b32 v[96:97], v[230:231], v[230:231] op_sel:[0,1]
	v_lshl_add_u64 v[222:223], v[240:241], 0, v[222:223]
	global_load_dwordx4 v[210:213], v[222:223], off
	global_load_dwordx4 v[214:217], v[222:223], off offset:16
	global_load_dwordx4 v[218:221], v[222:223], off offset:512
	global_load_dwordx4 v[228:231], v[222:223], off offset:528
	v_pk_add_f32 v[90:91], v[84:85], v[96:97]
	v_pk_add_f32 v[92:93], v[82:83], v[94:95]
	v_mul_f32_e32 v82, v87, v87
	v_mul_f32_e32 v83, v89, v89
	v_mul_f32_e32 v84, v93, v93
	v_mul_f32_e32 v85, v91, v91
	v_fmac_f32_e32 v82, v86, v86
	v_fmac_f32_e32 v83, v88, v88
	v_fmac_f32_e32 v84, v92, v92
	v_fmac_f32_e32 v85, v90, v90
	v_add_f32_e32 v82, v82, v83
	v_add_f32_e32 v83, v84, v85
	v_add_f32_e32 v82, v82, v83
	v_add_f32_e32 v82, v100, v82
	ds_bpermute_b32 v83, v122, v82
	v_cvt_pk_bf16_f32 v84, v86, v87
	v_cvt_pk_bf16_f32 v85, v88, v89
	v_cvt_pk_bf16_f32 v86, v92, v93
	v_cvt_pk_bf16_f32 v87, v90, v91
	s_waitcnt lgkmcnt(0)
	v_add_f32_e32 v82, v82, v83
	ds_bpermute_b32 v83, v116, v82
	global_store_dwordx4 v[108:109], v[84:87], off offset:256 nt
	s_and_saveexec_b64 s[24:25], s[4:5]
	s_cbranch_execz .LBB0_393
	s_waitcnt lgkmcnt(0)
	v_add_f32_e32 v82, v82, v83
	v_fma_f32 v82, v82, s55, 0.5
	v_trunc_f32_e32 v82, v82
	v_mul_f32_e32 v83, 0x2f800000, v82
	v_floor_f32_e32 v83, v83
	v_fmac_f32_e32 v82, 0xcf800000, v83
	v_cvt_u32_f32_e32 v82, v82
	v_cvt_u32_f32_e32 v83, v83
	v_lshl_add_u64 v[84:85], v[98:99], 3, s[10:11]
	global_atomic_add_x2 v[84:85], v[82:83], off
.LBB0_393:
	s_or_b64 exec, exec, s[24:25]
	v_or_b32_e32 v82, 48, v150
	s_waitcnt lgkmcnt(0)
	v_ashrrev_i32_e32 v83, 31, v82
	v_lshlrev_b64 v[84:85], 11, v[82:83]
	v_lshl_add_u64 v[92:93], v[84:85], 0, v[148:149]
	v_lshl_add_u64 v[94:95], v[92:93], 2, s[48:49]
	s_nop 0
	s_nop 0
	v_lshl_add_u64 v[92:93], v[92:93], 1, s[50:51]
	s_waitcnt vmcnt(13)
	s_nop 1
	v_pk_mov_b32 v[84:85], v[174:175], v[174:175] op_sel:[0,1]
	v_pk_mov_b32 v[86:87], v[176:177], v[176:177] op_sel:[0,1]
	v_pk_add_f32 v[86:87], v[80:81], v[86:87]
	v_pk_add_f32 v[84:85], v[78:79], v[84:85]
	s_nop 1
	v_pk_mov_b32 v[88:89], v[178:179], v[178:179] op_sel:[0,1]
	v_pk_mov_b32 v[90:91], v[180:181], v[180:181] op_sel:[0,1]
	v_pk_add_f32 v[90:91], v[76:77], v[90:91]
	v_pk_add_f32 v[88:89], v[74:75], v[88:89]
	v_cvt_pk_bf16_f32 v74, v84, v85
	v_cvt_pk_bf16_f32 v75, v86, v87
	v_mul_f32_e32 v85, v85, v85
	v_cvt_pk_bf16_f32 v76, v88, v89
	v_cvt_pk_bf16_f32 v77, v90, v91
	global_store_dwordx4 v[92:93], v[74:77], off nt
	s_nop 0
	s_nop 0
	s_nop 0
	v_mul_f32_e32 v87, v87, v87
	v_mul_f32_e32 v89, v89, v89
	v_mul_f32_e32 v91, v91, v91
	v_fmac_f32_e32 v85, v84, v84
	v_fmac_f32_e32 v87, v86, v86
	v_fmac_f32_e32 v89, v88, v88
	v_fmac_f32_e32 v91, v90, v90
	v_add_f32_e32 v84, v85, v87
	v_add_f32_e32 v85, v89, v91
	v_add_f32_e32 v84, v84, v85
	s_nop 1
	v_pk_mov_b32 v[74:75], v[182:183], v[182:183] op_sel:[0,1]
	v_pk_mov_b32 v[76:77], v[184:185], v[184:185] op_sel:[0,1]
	v_pk_add_f32 v[72:73], v[72:73], v[76:77]
	v_pk_add_f32 v[70:71], v[70:71], v[74:75]
	s_nop 1
	v_pk_mov_b32 v[78:79], v[190:191], v[190:191] op_sel:[0,1]
	v_pk_mov_b32 v[80:81], v[192:193], v[192:193] op_sel:[0,1]
	v_lshl_add_u64 v[222:223], v[240:241], 0, v[222:223]
	global_load_dwordx4 v[174:177], v[222:223], off
	global_load_dwordx4 v[178:181], v[222:223], off offset:16
	global_load_dwordx4 v[182:185], v[222:223], off offset:512
	global_load_dwordx4 v[190:193], v[222:223], off offset:528
	v_pk_add_f32 v[74:75], v[68:69], v[80:81]
	v_pk_add_f32 v[76:77], v[66:67], v[78:79]
	v_mul_f32_e32 v66, v71, v71
	v_mul_f32_e32 v67, v73, v73
	v_mul_f32_e32 v68, v77, v77
	v_mul_f32_e32 v69, v75, v75
	v_fmac_f32_e32 v66, v70, v70
	v_fmac_f32_e32 v67, v72, v72
	v_fmac_f32_e32 v68, v76, v76
	v_fmac_f32_e32 v69, v74, v74
	v_add_f32_e32 v66, v66, v67
	v_add_f32_e32 v67, v68, v69
	v_add_f32_e32 v66, v66, v67
	v_add_f32_e32 v66, v84, v66
	ds_bpermute_b32 v67, v122, v66
	v_cvt_pk_bf16_f32 v68, v70, v71
	v_cvt_pk_bf16_f32 v69, v72, v73
	v_cvt_pk_bf16_f32 v70, v76, v77
	v_cvt_pk_bf16_f32 v71, v74, v75
	s_waitcnt lgkmcnt(0)
	v_add_f32_e32 v66, v66, v67
	ds_bpermute_b32 v67, v116, v66
	global_store_dwordx4 v[92:93], v[68:71], off offset:256 nt
	s_and_saveexec_b64 s[24:25], s[4:5]
	s_cbranch_execz .LBB0_395
	s_waitcnt lgkmcnt(0)
	v_add_f32_e32 v66, v66, v67
	v_fma_f32 v66, v66, s55, 0.5
	v_trunc_f32_e32 v66, v66
	v_mul_f32_e32 v67, 0x2f800000, v66
	v_floor_f32_e32 v67, v67
	v_fmac_f32_e32 v66, 0xcf800000, v67
	v_cvt_u32_f32_e32 v66, v66
	v_cvt_u32_f32_e32 v67, v67
	v_lshl_add_u64 v[68:69], v[82:83], 3, s[10:11]
	global_atomic_add_x2 v[68:69], v[66:67], off
.LBB0_395:
	s_or_b64 exec, exec, s[24:25]
	v_add_u32_e32 v66, 0x80, v150
	s_waitcnt lgkmcnt(0)
	v_ashrrev_i32_e32 v67, 31, v66
	v_lshlrev_b64 v[68:69], 11, v[66:67]
	v_lshl_add_u64 v[76:77], v[68:69], 0, v[148:149]
	v_lshl_add_u64 v[78:79], v[76:77], 2, s[48:49]
	s_nop 0
	s_nop 0
	v_lshl_add_u64 v[76:77], v[76:77], 1, s[50:51]
	s_waitcnt vmcnt(13)
	s_nop 1
	v_pk_mov_b32 v[68:69], v[194:195], v[194:195] op_sel:[0,1]
	v_pk_mov_b32 v[70:71], v[196:197], v[196:197] op_sel:[0,1]
	v_pk_add_f32 v[70:71], v[64:65], v[70:71]
	v_pk_add_f32 v[68:69], v[62:63], v[68:69]
	s_nop 1
	v_pk_mov_b32 v[72:73], v[198:199], v[198:199] op_sel:[0,1]
	v_pk_mov_b32 v[74:75], v[200:201], v[200:201] op_sel:[0,1]
	v_pk_add_f32 v[74:75], v[60:61], v[74:75]
	v_pk_add_f32 v[72:73], v[58:59], v[72:73]
	v_cvt_pk_bf16_f32 v58, v68, v69
	v_cvt_pk_bf16_f32 v59, v70, v71
	v_mul_f32_e32 v69, v69, v69
	v_cvt_pk_bf16_f32 v60, v72, v73
	v_cvt_pk_bf16_f32 v61, v74, v75
	global_store_dwordx4 v[76:77], v[58:61], off nt
	s_nop 0
	s_nop 0
	s_nop 0
	v_mul_f32_e32 v71, v71, v71
	v_mul_f32_e32 v73, v73, v73
	v_mul_f32_e32 v75, v75, v75
	v_fmac_f32_e32 v69, v68, v68
	v_fmac_f32_e32 v71, v70, v70
	v_fmac_f32_e32 v73, v72, v72
	v_fmac_f32_e32 v75, v74, v74
	v_add_f32_e32 v68, v69, v71
	v_add_f32_e32 v69, v73, v75
	v_add_f32_e32 v68, v68, v69
	s_nop 1
	v_pk_mov_b32 v[58:59], v[202:203], v[202:203] op_sel:[0,1]
	v_pk_mov_b32 v[60:61], v[204:205], v[204:205] op_sel:[0,1]
	v_pk_add_f32 v[56:57], v[56:57], v[60:61]
	v_pk_add_f32 v[54:55], v[54:55], v[58:59]
	s_nop 1
	v_pk_mov_b32 v[62:63], v[206:207], v[206:207] op_sel:[0,1]
	v_pk_mov_b32 v[64:65], v[208:209], v[208:209] op_sel:[0,1]
	v_lshl_add_u64 v[222:223], v[240:241], 0, v[222:223]
	global_load_dwordx4 v[194:197], v[222:223], off
	global_load_dwordx4 v[198:201], v[222:223], off offset:16
	global_load_dwordx4 v[202:205], v[222:223], off offset:512
	global_load_dwordx4 v[206:209], v[222:223], off offset:528
	v_pk_add_f32 v[58:59], v[52:53], v[64:65]
	v_pk_add_f32 v[60:61], v[50:51], v[62:63]
	v_mul_f32_e32 v50, v55, v55
	v_mul_f32_e32 v51, v57, v57
	v_mul_f32_e32 v52, v61, v61
	v_mul_f32_e32 v53, v59, v59
	v_fmac_f32_e32 v50, v54, v54
	v_fmac_f32_e32 v51, v56, v56
	v_fmac_f32_e32 v52, v60, v60
	v_fmac_f32_e32 v53, v58, v58
	v_add_f32_e32 v50, v50, v51
	v_add_f32_e32 v51, v52, v53
	v_add_f32_e32 v50, v50, v51
	v_add_f32_e32 v50, v68, v50
	ds_bpermute_b32 v51, v122, v50
	v_cvt_pk_bf16_f32 v52, v54, v55
	v_cvt_pk_bf16_f32 v53, v56, v57
	v_cvt_pk_bf16_f32 v54, v60, v61
	v_cvt_pk_bf16_f32 v55, v58, v59
	s_waitcnt lgkmcnt(0)
	v_add_f32_e32 v50, v50, v51
	ds_bpermute_b32 v51, v116, v50
	global_store_dwordx4 v[76:77], v[52:55], off offset:256 nt
	s_and_saveexec_b64 s[24:25], s[4:5]
	s_cbranch_execz .LBB0_397
	s_waitcnt lgkmcnt(0)
	v_add_f32_e32 v50, v50, v51
	v_fma_f32 v50, v50, s55, 0.5
	v_trunc_f32_e32 v50, v50
	v_mul_f32_e32 v51, 0x2f800000, v50
	v_floor_f32_e32 v51, v51
	v_fmac_f32_e32 v50, 0xcf800000, v51
	v_cvt_u32_f32_e32 v50, v50
	v_cvt_u32_f32_e32 v51, v51
	v_lshl_add_u64 v[52:53], v[66:67], 3, s[10:11]
	global_atomic_add_x2 v[52:53], v[50:51], off
.LBB0_397:
	s_or_b64 exec, exec, s[24:25]
	v_add_u32_e32 v50, 0x90, v150
	s_waitcnt lgkmcnt(0)
	v_ashrrev_i32_e32 v51, 31, v50
	v_lshlrev_b64 v[52:53], 11, v[50:51]
	v_lshl_add_u64 v[60:61], v[52:53], 0, v[148:149]
	v_lshl_add_u64 v[62:63], v[60:61], 2, s[48:49]
	s_nop 0
	s_nop 0
	v_lshl_add_u64 v[60:61], v[60:61], 1, s[50:51]
	s_waitcnt vmcnt(13)
	s_nop 1
	v_pk_mov_b32 v[52:53], v[210:211], v[210:211] op_sel:[0,1]
	v_pk_mov_b32 v[54:55], v[212:213], v[212:213] op_sel:[0,1]
	v_pk_add_f32 v[54:55], v[48:49], v[54:55]
	v_pk_add_f32 v[52:53], v[46:47], v[52:53]
	s_nop 1
	v_pk_mov_b32 v[56:57], v[214:215], v[214:215] op_sel:[0,1]
	v_pk_mov_b32 v[58:59], v[216:217], v[216:217] op_sel:[0,1]
	v_pk_add_f32 v[58:59], v[44:45], v[58:59]
	v_pk_add_f32 v[56:57], v[42:43], v[56:57]
	v_cvt_pk_bf16_f32 v42, v52, v53
	v_cvt_pk_bf16_f32 v43, v54, v55
	v_mul_f32_e32 v53, v53, v53
	v_cvt_pk_bf16_f32 v44, v56, v57
	v_cvt_pk_bf16_f32 v45, v58, v59
	global_store_dwordx4 v[60:61], v[42:45], off nt
	s_nop 0
	s_nop 0
	s_nop 0
	v_mul_f32_e32 v55, v55, v55
	v_mul_f32_e32 v57, v57, v57
	v_mul_f32_e32 v59, v59, v59
	v_fmac_f32_e32 v53, v52, v52
	v_fmac_f32_e32 v55, v54, v54
	v_fmac_f32_e32 v57, v56, v56
	v_fmac_f32_e32 v59, v58, v58
	v_add_f32_e32 v52, v53, v55
	v_add_f32_e32 v53, v57, v59
	v_add_f32_e32 v52, v52, v53
	s_nop 1
	v_pk_mov_b32 v[42:43], v[218:219], v[218:219] op_sel:[0,1]
	v_pk_mov_b32 v[44:45], v[220:221], v[220:221] op_sel:[0,1]
	v_pk_add_f32 v[40:41], v[40:41], v[44:45]
	v_pk_add_f32 v[38:39], v[38:39], v[42:43]
	s_nop 1
	v_pk_mov_b32 v[46:47], v[228:229], v[228:229] op_sel:[0,1]
	v_pk_mov_b32 v[48:49], v[230:231], v[230:231] op_sel:[0,1]
	v_pk_add_f32 v[42:43], v[36:37], v[48:49]
	v_pk_add_f32 v[44:45], v[34:35], v[46:47]
	v_mul_f32_e32 v34, v39, v39
	v_mul_f32_e32 v35, v41, v41
	v_mul_f32_e32 v36, v45, v45
	v_mul_f32_e32 v37, v43, v43
	v_fmac_f32_e32 v34, v38, v38
	v_fmac_f32_e32 v35, v40, v40
	v_fmac_f32_e32 v36, v44, v44
	v_fmac_f32_e32 v37, v42, v42
	v_add_f32_e32 v34, v34, v35
	v_add_f32_e32 v35, v36, v37
	v_add_f32_e32 v34, v34, v35
	v_add_f32_e32 v34, v52, v34
	ds_bpermute_b32 v35, v122, v34
	v_cvt_pk_bf16_f32 v36, v38, v39
	v_cvt_pk_bf16_f32 v37, v40, v41
	v_cvt_pk_bf16_f32 v38, v44, v45
	v_cvt_pk_bf16_f32 v39, v42, v43
	s_waitcnt lgkmcnt(0)
	v_add_f32_e32 v34, v34, v35
	ds_bpermute_b32 v35, v116, v34
	global_store_dwordx4 v[60:61], v[36:39], off offset:256 nt
	s_and_saveexec_b64 s[24:25], s[4:5]
	s_cbranch_execz .LBB0_399
	s_waitcnt lgkmcnt(0)
	v_add_f32_e32 v34, v34, v35
	v_fma_f32 v34, v34, s55, 0.5
	v_trunc_f32_e32 v34, v34
	v_mul_f32_e32 v35, 0x2f800000, v34
	v_floor_f32_e32 v35, v35
	v_fmac_f32_e32 v34, 0xcf800000, v35
	v_cvt_u32_f32_e32 v34, v34
	v_cvt_u32_f32_e32 v35, v35
	v_lshl_add_u64 v[36:37], v[50:51], 3, s[10:11]
	global_atomic_add_x2 v[36:37], v[34:35], off
.LBB0_399:
	s_or_b64 exec, exec, s[24:25]
	v_add_u32_e32 v34, 0xa0, v150
	s_waitcnt lgkmcnt(0)
	v_ashrrev_i32_e32 v35, 31, v34
	v_lshlrev_b64 v[36:37], 11, v[34:35]
	v_lshl_add_u64 v[44:45], v[36:37], 0, v[148:149]
	v_lshl_add_u64 v[46:47], v[44:45], 2, s[48:49]
	s_nop 0
	s_nop 0
	v_lshl_add_u64 v[44:45], v[44:45], 1, s[50:51]
	s_waitcnt vmcnt(9)
	s_nop 1
	v_pk_mov_b32 v[36:37], v[174:175], v[174:175] op_sel:[0,1]
	v_pk_mov_b32 v[38:39], v[176:177], v[176:177] op_sel:[0,1]
	v_pk_add_f32 v[38:39], v[32:33], v[38:39]
	v_pk_add_f32 v[36:37], v[30:31], v[36:37]
	s_nop 1
	v_pk_mov_b32 v[40:41], v[178:179], v[178:179] op_sel:[0,1]
	v_pk_mov_b32 v[42:43], v[180:181], v[180:181] op_sel:[0,1]
	v_pk_add_f32 v[42:43], v[28:29], v[42:43]
	v_pk_add_f32 v[40:41], v[26:27], v[40:41]
	v_cvt_pk_bf16_f32 v26, v36, v37
	v_cvt_pk_bf16_f32 v27, v38, v39
	v_mul_f32_e32 v37, v37, v37
	v_cvt_pk_bf16_f32 v28, v40, v41
	v_cvt_pk_bf16_f32 v29, v42, v43
	global_store_dwordx4 v[44:45], v[26:29], off nt
	s_nop 0
	s_nop 0
	s_nop 0
	v_mul_f32_e32 v39, v39, v39
	v_mul_f32_e32 v41, v41, v41
	v_mul_f32_e32 v43, v43, v43
	v_fmac_f32_e32 v37, v36, v36
	v_fmac_f32_e32 v39, v38, v38
	v_fmac_f32_e32 v41, v40, v40
	v_fmac_f32_e32 v43, v42, v42
	v_add_f32_e32 v36, v37, v39
	v_add_f32_e32 v37, v41, v43
	v_add_f32_e32 v36, v36, v37
	s_nop 1
	v_pk_mov_b32 v[26:27], v[182:183], v[182:183] op_sel:[0,1]
	v_pk_mov_b32 v[28:29], v[184:185], v[184:185] op_sel:[0,1]
	v_pk_add_f32 v[24:25], v[24:25], v[28:29]
	v_pk_add_f32 v[22:23], v[22:23], v[26:27]
	s_nop 1
	v_pk_mov_b32 v[30:31], v[190:191], v[190:191] op_sel:[0,1]
	v_pk_mov_b32 v[32:33], v[192:193], v[192:193] op_sel:[0,1]
	v_pk_add_f32 v[26:27], v[20:21], v[32:33]
	v_pk_add_f32 v[28:29], v[18:19], v[30:31]
	v_mul_f32_e32 v18, v23, v23
	v_mul_f32_e32 v19, v25, v25
	v_mul_f32_e32 v20, v29, v29
	v_mul_f32_e32 v21, v27, v27
	v_fmac_f32_e32 v18, v22, v22
	v_fmac_f32_e32 v19, v24, v24
	v_fmac_f32_e32 v20, v28, v28
	v_fmac_f32_e32 v21, v26, v26
	v_add_f32_e32 v18, v18, v19
	v_add_f32_e32 v19, v20, v21
	v_add_f32_e32 v18, v18, v19
	v_add_f32_e32 v18, v36, v18
	ds_bpermute_b32 v19, v122, v18
	v_cvt_pk_bf16_f32 v20, v22, v23
	v_cvt_pk_bf16_f32 v21, v24, v25
	v_cvt_pk_bf16_f32 v22, v28, v29
	v_cvt_pk_bf16_f32 v23, v26, v27
	s_waitcnt lgkmcnt(0)
	v_add_f32_e32 v18, v18, v19
	ds_bpermute_b32 v19, v116, v18
	global_store_dwordx4 v[44:45], v[20:23], off offset:256 nt
	s_and_saveexec_b64 s[24:25], s[4:5]
	s_cbranch_execz .LBB0_401
	s_waitcnt lgkmcnt(0)
	v_add_f32_e32 v18, v18, v19
	v_fma_f32 v18, v18, s55, 0.5
	v_trunc_f32_e32 v18, v18
	v_mul_f32_e32 v19, 0x2f800000, v18
	v_floor_f32_e32 v19, v19
	v_fmac_f32_e32 v18, 0xcf800000, v19
	v_cvt_u32_f32_e32 v18, v18
	v_cvt_u32_f32_e32 v19, v19
	v_lshl_add_u64 v[20:21], v[34:35], 3, s[10:11]
	global_atomic_add_x2 v[20:21], v[18:19], off
.LBB0_401:
	s_or_b64 exec, exec, s[24:25]
	v_add_u32_e32 v18, 0xb0, v150
	s_waitcnt lgkmcnt(0)
	v_ashrrev_i32_e32 v19, 31, v18
	v_lshlrev_b64 v[20:21], 11, v[18:19]
	v_lshl_add_u64 v[28:29], v[20:21], 0, v[148:149]
	v_lshl_add_u64 v[30:31], v[28:29], 2, s[48:49]
	s_nop 0
	s_nop 0
	v_lshl_add_u64 v[28:29], v[28:29], 1, s[50:51]
	s_waitcnt vmcnt(5)
	s_nop 1
	v_pk_mov_b32 v[20:21], v[194:195], v[194:195] op_sel:[0,1]
	v_pk_mov_b32 v[22:23], v[196:197], v[196:197] op_sel:[0,1]
	v_pk_add_f32 v[22:23], v[16:17], v[22:23]
	v_pk_add_f32 v[20:21], v[14:15], v[20:21]
	s_nop 1
	v_pk_mov_b32 v[24:25], v[198:199], v[198:199] op_sel:[0,1]
	v_pk_mov_b32 v[26:27], v[200:201], v[200:201] op_sel:[0,1]
	v_pk_add_f32 v[26:27], v[12:13], v[26:27]
	v_pk_add_f32 v[24:25], v[10:11], v[24:25]
	v_cvt_pk_bf16_f32 v10, v20, v21
	v_cvt_pk_bf16_f32 v11, v22, v23
	v_mul_f32_e32 v21, v21, v21
	v_cvt_pk_bf16_f32 v12, v24, v25
	v_cvt_pk_bf16_f32 v13, v26, v27
	global_store_dwordx4 v[28:29], v[10:13], off nt
	s_nop 0
	s_nop 0
	s_nop 0
	v_mul_f32_e32 v23, v23, v23
	v_mul_f32_e32 v25, v25, v25
	v_mul_f32_e32 v27, v27, v27
	v_fmac_f32_e32 v21, v20, v20
	v_fmac_f32_e32 v23, v22, v22
	v_fmac_f32_e32 v25, v24, v24
	v_fmac_f32_e32 v27, v26, v26
	v_add_f32_e32 v20, v21, v23
	v_add_f32_e32 v21, v25, v27
	v_add_f32_e32 v20, v20, v21
	s_nop 1
	v_pk_mov_b32 v[10:11], v[202:203], v[202:203] op_sel:[0,1]
	v_pk_mov_b32 v[12:13], v[204:205], v[204:205] op_sel:[0,1]
	v_pk_add_f32 v[8:9], v[8:9], v[12:13]
	v_pk_add_f32 v[6:7], v[6:7], v[10:11]
	s_nop 1
	v_pk_mov_b32 v[14:15], v[206:207], v[206:207] op_sel:[0,1]
	v_pk_mov_b32 v[16:17], v[208:209], v[208:209] op_sel:[0,1]
	v_pk_add_f32 v[10:11], v[4:5], v[16:17]
	v_pk_add_f32 v[12:13], v[2:3], v[14:15]
	v_mul_f32_e32 v2, v7, v7
	v_mul_f32_e32 v3, v9, v9
	v_mul_f32_e32 v4, v13, v13
	v_mul_f32_e32 v5, v11, v11
	v_fmac_f32_e32 v2, v6, v6
	v_fmac_f32_e32 v3, v8, v8
	v_fmac_f32_e32 v4, v12, v12
	v_fmac_f32_e32 v5, v10, v10
	v_add_f32_e32 v2, v2, v3
	v_add_f32_e32 v3, v4, v5
	v_add_f32_e32 v2, v2, v3
	v_add_f32_e32 v2, v20, v2
	ds_bpermute_b32 v3, v122, v2
	v_cvt_pk_bf16_f32 v4, v6, v7
	v_cvt_pk_bf16_f32 v5, v8, v9
	v_cvt_pk_bf16_f32 v6, v12, v13
	v_cvt_pk_bf16_f32 v7, v10, v11
	s_waitcnt lgkmcnt(0)
	v_add_f32_e32 v2, v2, v3
	ds_bpermute_b32 v3, v116, v2
	global_store_dwordx4 v[28:29], v[4:7], off offset:256 nt
	s_and_saveexec_b64 s[24:25], s[4:5]
	s_cbranch_execz .LBB0_403
	s_waitcnt lgkmcnt(0)
	v_add_f32_e32 v2, v2, v3
	v_fma_f32 v2, v2, s55, 0.5
	v_trunc_f32_e32 v2, v2
	v_mul_f32_e32 v3, 0x2f800000, v2
	v_floor_f32_e32 v3, v3
	v_fmac_f32_e32 v2, 0xcf800000, v3
	v_cvt_u32_f32_e32 v2, v2
	v_cvt_u32_f32_e32 v3, v3
	v_lshl_add_u64 v[4:5], v[18:19], 3, s[10:11]
	global_atomic_add_x2 v[4:5], v[2:3], off

.LBB0_474:
	v_lshl_add_u32 v152, s24, 8, v156
	v_ashrrev_i32_e32 v153, 31, v152
	v_lshl_add_u64 v[154:155], v[152:153], 3, s[10:11]
	global_load_dwordx2 v[166:167], v[154:155], off
	global_load_dwordx2 v[178:179], v[154:155], off offset:128
	global_load_dwordx2 v[180:181], v[154:155], off offset:256
	global_load_dwordx2 v[182:183], v[154:155], off offset:384
	global_load_dwordx2 v[184:185], v[154:155], off offset:1024
	global_load_dwordx2 v[186:187], v[154:155], off offset:1152
	global_load_dwordx2 v[188:189], v[154:155], off offset:1280
	global_load_dwordx2 v[190:191], v[154:155], off offset:1408
	v_pk_mul_f32 v[126:127], v[118:119], v[126:127]
	v_pk_mul_f32 v[122:123], v[114:115], v[122:123]
	v_pk_mul_f32 v[128:129], v[120:121], v[128:129]
	v_pk_mul_f32 v[124:125], v[116:117], v[124:125]
	v_mov_b32_e32 v168, 0
	v_mov_b32_e32 v169, 0
	v_lshl_or_b32 v148, s54, 7, v159
	v_mov_b64_e32 v[150:151], s[8:9]
	v_or_b32_e32 v170, 16, v152
	v_ashrrev_i32_e32 v171, 31, v170
	v_pk_mul_f32 v[110:111], v[102:103], v[110:111]
	v_pk_mul_f32 v[106:107], v[98:99], v[106:107]
	v_pk_mul_f32 v[112:113], v[104:105], v[112:113]
	v_pk_mul_f32 v[108:109], v[100:101], v[108:109]
	v_pk_mul_f32 v[94:95], v[86:87], v[94:95]
	v_pk_mul_f32 v[90:91], v[82:83], v[90:91]
	v_pk_mul_f32 v[96:97], v[88:89], v[96:97]
	v_pk_mul_f32 v[92:93], v[84:85], v[92:93]
	v_pk_mul_f32 v[78:79], v[74:75], v[78:79]
	v_pk_mul_f32 v[66:67], v[70:71], v[66:67]
	v_pk_mul_f32 v[80:81], v[76:77], v[80:81]
	v_pk_mul_f32 v[68:69], v[72:73], v[68:69]
	v_pk_mul_f32 v[62:63], v[58:59], v[62:63]
	v_pk_mul_f32 v[50:51], v[54:55], v[50:51]
	v_pk_mul_f32 v[64:65], v[60:61], v[64:65]
	v_pk_mul_f32 v[52:53], v[56:57], v[52:53]
	v_pk_mul_f32 v[46:47], v[42:43], v[46:47]
	v_pk_mul_f32 v[34:35], v[38:39], v[34:35]
	v_pk_mul_f32 v[48:49], v[44:45], v[48:49]
	v_pk_mul_f32 v[36:37], v[40:41], v[36:37]
	v_pk_mul_f32 v[30:31], v[26:27], v[30:31]
	v_pk_mul_f32 v[18:19], v[22:23], v[18:19]
	v_pk_mul_f32 v[32:33], v[28:29], v[32:33]
	v_pk_mul_f32 v[20:21], v[24:25], v[20:21]
	v_pk_mul_f32 v[14:15], v[6:7], v[14:15]
	v_pk_mul_f32 v[10:11], v[2:3], v[10:11]
	v_pk_mul_f32 v[16:17], v[8:9], v[16:17]
	v_pk_mul_f32 v[12:13], v[4:5], v[12:13]
	s_andn2_b64 vcc, exec, s[4:5]
	s_mov_b64 s[4:5], -1
	s_waitcnt vmcnt(7)
	v_ffbh_u32_e32 v149, v167
	v_min_u32_e32 v153, 32, v149
	v_lshlrev_b64 v[166:167], v153, v[166:167]
	v_min_u32_e32 v149, 1, v166
	v_or_b32_e32 v149, v167, v149
	v_cvt_f32_u32_e32 v165, v149
	v_sub_u32_e32 v153, 32, v153
	v_ashrrev_i32_e32 v149, 31, v148
	v_mad_i64_i32 v[166:167], s[26:27], v152, s48, v[150:151]
	v_ldexp_f32 v153, v165, v153
	v_fmamk_f32 v153, v153, 0x30000000, v163
	v_rsq_f32_e32 v165, v153
	v_mul_f32_e32 v172, 0x3e000000, v153
	v_mul_f32_e32 v174, 0xbfb8aa3b, v165
	v_pk_mul_f32 v[118:119], v[118:119], v[174:175] op_sel_hi:[1,0]
	v_pk_mul_f32 v[114:115], v[114:115], v[174:175] op_sel_hi:[1,0]
	v_exp_f32_e32 v118, v118
	v_exp_f32_e32 v119, v119
	v_exp_f32_e32 v114, v114
	v_exp_f32_e32 v115, v115
	v_pk_mul_f32 v[120:121], v[120:121], v[174:175] op_sel_hi:[1,0]
	v_pk_mul_f32 v[116:117], v[116:117], v[174:175] op_sel_hi:[1,0]
	v_exp_f32_e32 v120, v120
	v_exp_f32_e32 v121, v121
	v_exp_f32_e32 v116, v116
	v_exp_f32_e32 v117, v117
	v_pk_fma_f32 v[118:119], v[172:173], v[118:119], v[172:173] op_sel_hi:[0,1,0]
	v_pk_fma_f32 v[114:115], v[172:173], v[114:115], v[172:173] op_sel_hi:[0,1,0]
	v_rcp_f32_e32 v118, v118
	v_rcp_f32_e32 v119, v119
	v_rcp_f32_e32 v114, v114
	v_rcp_f32_e32 v115, v115
	v_pk_fma_f32 v[120:121], v[172:173], v[120:121], v[172:173] op_sel_hi:[0,1,0]
	v_pk_fma_f32 v[116:117], v[172:173], v[116:117], v[172:173] op_sel_hi:[0,1,0]
	v_rcp_f32_e32 v120, v120
	v_rcp_f32_e32 v121, v121
	v_rcp_f32_e32 v116, v116
	v_rcp_f32_e32 v117, v117
	v_pk_mul_f32 v[118:119], v[126:127], v[118:119]
	v_pk_mul_f32 v[114:115], v[122:123], v[114:115]
	v_med3_f32 v118, v118, s49, v164
	v_med3_f32 v119, v119, s49, v164
	v_med3_f32 v114, v114, s49, v164
	v_med3_f32 v115, v115, s49, v164
	v_cvt_pk_fp8_f32 v168, v118, v119
	v_cvt_pk_fp8_f32 v169, v114, v115
	v_pk_mul_f32 v[120:121], v[128:129], v[120:121]
	v_pk_mul_f32 v[116:117], v[124:125], v[116:117]
	v_med3_f32 v120, v120, s49, v164
	v_med3_f32 v121, v121, s49, v164
	v_med3_f32 v114, v116, s49, v164
	v_med3_f32 v115, v117, s49, v164
	v_cvt_pk_fp8_f32 v168, v120, v121 op_sel:[0,0,1]
	v_cvt_pk_fp8_f32 v169, v114, v115 op_sel:[0,0,1]
	v_lshl_add_u64 v[114:115], v[166:167], 0, v[148:149]
	v_lshl_add_u64 v[116:117], v[170:171], 3, s[10:11]
	global_store_dwordx2 v[114:115], v[168:169], off nt
	s_nop 0
	v_mov_b32_e32 v116, 0
	s_waitcnt vmcnt(7)
	v_mov_b32_e32 v114, v178
	v_mov_b32_e32 v115, v179
	v_ffbh_u32_e32 v117, v115
	v_min_u32_e32 v118, 32, v117
	v_lshlrev_b64 v[114:115], v118, v[114:115]
	v_min_u32_e32 v114, 1, v114
	v_or_b32_e32 v114, v115, v114
	v_cvt_f32_u32_e32 v115, v114
	v_sub_u32_e32 v118, 32, v118
	v_mov_b32_e32 v117, 0
	v_or_b32_e32 v114, 32, v152
	v_ldexp_f32 v115, v115, v118
	v_fmamk_f32 v115, v115, 0x30000000, v163
	v_rsq_f32_e32 v121, v115
	v_mul_f32_e32 v120, 0x3e000000, v115
	v_mad_i64_i32 v[118:119], s[26:27], v170, s48, v[150:151]
	v_mul_f32_e32 v122, 0xbfb8aa3b, v121
	v_pk_mul_f32 v[102:103], v[102:103], v[122:123] op_sel_hi:[1,0]
	v_pk_mul_f32 v[98:99], v[98:99], v[122:123] op_sel_hi:[1,0]
	v_exp_f32_e32 v102, v102
	v_exp_f32_e32 v103, v103
	v_exp_f32_e32 v98, v98
	v_exp_f32_e32 v99, v99
	v_pk_mul_f32 v[104:105], v[104:105], v[122:123] op_sel_hi:[1,0]
	v_pk_mul_f32 v[100:101], v[100:101], v[122:123] op_sel_hi:[1,0]
	v_exp_f32_e32 v104, v104
	v_exp_f32_e32 v105, v105
	v_exp_f32_e32 v100, v100
	v_exp_f32_e32 v101, v101
	v_pk_fma_f32 v[102:103], v[120:121], v[102:103], v[120:121] op_sel_hi:[0,1,0]
	v_pk_fma_f32 v[98:99], v[120:121], v[98:99], v[120:121] op_sel_hi:[0,1,0]
	v_rcp_f32_e32 v102, v102
	v_rcp_f32_e32 v103, v103
	v_rcp_f32_e32 v98, v98
	v_rcp_f32_e32 v99, v99
	v_pk_fma_f32 v[104:105], v[120:121], v[104:105], v[120:121] op_sel_hi:[0,1,0]
	v_pk_fma_f32 v[100:101], v[120:121], v[100:101], v[120:121] op_sel_hi:[0,1,0]
	v_rcp_f32_e32 v104, v104
	v_rcp_f32_e32 v105, v105
	v_rcp_f32_e32 v100, v100
	v_rcp_f32_e32 v101, v101
	v_pk_mul_f32 v[102:103], v[110:111], v[102:103]
	v_pk_mul_f32 v[98:99], v[106:107], v[98:99]
	v_med3_f32 v102, v102, s49, v164
	v_med3_f32 v103, v103, s49, v164
	v_med3_f32 v98, v98, s49, v164
	v_med3_f32 v99, v99, s49, v164
	v_cvt_pk_fp8_f32 v116, v102, v103
	v_cvt_pk_fp8_f32 v117, v98, v99
	v_pk_mul_f32 v[104:105], v[112:113], v[104:105]
	v_pk_mul_f32 v[100:101], v[108:109], v[100:101]
	v_med3_f32 v104, v104, s49, v164
	v_med3_f32 v105, v105, s49, v164
	v_med3_f32 v98, v100, s49, v164
	v_med3_f32 v99, v101, s49, v164
	v_cvt_pk_fp8_f32 v116, v104, v105 op_sel:[0,0,1]
	v_cvt_pk_fp8_f32 v117, v98, v99 op_sel:[0,0,1]
	v_ashrrev_i32_e32 v115, 31, v114
	v_lshl_add_u64 v[98:99], v[118:119], 0, v[148:149]
	v_lshl_add_u64 v[100:101], v[114:115], 3, s[10:11]
	global_store_dwordx2 v[98:99], v[116:117], off nt
	s_nop 0
	v_mov_b32_e32 v100, 0
	s_waitcnt vmcnt(7)
	v_mov_b32_e32 v98, v180
	v_mov_b32_e32 v99, v181
	v_ffbh_u32_e32 v101, v99
	v_min_u32_e32 v102, 32, v101
	v_lshlrev_b64 v[98:99], v102, v[98:99]
	v_min_u32_e32 v98, 1, v98
	v_or_b32_e32 v98, v99, v98
	v_cvt_f32_u32_e32 v99, v98
	v_sub_u32_e32 v102, 32, v102
	v_mov_b32_e32 v101, 0
	v_or_b32_e32 v98, 48, v152
	v_ldexp_f32 v99, v99, v102
	v_fmamk_f32 v99, v99, 0x30000000, v163
	v_rsq_f32_e32 v105, v99
	v_mul_f32_e32 v104, 0x3e000000, v99
	v_mad_i64_i32 v[102:103], s[26:27], v114, s48, v[150:151]
	v_mul_f32_e32 v106, 0xbfb8aa3b, v105
	v_pk_mul_f32 v[86:87], v[86:87], v[106:107] op_sel_hi:[1,0]
	v_pk_mul_f32 v[82:83], v[82:83], v[106:107] op_sel_hi:[1,0]
	v_exp_f32_e32 v86, v86
	v_exp_f32_e32 v87, v87
	v_exp_f32_e32 v82, v82
	v_exp_f32_e32 v83, v83
	v_pk_mul_f32 v[88:89], v[88:89], v[106:107] op_sel_hi:[1,0]
	v_pk_mul_f32 v[84:85], v[84:85], v[106:107] op_sel_hi:[1,0]
	v_exp_f32_e32 v88, v88
	v_exp_f32_e32 v89, v89
	v_exp_f32_e32 v84, v84
	v_exp_f32_e32 v85, v85
	v_pk_fma_f32 v[86:87], v[104:105], v[86:87], v[104:105] op_sel_hi:[0,1,0]
	v_pk_fma_f32 v[82:83], v[104:105], v[82:83], v[104:105] op_sel_hi:[0,1,0]
	v_rcp_f32_e32 v86, v86
	v_rcp_f32_e32 v87, v87
	v_rcp_f32_e32 v82, v82
	v_rcp_f32_e32 v83, v83
	v_pk_fma_f32 v[88:89], v[104:105], v[88:89], v[104:105] op_sel_hi:[0,1,0]
	v_pk_fma_f32 v[84:85], v[104:105], v[84:85], v[104:105] op_sel_hi:[0,1,0]
	v_rcp_f32_e32 v88, v88
	v_rcp_f32_e32 v89, v89
	v_rcp_f32_e32 v84, v84
	v_rcp_f32_e32 v85, v85
	v_pk_mul_f32 v[86:87], v[94:95], v[86:87]
	v_pk_mul_f32 v[82:83], v[90:91], v[82:83]
	v_med3_f32 v86, v86, s49, v164
	v_med3_f32 v87, v87, s49, v164
	v_med3_f32 v82, v82, s49, v164
	v_med3_f32 v83, v83, s49, v164
	v_cvt_pk_fp8_f32 v100, v86, v87
	v_cvt_pk_fp8_f32 v101, v82, v83
	v_pk_mul_f32 v[88:89], v[96:97], v[88:89]
	v_pk_mul_f32 v[84:85], v[92:93], v[84:85]
	v_med3_f32 v88, v88, s49, v164
	v_med3_f32 v89, v89, s49, v164
	v_med3_f32 v82, v84, s49, v164
	v_med3_f32 v83, v85, s49, v164
	v_cvt_pk_fp8_f32 v100, v88, v89 op_sel:[0,0,1]
	v_cvt_pk_fp8_f32 v101, v82, v83 op_sel:[0,0,1]
	v_ashrrev_i32_e32 v99, 31, v98
	v_lshl_add_u64 v[82:83], v[102:103], 0, v[148:149]
	v_lshl_add_u64 v[84:85], v[98:99], 3, s[10:11]
	global_store_dwordx2 v[82:83], v[100:101], off nt
	s_nop 0
	s_waitcnt vmcnt(7)
	v_mov_b32_e32 v82, v182
	v_mov_b32_e32 v83, v183
	v_ffbh_u32_e32 v84, v83
	v_min_u32_e32 v84, 32, v84
	v_lshlrev_b64 v[82:83], v84, v[82:83]
	v_min_u32_e32 v82, 1, v82
	v_or_b32_e32 v82, v83, v82
	v_cvt_f32_u32_e32 v82, v82
	v_sub_u32_e32 v83, 32, v84
	v_ldexp_f32 v82, v82, v83
	v_fmamk_f32 v84, v82, 0x30000000, v163
	v_rsq_f32_e32 v85, v84
	v_mul_f32_e32 v84, 0x3e000000, v84
	v_mov_b32_e32 v82, 0
	v_mov_b32_e32 v83, 0
	v_mul_f32_e32 v86, 0xbfb8aa3b, v85
	v_pk_mul_f32 v[74:75], v[74:75], v[86:87] op_sel_hi:[1,0]
	v_pk_mul_f32 v[70:71], v[70:71], v[86:87] op_sel_hi:[1,0]
	v_exp_f32_e32 v74, v74
	v_exp_f32_e32 v75, v75
	v_exp_f32_e32 v70, v70
	v_exp_f32_e32 v71, v71
	v_pk_mul_f32 v[76:77], v[76:77], v[86:87] op_sel_hi:[1,0]
	v_pk_mul_f32 v[72:73], v[72:73], v[86:87] op_sel_hi:[1,0]
	v_exp_f32_e32 v76, v76
	v_exp_f32_e32 v77, v77
	v_exp_f32_e32 v72, v72
	v_exp_f32_e32 v73, v73
	v_pk_fma_f32 v[74:75], v[84:85], v[74:75], v[84:85] op_sel_hi:[0,1,0]
	v_pk_fma_f32 v[70:71], v[84:85], v[70:71], v[84:85] op_sel_hi:[0,1,0]
	v_rcp_f32_e32 v74, v74
	v_rcp_f32_e32 v75, v75
	v_rcp_f32_e32 v70, v70
	v_rcp_f32_e32 v71, v71
	v_pk_fma_f32 v[76:77], v[84:85], v[76:77], v[84:85] op_sel_hi:[0,1,0]
	v_pk_fma_f32 v[72:73], v[84:85], v[72:73], v[84:85] op_sel_hi:[0,1,0]
	v_rcp_f32_e32 v76, v76
	v_rcp_f32_e32 v77, v77
	v_rcp_f32_e32 v72, v72
	v_rcp_f32_e32 v73, v73
	v_pk_mul_f32 v[74:75], v[78:79], v[74:75]
	v_pk_mul_f32 v[66:67], v[66:67], v[70:71]
	v_med3_f32 v70, v74, s49, v164
	v_med3_f32 v71, v75, s49, v164
	v_med3_f32 v66, v66, s49, v164
	v_med3_f32 v67, v67, s49, v164
	v_cvt_pk_fp8_f32 v82, v70, v71
	v_cvt_pk_fp8_f32 v83, v66, v67
	v_pk_mul_f32 v[76:77], v[80:81], v[76:77]
	v_pk_mul_f32 v[68:69], v[68:69], v[72:73]
	v_med3_f32 v72, v76, s49, v164
	v_med3_f32 v73, v77, s49, v164
	v_med3_f32 v66, v68, s49, v164
	v_med3_f32 v67, v69, s49, v164
	v_cvt_pk_fp8_f32 v82, v72, v73 op_sel:[0,0,1]
	v_cvt_pk_fp8_f32 v83, v66, v67 op_sel:[0,0,1]
	v_mad_i64_i32 v[66:67], s[26:27], v98, s48, v[150:151]
	v_lshl_add_u64 v[66:67], v[66:67], 0, v[148:149]
	global_store_dwordx2 v[66:67], v[82:83], off nt
	s_nop 0
	v_add_u32_e32 v71, 0x80, v152
	s_waitcnt vmcnt(7)
	v_mov_b32_e32 v66, v184
	v_mov_b32_e32 v67, v185
	v_ffbh_u32_e32 v68, v67
	v_min_u32_e32 v68, 32, v68
	v_lshlrev_b64 v[66:67], v68, v[66:67]
	v_min_u32_e32 v66, 1, v66
	v_or_b32_e32 v66, v67, v66
	v_cvt_f32_u32_e32 v67, v66
	v_sub_u32_e32 v68, 32, v68
	v_mov_b32_e32 v66, 0
	v_ldexp_f32 v67, v67, v68
	v_fmamk_f32 v68, v67, 0x30000000, v163
	v_rsq_f32_e32 v69, v68
	v_mul_f32_e32 v68, 0x3e000000, v68
	v_mov_b32_e32 v67, 0
	v_mul_f32_e32 v70, 0xbfb8aa3b, v69
	v_pk_mul_f32 v[58:59], v[58:59], v[70:71] op_sel_hi:[1,0]
	v_pk_mul_f32 v[54:55], v[54:55], v[70:71] op_sel_hi:[1,0]
	v_exp_f32_e32 v58, v58
	v_exp_f32_e32 v59, v59
	v_exp_f32_e32 v54, v54
	v_exp_f32_e32 v55, v55
	v_pk_mul_f32 v[60:61], v[60:61], v[70:71] op_sel_hi:[1,0]
	v_pk_mul_f32 v[56:57], v[56:57], v[70:71] op_sel_hi:[1,0]
	v_exp_f32_e32 v60, v60
	v_exp_f32_e32 v61, v61
	v_exp_f32_e32 v56, v56
	v_exp_f32_e32 v57, v57
	v_pk_fma_f32 v[58:59], v[68:69], v[58:59], v[68:69] op_sel_hi:[0,1,0]
	v_pk_fma_f32 v[54:55], v[68:69], v[54:55], v[68:69] op_sel_hi:[0,1,0]
	v_rcp_f32_e32 v58, v58
	v_rcp_f32_e32 v59, v59
	v_rcp_f32_e32 v54, v54
	v_rcp_f32_e32 v55, v55
	v_pk_fma_f32 v[60:61], v[68:69], v[60:61], v[68:69] op_sel_hi:[0,1,0]
	v_pk_fma_f32 v[56:57], v[68:69], v[56:57], v[68:69] op_sel_hi:[0,1,0]
	v_rcp_f32_e32 v60, v60
	v_rcp_f32_e32 v61, v61
	v_rcp_f32_e32 v56, v56
	v_rcp_f32_e32 v57, v57
	v_pk_mul_f32 v[58:59], v[62:63], v[58:59]
	v_pk_mul_f32 v[50:51], v[50:51], v[54:55]
	v_med3_f32 v54, v58, s49, v164
	v_med3_f32 v55, v59, s49, v164
	v_med3_f32 v50, v50, s49, v164
	v_med3_f32 v51, v51, s49, v164
	v_cvt_pk_fp8_f32 v66, v54, v55
	v_cvt_pk_fp8_f32 v67, v50, v51
	v_pk_mul_f32 v[60:61], v[64:65], v[60:61]
	v_pk_mul_f32 v[52:53], v[52:53], v[56:57]
	v_med3_f32 v56, v60, s49, v164
	v_med3_f32 v57, v61, s49, v164
	v_med3_f32 v50, v52, s49, v164
	v_med3_f32 v51, v53, s49, v164
	v_cvt_pk_fp8_f32 v66, v56, v57 op_sel:[0,0,1]
	v_cvt_pk_fp8_f32 v67, v50, v51 op_sel:[0,0,1]
	v_mad_i64_i32 v[50:51], s[26:27], v71, s48, v[150:151]
	v_lshl_add_u64 v[50:51], v[50:51], 0, v[148:149]
	global_store_dwordx2 v[50:51], v[66:67], off nt
	s_nop 0
	v_add_u32_e32 v55, 0x90, v152
	s_waitcnt vmcnt(7)
	v_mov_b32_e32 v50, v186
	v_mov_b32_e32 v51, v187
	v_ffbh_u32_e32 v52, v51
	v_min_u32_e32 v52, 32, v52
	v_lshlrev_b64 v[50:51], v52, v[50:51]
	v_min_u32_e32 v50, 1, v50
	v_or_b32_e32 v50, v51, v50
	v_cvt_f32_u32_e32 v51, v50
	v_sub_u32_e32 v52, 32, v52
	v_mov_b32_e32 v50, 0
	v_ldexp_f32 v51, v51, v52
	v_fmamk_f32 v52, v51, 0x30000000, v163
	v_rsq_f32_e32 v53, v52
	v_mul_f32_e32 v52, 0x3e000000, v52
	v_mov_b32_e32 v51, 0
	v_mul_f32_e32 v54, 0xbfb8aa3b, v53
	v_pk_mul_f32 v[42:43], v[42:43], v[54:55] op_sel_hi:[1,0]
	v_pk_mul_f32 v[38:39], v[38:39], v[54:55] op_sel_hi:[1,0]
	v_exp_f32_e32 v42, v42
	v_exp_f32_e32 v43, v43
	v_exp_f32_e32 v38, v38
	v_exp_f32_e32 v39, v39
	v_pk_mul_f32 v[44:45], v[44:45], v[54:55] op_sel_hi:[1,0]
	v_pk_mul_f32 v[40:41], v[40:41], v[54:55] op_sel_hi:[1,0]
	v_exp_f32_e32 v44, v44
	v_exp_f32_e32 v45, v45
	v_exp_f32_e32 v40, v40
	v_exp_f32_e32 v41, v41
	v_pk_fma_f32 v[42:43], v[52:53], v[42:43], v[52:53] op_sel_hi:[0,1,0]
	v_pk_fma_f32 v[38:39], v[52:53], v[38:39], v[52:53] op_sel_hi:[0,1,0]
	v_rcp_f32_e32 v42, v42
	v_rcp_f32_e32 v43, v43
	v_rcp_f32_e32 v38, v38
	v_rcp_f32_e32 v39, v39
	v_pk_fma_f32 v[44:45], v[52:53], v[44:45], v[52:53] op_sel_hi:[0,1,0]
	v_pk_fma_f32 v[40:41], v[52:53], v[40:41], v[52:53] op_sel_hi:[0,1,0]
	v_rcp_f32_e32 v44, v44
	v_rcp_f32_e32 v45, v45
	v_rcp_f32_e32 v40, v40
	v_rcp_f32_e32 v41, v41
	v_pk_mul_f32 v[42:43], v[46:47], v[42:43]
	v_pk_mul_f32 v[34:35], v[34:35], v[38:39]
	v_med3_f32 v38, v42, s49, v164
	v_med3_f32 v39, v43, s49, v164
	v_med3_f32 v34, v34, s49, v164
	v_med3_f32 v35, v35, s49, v164
	v_cvt_pk_fp8_f32 v50, v38, v39
	v_cvt_pk_fp8_f32 v51, v34, v35
	v_pk_mul_f32 v[44:45], v[48:49], v[44:45]
	v_pk_mul_f32 v[36:37], v[36:37], v[40:41]
	v_med3_f32 v40, v44, s49, v164
	v_med3_f32 v41, v45, s49, v164
	v_med3_f32 v34, v36, s49, v164
	v_med3_f32 v35, v37, s49, v164
	v_cvt_pk_fp8_f32 v50, v40, v41 op_sel:[0,0,1]
	v_cvt_pk_fp8_f32 v51, v34, v35 op_sel:[0,0,1]
	v_mad_i64_i32 v[34:35], s[26:27], v55, s48, v[150:151]
	v_lshl_add_u64 v[34:35], v[34:35], 0, v[148:149]
	global_store_dwordx2 v[34:35], v[50:51], off nt
	s_nop 0
	v_add_u32_e32 v39, 0xa0, v152
	s_waitcnt vmcnt(7)
	v_mov_b32_e32 v34, v188
	v_mov_b32_e32 v35, v189
	v_ffbh_u32_e32 v36, v35
	v_min_u32_e32 v36, 32, v36
	v_lshlrev_b64 v[34:35], v36, v[34:35]
	v_min_u32_e32 v34, 1, v34
	v_or_b32_e32 v34, v35, v34
	v_cvt_f32_u32_e32 v35, v34
	v_sub_u32_e32 v36, 32, v36
	v_mov_b32_e32 v34, 0
	v_ldexp_f32 v35, v35, v36
	v_fmamk_f32 v36, v35, 0x30000000, v163
	v_rsq_f32_e32 v37, v36
	v_mul_f32_e32 v36, 0x3e000000, v36
	v_mov_b32_e32 v35, 0
	v_mul_f32_e32 v38, 0xbfb8aa3b, v37
	v_pk_mul_f32 v[26:27], v[26:27], v[38:39] op_sel_hi:[1,0]
	v_pk_mul_f32 v[22:23], v[22:23], v[38:39] op_sel_hi:[1,0]
	v_exp_f32_e32 v26, v26
	v_exp_f32_e32 v27, v27
	v_exp_f32_e32 v22, v22
	v_exp_f32_e32 v23, v23
	v_pk_mul_f32 v[28:29], v[28:29], v[38:39] op_sel_hi:[1,0]
	v_pk_mul_f32 v[24:25], v[24:25], v[38:39] op_sel_hi:[1,0]
	v_exp_f32_e32 v28, v28
	v_exp_f32_e32 v29, v29
	v_exp_f32_e32 v24, v24
	v_exp_f32_e32 v25, v25
	v_pk_fma_f32 v[26:27], v[36:37], v[26:27], v[36:37] op_sel_hi:[0,1,0]
	v_pk_fma_f32 v[22:23], v[36:37], v[22:23], v[36:37] op_sel_hi:[0,1,0]
	v_rcp_f32_e32 v26, v26
	v_rcp_f32_e32 v27, v27
	v_rcp_f32_e32 v22, v22
	v_rcp_f32_e32 v23, v23
	v_pk_fma_f32 v[28:29], v[36:37], v[28:29], v[36:37] op_sel_hi:[0,1,0]
	v_pk_fma_f32 v[24:25], v[36:37], v[24:25], v[36:37] op_sel_hi:[0,1,0]
	v_rcp_f32_e32 v28, v28
	v_rcp_f32_e32 v29, v29
	v_rcp_f32_e32 v24, v24
	v_rcp_f32_e32 v25, v25
	v_pk_mul_f32 v[26:27], v[30:31], v[26:27]
	v_pk_mul_f32 v[18:19], v[18:19], v[22:23]
	v_med3_f32 v22, v26, s49, v164
	v_med3_f32 v23, v27, s49, v164
	v_med3_f32 v18, v18, s49, v164
	v_med3_f32 v19, v19, s49, v164
	v_cvt_pk_fp8_f32 v34, v22, v23
	v_cvt_pk_fp8_f32 v35, v18, v19
	v_pk_mul_f32 v[28:29], v[32:33], v[28:29]
	v_pk_mul_f32 v[20:21], v[20:21], v[24:25]
	v_med3_f32 v24, v28, s49, v164
	v_med3_f32 v25, v29, s49, v164
	v_med3_f32 v18, v20, s49, v164
	v_med3_f32 v19, v21, s49, v164
	v_cvt_pk_fp8_f32 v34, v24, v25 op_sel:[0,0,1]
	v_cvt_pk_fp8_f32 v35, v18, v19 op_sel:[0,0,1]
	v_mad_i64_i32 v[18:19], s[26:27], v39, s48, v[150:151]
	v_lshl_add_u64 v[18:19], v[18:19], 0, v[148:149]
	global_store_dwordx2 v[18:19], v[34:35], off nt
	s_nop 0
	v_add_u32_e32 v23, 0xb0, v152
	v_mov_b32_e32 v20, 0
	s_waitcnt vmcnt(7)
	v_mov_b32_e32 v18, v190
	v_mov_b32_e32 v19, v191
	v_ffbh_u32_e32 v21, v19
	v_min_u32_e32 v22, 32, v21
	v_lshlrev_b64 v[18:19], v22, v[18:19]
	v_min_u32_e32 v18, 1, v18
	v_or_b32_e32 v18, v19, v18
	v_cvt_f32_u32_e32 v18, v18
	v_sub_u32_e32 v19, 32, v22
	v_mov_b32_e32 v21, 0
	v_ldexp_f32 v18, v18, v19
	v_fmamk_f32 v18, v18, 0x30000000, v163
	v_rsq_f32_e32 v19, v18
	v_mul_f32_e32 v18, 0x3e000000, v18
	v_mul_f32_e32 v22, 0xbfb8aa3b, v19
	v_pk_mul_f32 v[6:7], v[6:7], v[22:23] op_sel_hi:[1,0]
	v_pk_mul_f32 v[2:3], v[2:3], v[22:23] op_sel_hi:[1,0]
	v_exp_f32_e32 v6, v6
	v_exp_f32_e32 v7, v7
	v_exp_f32_e32 v2, v2
	v_exp_f32_e32 v3, v3
	v_pk_mul_f32 v[8:9], v[8:9], v[22:23] op_sel_hi:[1,0]
	v_pk_mul_f32 v[4:5], v[4:5], v[22:23] op_sel_hi:[1,0]
	v_exp_f32_e32 v8, v8
	v_exp_f32_e32 v9, v9
	v_exp_f32_e32 v4, v4
	v_exp_f32_e32 v5, v5
	v_pk_fma_f32 v[6:7], v[18:19], v[6:7], v[18:19] op_sel_hi:[0,1,0]
	v_pk_fma_f32 v[2:3], v[18:19], v[2:3], v[18:19] op_sel_hi:[0,1,0]
	v_rcp_f32_e32 v6, v6
	v_rcp_f32_e32 v7, v7
	v_rcp_f32_e32 v2, v2
	v_rcp_f32_e32 v3, v3
	v_pk_fma_f32 v[8:9], v[18:19], v[8:9], v[18:19] op_sel_hi:[0,1,0]
	v_pk_fma_f32 v[4:5], v[18:19], v[4:5], v[18:19] op_sel_hi:[0,1,0]
	v_rcp_f32_e32 v8, v8
	v_rcp_f32_e32 v9, v9
	v_rcp_f32_e32 v4, v4
	v_rcp_f32_e32 v5, v5
	v_pk_mul_f32 v[6:7], v[14:15], v[6:7]
	v_pk_mul_f32 v[2:3], v[10:11], v[2:3]
	v_med3_f32 v6, v6, s49, v164
	v_med3_f32 v7, v7, s49, v164
	v_med3_f32 v2, v2, s49, v164
	v_med3_f32 v3, v3, s49, v164
	v_cvt_pk_fp8_f32 v20, v6, v7
	v_cvt_pk_fp8_f32 v21, v2, v3
	v_pk_mul_f32 v[8:9], v[16:17], v[8:9]
	v_pk_mul_f32 v[4:5], v[12:13], v[4:5]
	v_med3_f32 v8, v8, s49, v164
	v_med3_f32 v9, v9, s49, v164
	v_med3_f32 v2, v4, s49, v164
	v_med3_f32 v3, v5, s49, v164
	v_cvt_pk_fp8_f32 v20, v8, v9 op_sel:[0,0,1]
	v_cvt_pk_fp8_f32 v21, v2, v3 op_sel:[0,0,1]
	v_mad_i64_i32 v[2:3], s[26:27], v23, s48, v[150:151]
	v_lshl_add_u64 v[2:3], v[2:3], 0, v[148:149]
	global_store_dwordx2 v[2:3], v[20:21], off nt
	s_cbranch_vccnz .LBB0_467
	s_andn2_b64 vcc, exec, s[6:7]
	s_cbranch_vccnz .LBB0_466
	s_barrier
	s_branch .LBB0_466

.LBB0_559:
	v_lshl_add_u32 v150, s45, 8, v152
	v_ashrrev_i32_e32 v151, 31, v150
	v_lshl_or_b32 v148, s48, 8, v154
	v_lshlrev_b64 v[162:163], 12, v[150:151]
	v_ashrrev_i32_e32 v149, 31, v148
	v_lshl_add_u64 v[162:163], s[50:51], 0, v[162:163]
	v_lshl_add_u64 v[166:167], v[148:149], 1, v[162:163]
	v_mov_b32_e32 v184, v166
	v_mov_b32_e32 v185, v167
	v_mov_b32_e32 v222, 0x10000
	v_mov_b32_e32 v223, 0
	global_load_dwordx4 v[176:179], v[184:185], off
	global_load_dwordx4 v[180:183], v[184:185], off offset:256
	v_lshl_add_u64 v[184:185], v[222:223], 0, v[184:185]
	global_load_dwordx4 v[190:193], v[184:185], off
	global_load_dwordx4 v[194:197], v[184:185], off offset:256
	v_lshl_add_u64 v[184:185], v[222:223], 0, v[184:185]
	global_load_dwordx4 v[198:201], v[184:185], off
	global_load_dwordx4 v[202:205], v[184:185], off offset:256
	v_lshl_add_u64 v[184:185], v[222:223], 0, v[184:185]
	global_load_dwordx4 v[206:209], v[184:185], off
	global_load_dwordx4 v[210:213], v[184:185], off offset:256
	v_lshl_add_u64 v[184:185], v[222:223], 2, v[184:185]
	v_lshl_add_u64 v[184:185], v[222:223], 0, v[184:185]
	global_load_dwordx4 v[214:217], v[184:185], off
	global_load_dwordx4 v[218:221], v[184:185], off offset:256
	s_nop 0
	v_xor_b32_e32 v174, 32, v161
	s_waitcnt vmcnt(8)
	s_nop 1
	v_pk_mov_b32 v[162:163], v[176:177], v[176:177] op_sel:[0,1]
	v_pk_mov_b32 v[164:165], v[178:179], v[178:179] op_sel:[0,1]
	v_lshlrev_b32_e32 v168, 16, v162
	v_and_b32_e32 v169, 0xffff0000, v162
	v_lshlrev_b32_e32 v162, 16, v163
	v_and_b32_e32 v163, 0xffff0000, v163
	v_lshlrev_b32_e32 v170, 16, v164
	v_and_b32_e32 v171, 0xffff0000, v164
	v_lshlrev_b32_e32 v164, 16, v165
	v_and_b32_e32 v165, 0xffff0000, v165
	v_pk_add_f32 v[128:129], v[128:129], v[162:163]
	v_pk_add_f32 v[168:169], v[126:127], v[168:169]
	v_pk_add_f32 v[172:173], v[124:125], v[164:165]
	v_pk_add_f32 v[170:171], v[122:123], v[170:171]
	v_cvt_pk_bf16_f32 v124, v168, v169
	v_cvt_pk_bf16_f32 v125, v128, v129
	v_mul_f32_e32 v169, v169, v169
	v_cvt_pk_bf16_f32 v126, v170, v171
	v_cvt_pk_bf16_f32 v127, v172, v173
	s_nop 0
	v_mul_f32_e32 v129, v129, v129
	v_mul_f32_e32 v171, v171, v171
	v_mul_f32_e32 v173, v173, v173
	v_fmac_f32_e32 v169, v168, v168
	v_fmac_f32_e32 v129, v128, v128
	v_fmac_f32_e32 v171, v170, v170
	v_fmac_f32_e32 v173, v172, v172
	v_add_f32_e32 v128, v169, v129
	v_add_f32_e32 v129, v171, v173
	v_add_f32_e32 v170, v128, v129
	v_and_b32_e32 v123, 64, v161
	v_xor_b32_e32 v122, 16, v161
	v_add_u32_e32 v123, 64, v123
	v_cmp_lt_i32_e32 vcc, v122, v123
	global_store_dwordx4 v[166:167], v[124:127], off nt
	s_nop 1
	v_pk_mov_b32 v[162:163], v[180:181], v[180:181] op_sel:[0,1]
	v_pk_mov_b32 v[164:165], v[182:183], v[182:183] op_sel:[0,1]
	v_lshl_add_u64 v[184:185], v[222:223], 0, v[184:185]
	global_load_dwordx4 v[176:179], v[184:185], off
	global_load_dwordx4 v[180:183], v[184:185], off offset:256
	v_lshlrev_b32_e32 v128, 16, v162
	v_and_b32_e32 v129, 0xffff0000, v162
	v_lshlrev_b32_e32 v162, 16, v163
	v_and_b32_e32 v163, 0xffff0000, v163
	v_lshlrev_b32_e32 v168, 16, v164
	v_and_b32_e32 v169, 0xffff0000, v164
	v_lshlrev_b32_e32 v164, 16, v165
	v_and_b32_e32 v165, 0xffff0000, v165
	v_pk_add_f32 v[120:121], v[120:121], v[162:163]
	v_pk_add_f32 v[118:119], v[118:119], v[128:129]
	v_pk_add_f32 v[128:129], v[116:117], v[164:165]
	v_pk_add_f32 v[162:163], v[114:115], v[168:169]
	v_mul_f32_e32 v114, v119, v119
	v_mul_f32_e32 v115, v121, v121
	v_mul_f32_e32 v116, v163, v163
	v_mul_f32_e32 v117, v129, v129
	v_fmac_f32_e32 v114, v118, v118
	v_fmac_f32_e32 v115, v120, v120
	v_fmac_f32_e32 v116, v162, v162
	v_fmac_f32_e32 v117, v128, v128
	v_add_f32_e32 v114, v114, v115
	v_add_f32_e32 v115, v116, v117
	v_cndmask_b32_e32 v122, v161, v122, vcc
	v_add_f32_e32 v114, v114, v115
	v_lshlrev_b32_e32 v122, 2, v122
	v_add_f32_e32 v114, v170, v114
	ds_bpermute_b32 v115, v122, v114
	v_cmp_lt_i32_e32 vcc, v174, v123
	v_cvt_pk_bf16_f32 v118, v118, v119
	v_cvt_pk_bf16_f32 v119, v120, v121
	v_cvt_pk_bf16_f32 v120, v162, v163
	s_waitcnt lgkmcnt(0)
	v_add_f32_e32 v114, v114, v115
	v_cvt_pk_bf16_f32 v121, v128, v129
	v_cndmask_b32_e32 v116, v161, v174, vcc
	v_lshlrev_b32_e32 v116, 2, v116
	ds_bpermute_b32 v115, v116, v114
	global_store_dwordx4 v[166:167], v[118:121], off offset:256 nt
	s_and_saveexec_b64 s[20:21], s[4:5]
	s_cbranch_execz .LBB0_561
	s_waitcnt lgkmcnt(0)
	v_add_f32_e32 v114, v114, v115
	v_fma_f32 v114, v114, s42, 0.5
	v_trunc_f32_e32 v114, v114
	v_mul_f32_e32 v115, 0x2f800000, v114
	v_floor_f32_e32 v115, v115
	v_fmac_f32_e32 v114, 0xcf800000, v115
	v_cvt_u32_f32_e32 v114, v114
	v_cvt_u32_f32_e32 v115, v115
	v_lshl_add_u64 v[118:119], v[150:151], 3, s[12:13]
	global_atomic_add_x2 v[118:119], v[114:115], off
.LBB0_561:
	s_or_b64 exec, exec, s[20:21]
	v_or_b32_e32 v114, 16, v150
	s_waitcnt lgkmcnt(0)
	v_ashrrev_i32_e32 v115, 31, v114
	v_lshlrev_b64 v[118:119], 12, v[114:115]
	v_lshl_add_u64 v[118:119], s[50:51], 0, v[118:119]
	v_lshl_add_u64 v[124:125], v[148:149], 1, v[118:119]
	s_nop 0
	s_waitcnt vmcnt(10)
	s_nop 1
	v_pk_mov_b32 v[118:119], v[190:191], v[190:191] op_sel:[0,1]
	v_pk_mov_b32 v[120:121], v[192:193], v[192:193] op_sel:[0,1]
	v_lshlrev_b32_e32 v126, 16, v118
	v_and_b32_e32 v127, 0xffff0000, v118
	v_lshlrev_b32_e32 v118, 16, v119
	v_and_b32_e32 v119, 0xffff0000, v119
	v_lshlrev_b32_e32 v128, 16, v120
	v_and_b32_e32 v129, 0xffff0000, v120
	v_lshlrev_b32_e32 v120, 16, v121
	v_and_b32_e32 v121, 0xffff0000, v121
	v_pk_add_f32 v[118:119], v[112:113], v[118:119]
	v_pk_add_f32 v[126:127], v[110:111], v[126:127]
	v_pk_add_f32 v[120:121], v[108:109], v[120:121]
	v_pk_add_f32 v[128:129], v[106:107], v[128:129]
	v_cvt_pk_bf16_f32 v106, v126, v127
	v_cvt_pk_bf16_f32 v107, v118, v119
	v_mul_f32_e32 v117, v127, v127
	v_cvt_pk_bf16_f32 v108, v128, v129
	v_cvt_pk_bf16_f32 v109, v120, v121
	s_nop 0
	v_mul_f32_e32 v119, v119, v119
	v_mul_f32_e32 v123, v129, v129
	v_mul_f32_e32 v121, v121, v121
	v_fmac_f32_e32 v117, v126, v126
	v_fmac_f32_e32 v119, v118, v118
	v_fmac_f32_e32 v123, v128, v128
	v_fmac_f32_e32 v121, v120, v120
	v_add_f32_e32 v117, v117, v119
	v_add_f32_e32 v118, v123, v121
	v_add_f32_e32 v117, v117, v118
	global_store_dwordx4 v[124:125], v[106:109], off nt
	s_nop 1
	v_pk_mov_b32 v[110:111], v[194:195], v[194:195] op_sel:[0,1]
	v_pk_mov_b32 v[112:113], v[196:197], v[196:197] op_sel:[0,1]
	v_lshl_add_u64 v[184:185], v[222:223], 0, v[184:185]
	global_load_dwordx4 v[190:193], v[184:185], off
	global_load_dwordx4 v[194:197], v[184:185], off offset:256
	v_lshlrev_b32_e32 v118, 16, v110
	v_and_b32_e32 v119, 0xffff0000, v110
	v_lshlrev_b32_e32 v110, 16, v111
	v_and_b32_e32 v111, 0xffff0000, v111
	v_lshlrev_b32_e32 v120, 16, v112
	v_and_b32_e32 v121, 0xffff0000, v112
	v_lshlrev_b32_e32 v112, 16, v113
	v_and_b32_e32 v113, 0xffff0000, v113
	v_pk_add_f32 v[104:105], v[104:105], v[110:111]
	v_pk_add_f32 v[102:103], v[102:103], v[118:119]
	v_pk_add_f32 v[110:111], v[100:101], v[112:113]
	v_pk_add_f32 v[112:113], v[98:99], v[120:121]
	v_mul_f32_e32 v98, v103, v103
	v_mul_f32_e32 v99, v105, v105
	v_mul_f32_e32 v100, v113, v113
	v_mul_f32_e32 v101, v111, v111
	v_fmac_f32_e32 v98, v102, v102
	v_fmac_f32_e32 v99, v104, v104
	v_fmac_f32_e32 v100, v112, v112
	v_fmac_f32_e32 v101, v110, v110
	v_add_f32_e32 v98, v98, v99
	v_add_f32_e32 v99, v100, v101
	v_add_f32_e32 v98, v98, v99
	v_add_f32_e32 v98, v117, v98
	ds_bpermute_b32 v99, v122, v98
	v_cvt_pk_bf16_f32 v100, v102, v103
	v_cvt_pk_bf16_f32 v101, v104, v105
	v_cvt_pk_bf16_f32 v102, v112, v113
	v_cvt_pk_bf16_f32 v103, v110, v111
	s_waitcnt lgkmcnt(0)
	v_add_f32_e32 v98, v98, v99
	ds_bpermute_b32 v99, v116, v98
	global_store_dwordx4 v[124:125], v[100:103], off offset:256 nt
	s_and_saveexec_b64 s[20:21], s[4:5]
	s_cbranch_execz .LBB0_563
	s_waitcnt lgkmcnt(0)
	v_add_f32_e32 v98, v98, v99
	v_fma_f32 v98, v98, s42, 0.5
	v_trunc_f32_e32 v98, v98
	v_mul_f32_e32 v99, 0x2f800000, v98
	v_floor_f32_e32 v99, v99
	v_fmac_f32_e32 v98, 0xcf800000, v99
	v_cvt_u32_f32_e32 v98, v98
	v_cvt_u32_f32_e32 v99, v99
	v_lshl_add_u64 v[100:101], v[114:115], 3, s[12:13]
	global_atomic_add_x2 v[100:101], v[98:99], off
.LBB0_563:
	s_or_b64 exec, exec, s[20:21]
	v_or_b32_e32 v98, 32, v150
	s_waitcnt lgkmcnt(0)
	v_ashrrev_i32_e32 v99, 31, v98
	v_lshlrev_b64 v[100:101], 12, v[98:99]
	v_lshl_add_u64 v[100:101], s[50:51], 0, v[100:101]
	v_lshl_add_u64 v[104:105], v[148:149], 1, v[100:101]
	s_nop 0
	s_waitcnt vmcnt(12)
	s_nop 1
	v_pk_mov_b32 v[100:101], v[198:199], v[198:199] op_sel:[0,1]
	v_pk_mov_b32 v[102:103], v[200:201], v[200:201] op_sel:[0,1]
	v_lshlrev_b32_e32 v106, 16, v100
	v_and_b32_e32 v107, 0xffff0000, v100
	v_lshlrev_b32_e32 v100, 16, v101
	v_and_b32_e32 v101, 0xffff0000, v101
	v_lshlrev_b32_e32 v108, 16, v102
	v_and_b32_e32 v109, 0xffff0000, v102
	v_lshlrev_b32_e32 v102, 16, v103
	v_and_b32_e32 v103, 0xffff0000, v103
	v_pk_add_f32 v[100:101], v[96:97], v[100:101]
	v_pk_add_f32 v[106:107], v[94:95], v[106:107]
	v_pk_add_f32 v[102:103], v[92:93], v[102:103]
	v_pk_add_f32 v[108:109], v[90:91], v[108:109]
	v_cvt_pk_bf16_f32 v90, v106, v107
	v_cvt_pk_bf16_f32 v91, v100, v101
	v_mul_f32_e32 v107, v107, v107
	v_cvt_pk_bf16_f32 v92, v108, v109
	v_cvt_pk_bf16_f32 v93, v102, v103
	s_nop 0
	v_mul_f32_e32 v101, v101, v101
	v_mul_f32_e32 v109, v109, v109
	v_mul_f32_e32 v103, v103, v103
	v_fmac_f32_e32 v107, v106, v106
	v_fmac_f32_e32 v101, v100, v100
	v_fmac_f32_e32 v109, v108, v108
	v_fmac_f32_e32 v103, v102, v102
	v_add_f32_e32 v100, v107, v101
	v_add_f32_e32 v101, v109, v103
	v_add_f32_e32 v106, v100, v101
	global_store_dwordx4 v[104:105], v[90:93], off nt
	s_nop 1
	v_pk_mov_b32 v[94:95], v[202:203], v[202:203] op_sel:[0,1]
	v_pk_mov_b32 v[96:97], v[204:205], v[204:205] op_sel:[0,1]
	v_lshl_add_u64 v[184:185], v[222:223], 0, v[184:185]
	global_load_dwordx4 v[198:201], v[184:185], off
	global_load_dwordx4 v[202:205], v[184:185], off offset:256
	v_lshlrev_b32_e32 v100, 16, v94
	v_and_b32_e32 v101, 0xffff0000, v94
	v_lshlrev_b32_e32 v94, 16, v95
	v_and_b32_e32 v95, 0xffff0000, v95
	v_lshlrev_b32_e32 v102, 16, v96
	v_and_b32_e32 v103, 0xffff0000, v96
	v_lshlrev_b32_e32 v96, 16, v97
	v_and_b32_e32 v97, 0xffff0000, v97
	v_pk_add_f32 v[88:89], v[88:89], v[94:95]
	v_pk_add_f32 v[86:87], v[86:87], v[100:101]
	v_pk_add_f32 v[94:95], v[84:85], v[96:97]
	v_pk_add_f32 v[96:97], v[82:83], v[102:103]
	v_mul_f32_e32 v82, v87, v87
	v_mul_f32_e32 v83, v89, v89
	v_mul_f32_e32 v84, v97, v97
	v_mul_f32_e32 v85, v95, v95
	v_fmac_f32_e32 v82, v86, v86
	v_fmac_f32_e32 v83, v88, v88
	v_fmac_f32_e32 v84, v96, v96
	v_fmac_f32_e32 v85, v94, v94
	v_add_f32_e32 v82, v82, v83
	v_add_f32_e32 v83, v84, v85
	v_add_f32_e32 v82, v82, v83
	v_add_f32_e32 v82, v106, v82
	ds_bpermute_b32 v83, v122, v82
	v_cvt_pk_bf16_f32 v84, v86, v87
	v_cvt_pk_bf16_f32 v85, v88, v89
	v_cvt_pk_bf16_f32 v86, v96, v97
	v_cvt_pk_bf16_f32 v87, v94, v95
	s_waitcnt lgkmcnt(0)
	v_add_f32_e32 v82, v82, v83
	ds_bpermute_b32 v83, v116, v82
	global_store_dwordx4 v[104:105], v[84:87], off offset:256 nt
	s_and_saveexec_b64 s[20:21], s[4:5]
	s_cbranch_execz .LBB0_565
	s_waitcnt lgkmcnt(0)
	v_add_f32_e32 v82, v82, v83
	v_fma_f32 v82, v82, s42, 0.5
	v_trunc_f32_e32 v82, v82
	v_mul_f32_e32 v83, 0x2f800000, v82
	v_floor_f32_e32 v83, v83
	v_fmac_f32_e32 v82, 0xcf800000, v83
	v_cvt_u32_f32_e32 v82, v82
	v_cvt_u32_f32_e32 v83, v83
	v_lshl_add_u64 v[84:85], v[98:99], 3, s[12:13]
	global_atomic_add_x2 v[84:85], v[82:83], off
.LBB0_565:
	s_or_b64 exec, exec, s[20:21]
	v_or_b32_e32 v82, 48, v150
	s_waitcnt lgkmcnt(0)
	v_ashrrev_i32_e32 v83, 31, v82
	v_lshlrev_b64 v[84:85], 12, v[82:83]
	v_lshl_add_u64 v[84:85], s[50:51], 0, v[84:85]
	v_lshl_add_u64 v[88:89], v[148:149], 1, v[84:85]
	s_nop 0
	s_waitcnt vmcnt(14)
	s_nop 1
	v_pk_mov_b32 v[84:85], v[206:207], v[206:207] op_sel:[0,1]
	v_pk_mov_b32 v[86:87], v[208:209], v[208:209] op_sel:[0,1]
	v_lshlrev_b32_e32 v90, 16, v84
	v_and_b32_e32 v91, 0xffff0000, v84
	v_lshlrev_b32_e32 v84, 16, v85
	v_and_b32_e32 v85, 0xffff0000, v85
	v_lshlrev_b32_e32 v92, 16, v86
	v_and_b32_e32 v93, 0xffff0000, v86
	v_lshlrev_b32_e32 v86, 16, v87
	v_and_b32_e32 v87, 0xffff0000, v87
	v_pk_add_f32 v[84:85], v[80:81], v[84:85]
	v_pk_add_f32 v[90:91], v[78:79], v[90:91]
	v_pk_add_f32 v[86:87], v[76:77], v[86:87]
	v_pk_add_f32 v[92:93], v[74:75], v[92:93]
	v_cvt_pk_bf16_f32 v74, v90, v91
	v_cvt_pk_bf16_f32 v75, v84, v85
	v_mul_f32_e32 v91, v91, v91
	v_cvt_pk_bf16_f32 v76, v92, v93
	v_cvt_pk_bf16_f32 v77, v86, v87
	s_nop 0
	v_mul_f32_e32 v85, v85, v85
	v_mul_f32_e32 v93, v93, v93
	v_mul_f32_e32 v87, v87, v87
	v_fmac_f32_e32 v91, v90, v90
	v_fmac_f32_e32 v85, v84, v84
	v_fmac_f32_e32 v93, v92, v92
	v_fmac_f32_e32 v87, v86, v86
	v_add_f32_e32 v84, v91, v85
	v_add_f32_e32 v85, v93, v87
	v_add_f32_e32 v90, v84, v85
	global_store_dwordx4 v[88:89], v[74:77], off nt
	s_nop 1
	v_pk_mov_b32 v[78:79], v[210:211], v[210:211] op_sel:[0,1]
	v_pk_mov_b32 v[80:81], v[212:213], v[212:213] op_sel:[0,1]
	v_lshlrev_b32_e32 v84, 16, v78
	v_and_b32_e32 v85, 0xffff0000, v78
	v_lshlrev_b32_e32 v78, 16, v79
	v_and_b32_e32 v79, 0xffff0000, v79
	v_lshlrev_b32_e32 v86, 16, v80
	v_and_b32_e32 v87, 0xffff0000, v80
	v_lshlrev_b32_e32 v80, 16, v81
	v_and_b32_e32 v81, 0xffff0000, v81
	v_pk_add_f32 v[72:73], v[72:73], v[78:79]
	v_pk_add_f32 v[70:71], v[70:71], v[84:85]
	v_pk_add_f32 v[78:79], v[68:69], v[80:81]
	v_pk_add_f32 v[80:81], v[66:67], v[86:87]
	v_mul_f32_e32 v66, v71, v71
	v_mul_f32_e32 v67, v73, v73
	v_mul_f32_e32 v68, v81, v81
	v_mul_f32_e32 v69, v79, v79
	v_fmac_f32_e32 v66, v70, v70
	v_fmac_f32_e32 v67, v72, v72
	v_fmac_f32_e32 v68, v80, v80
	v_fmac_f32_e32 v69, v78, v78
	v_add_f32_e32 v66, v66, v67
	v_add_f32_e32 v67, v68, v69
	v_add_f32_e32 v66, v66, v67
	v_add_f32_e32 v66, v90, v66
	ds_bpermute_b32 v67, v122, v66
	v_cvt_pk_bf16_f32 v68, v70, v71
	v_cvt_pk_bf16_f32 v69, v72, v73
	v_cvt_pk_bf16_f32 v70, v80, v81
	v_cvt_pk_bf16_f32 v71, v78, v79
	s_waitcnt lgkmcnt(0)
	v_add_f32_e32 v66, v66, v67
	ds_bpermute_b32 v67, v116, v66
	global_store_dwordx4 v[88:89], v[68:71], off offset:256 nt
	s_and_saveexec_b64 s[20:21], s[4:5]
	s_cbranch_execz .LBB0_567
	s_waitcnt lgkmcnt(0)
	v_add_f32_e32 v66, v66, v67
	v_fma_f32 v66, v66, s42, 0.5
	v_trunc_f32_e32 v66, v66
	v_mul_f32_e32 v67, 0x2f800000, v66
	v_floor_f32_e32 v67, v67
	v_fmac_f32_e32 v66, 0xcf800000, v67
	v_cvt_u32_f32_e32 v66, v66
	v_cvt_u32_f32_e32 v67, v67
	v_lshl_add_u64 v[68:69], v[82:83], 3, s[12:13]
	global_atomic_add_x2 v[68:69], v[66:67], off
.LBB0_567:
	s_or_b64 exec, exec, s[20:21]
	v_add_u32_e32 v66, 0x80, v150
	s_waitcnt lgkmcnt(0)
	v_ashrrev_i32_e32 v67, 31, v66
	v_lshlrev_b64 v[68:69], 12, v[66:67]
	v_lshl_add_u64 v[68:69], s[50:51], 0, v[68:69]
	v_lshl_add_u64 v[72:73], v[148:149], 1, v[68:69]
	s_nop 0
	s_waitcnt vmcnt(14)
	s_nop 1
	v_pk_mov_b32 v[68:69], v[214:215], v[214:215] op_sel:[0,1]
	v_pk_mov_b32 v[70:71], v[216:217], v[216:217] op_sel:[0,1]
	v_lshlrev_b32_e32 v74, 16, v68
	v_and_b32_e32 v75, 0xffff0000, v68
	v_lshlrev_b32_e32 v68, 16, v69
	v_and_b32_e32 v69, 0xffff0000, v69
	v_lshlrev_b32_e32 v76, 16, v70
	v_and_b32_e32 v77, 0xffff0000, v70
	v_lshlrev_b32_e32 v70, 16, v71
	v_and_b32_e32 v71, 0xffff0000, v71
	v_pk_add_f32 v[68:69], v[64:65], v[68:69]
	v_pk_add_f32 v[74:75], v[62:63], v[74:75]
	v_pk_add_f32 v[70:71], v[60:61], v[70:71]
	v_pk_add_f32 v[76:77], v[58:59], v[76:77]
	v_cvt_pk_bf16_f32 v58, v74, v75
	v_cvt_pk_bf16_f32 v59, v68, v69
	v_mul_f32_e32 v75, v75, v75
	v_cvt_pk_bf16_f32 v60, v76, v77
	v_cvt_pk_bf16_f32 v61, v70, v71
	s_nop 0
	v_mul_f32_e32 v69, v69, v69
	v_mul_f32_e32 v77, v77, v77
	v_mul_f32_e32 v71, v71, v71
	v_fmac_f32_e32 v75, v74, v74
	v_fmac_f32_e32 v69, v68, v68
	v_fmac_f32_e32 v77, v76, v76
	v_fmac_f32_e32 v71, v70, v70
	v_add_f32_e32 v68, v75, v69
	v_add_f32_e32 v69, v77, v71
	v_add_f32_e32 v74, v68, v69
	global_store_dwordx4 v[72:73], v[58:61], off nt
	s_nop 1
	v_pk_mov_b32 v[62:63], v[218:219], v[218:219] op_sel:[0,1]
	v_pk_mov_b32 v[64:65], v[220:221], v[220:221] op_sel:[0,1]
	v_lshlrev_b32_e32 v68, 16, v62
	v_and_b32_e32 v69, 0xffff0000, v62
	v_lshlrev_b32_e32 v62, 16, v63
	v_and_b32_e32 v63, 0xffff0000, v63
	v_lshlrev_b32_e32 v70, 16, v64
	v_and_b32_e32 v71, 0xffff0000, v64
	v_lshlrev_b32_e32 v64, 16, v65
	v_and_b32_e32 v65, 0xffff0000, v65
	v_pk_add_f32 v[56:57], v[56:57], v[62:63]
	v_pk_add_f32 v[54:55], v[54:55], v[68:69]
	v_pk_add_f32 v[62:63], v[52:53], v[64:65]
	v_pk_add_f32 v[64:65], v[50:51], v[70:71]
	v_mul_f32_e32 v50, v55, v55
	v_mul_f32_e32 v51, v57, v57
	v_mul_f32_e32 v52, v65, v65
	v_mul_f32_e32 v53, v63, v63
	v_fmac_f32_e32 v50, v54, v54
	v_fmac_f32_e32 v51, v56, v56
	v_fmac_f32_e32 v52, v64, v64
	v_fmac_f32_e32 v53, v62, v62
	v_add_f32_e32 v50, v50, v51
	v_add_f32_e32 v51, v52, v53
	v_add_f32_e32 v50, v50, v51
	v_add_f32_e32 v50, v74, v50
	ds_bpermute_b32 v51, v122, v50
	v_cvt_pk_bf16_f32 v52, v54, v55
	v_cvt_pk_bf16_f32 v53, v56, v57
	v_cvt_pk_bf16_f32 v54, v64, v65
	v_cvt_pk_bf16_f32 v55, v62, v63
	s_waitcnt lgkmcnt(0)
	v_add_f32_e32 v50, v50, v51
	ds_bpermute_b32 v51, v116, v50
	global_store_dwordx4 v[72:73], v[52:55], off offset:256 nt
	s_and_saveexec_b64 s[20:21], s[4:5]
	s_cbranch_execz .LBB0_569
	s_waitcnt lgkmcnt(0)
	v_add_f32_e32 v50, v50, v51
	v_fma_f32 v50, v50, s42, 0.5
	v_trunc_f32_e32 v50, v50
	v_mul_f32_e32 v51, 0x2f800000, v50
	v_floor_f32_e32 v51, v51
	v_fmac_f32_e32 v50, 0xcf800000, v51
	v_cvt_u32_f32_e32 v50, v50
	v_cvt_u32_f32_e32 v51, v51
	v_lshl_add_u64 v[52:53], v[66:67], 3, s[12:13]
	global_atomic_add_x2 v[52:53], v[50:51], off
.LBB0_569:
	s_or_b64 exec, exec, s[20:21]
	v_add_u32_e32 v50, 0x90, v150
	s_waitcnt lgkmcnt(0)
	v_ashrrev_i32_e32 v51, 31, v50
	v_lshlrev_b64 v[52:53], 12, v[50:51]
	v_lshl_add_u64 v[52:53], s[50:51], 0, v[52:53]
	v_lshl_add_u64 v[56:57], v[148:149], 1, v[52:53]
	s_nop 0
	s_waitcnt vmcnt(13)
	s_nop 1
	v_pk_mov_b32 v[52:53], v[176:177], v[176:177] op_sel:[0,1]
	v_pk_mov_b32 v[54:55], v[178:179], v[178:179] op_sel:[0,1]
	v_lshlrev_b32_e32 v58, 16, v52
	v_and_b32_e32 v59, 0xffff0000, v52
	v_lshlrev_b32_e32 v52, 16, v53
	v_and_b32_e32 v53, 0xffff0000, v53
	v_lshlrev_b32_e32 v60, 16, v54
	v_and_b32_e32 v61, 0xffff0000, v54
	v_lshlrev_b32_e32 v54, 16, v55
	v_and_b32_e32 v55, 0xffff0000, v55
	v_pk_add_f32 v[52:53], v[48:49], v[52:53]
	v_pk_add_f32 v[58:59], v[46:47], v[58:59]
	v_pk_add_f32 v[54:55], v[44:45], v[54:55]
	v_pk_add_f32 v[60:61], v[42:43], v[60:61]
	v_cvt_pk_bf16_f32 v42, v58, v59
	v_cvt_pk_bf16_f32 v43, v52, v53
	v_mul_f32_e32 v59, v59, v59
	v_cvt_pk_bf16_f32 v44, v60, v61
	v_cvt_pk_bf16_f32 v45, v54, v55
	s_nop 0
	v_mul_f32_e32 v53, v53, v53
	v_mul_f32_e32 v61, v61, v61
	v_mul_f32_e32 v55, v55, v55
	v_fmac_f32_e32 v59, v58, v58
	v_fmac_f32_e32 v53, v52, v52
	v_fmac_f32_e32 v61, v60, v60
	v_fmac_f32_e32 v55, v54, v54
	v_add_f32_e32 v52, v59, v53
	v_add_f32_e32 v53, v61, v55
	v_add_f32_e32 v58, v52, v53
	global_store_dwordx4 v[56:57], v[42:45], off nt
	s_nop 1
	v_pk_mov_b32 v[46:47], v[180:181], v[180:181] op_sel:[0,1]
	v_pk_mov_b32 v[48:49], v[182:183], v[182:183] op_sel:[0,1]
	v_lshlrev_b32_e32 v52, 16, v46
	v_and_b32_e32 v53, 0xffff0000, v46
	v_lshlrev_b32_e32 v46, 16, v47
	v_and_b32_e32 v47, 0xffff0000, v47
	v_lshlrev_b32_e32 v54, 16, v48
	v_and_b32_e32 v55, 0xffff0000, v48
	v_lshlrev_b32_e32 v48, 16, v49
	v_and_b32_e32 v49, 0xffff0000, v49
	v_pk_add_f32 v[40:41], v[40:41], v[46:47]
	v_pk_add_f32 v[38:39], v[38:39], v[52:53]
	v_pk_add_f32 v[46:47], v[36:37], v[48:49]
	v_pk_add_f32 v[48:49], v[34:35], v[54:55]
	v_mul_f32_e32 v34, v39, v39
	v_mul_f32_e32 v35, v41, v41
	v_mul_f32_e32 v36, v49, v49
	v_mul_f32_e32 v37, v47, v47
	v_fmac_f32_e32 v34, v38, v38
	v_fmac_f32_e32 v35, v40, v40
	v_fmac_f32_e32 v36, v48, v48
	v_fmac_f32_e32 v37, v46, v46
	v_add_f32_e32 v34, v34, v35
	v_add_f32_e32 v35, v36, v37
	v_add_f32_e32 v34, v34, v35
	v_add_f32_e32 v34, v58, v34
	ds_bpermute_b32 v35, v122, v34
	v_cvt_pk_bf16_f32 v36, v38, v39
	v_cvt_pk_bf16_f32 v37, v40, v41
	v_cvt_pk_bf16_f32 v38, v48, v49
	v_cvt_pk_bf16_f32 v39, v46, v47
	s_waitcnt lgkmcnt(0)
	v_add_f32_e32 v34, v34, v35
	ds_bpermute_b32 v35, v116, v34
	global_store_dwordx4 v[56:57], v[36:39], off offset:256 nt
	s_and_saveexec_b64 s[20:21], s[4:5]
	s_cbranch_execz .LBB0_571
	s_waitcnt lgkmcnt(0)
	v_add_f32_e32 v34, v34, v35
	v_fma_f32 v34, v34, s42, 0.5
	v_trunc_f32_e32 v34, v34
	v_mul_f32_e32 v35, 0x2f800000, v34
	v_floor_f32_e32 v35, v35
	v_fmac_f32_e32 v34, 0xcf800000, v35
	v_cvt_u32_f32_e32 v34, v34
	v_cvt_u32_f32_e32 v35, v35
	v_lshl_add_u64 v[36:37], v[50:51], 3, s[12:13]
	global_atomic_add_x2 v[36:37], v[34:35], off
.LBB0_571:
	s_or_b64 exec, exec, s[20:21]
	v_add_u32_e32 v34, 0xa0, v150
	s_waitcnt lgkmcnt(0)
	v_ashrrev_i32_e32 v35, 31, v34
	v_lshlrev_b64 v[36:37], 12, v[34:35]
	v_lshl_add_u64 v[36:37], s[50:51], 0, v[36:37]
	v_lshl_add_u64 v[40:41], v[148:149], 1, v[36:37]
	s_nop 0
	s_waitcnt vmcnt(11)
	s_nop 1
	v_pk_mov_b32 v[36:37], v[190:191], v[190:191] op_sel:[0,1]
	v_pk_mov_b32 v[38:39], v[192:193], v[192:193] op_sel:[0,1]
	v_lshlrev_b32_e32 v42, 16, v36
	v_and_b32_e32 v43, 0xffff0000, v36
	v_lshlrev_b32_e32 v36, 16, v37
	v_and_b32_e32 v37, 0xffff0000, v37
	v_lshlrev_b32_e32 v44, 16, v38
	v_and_b32_e32 v45, 0xffff0000, v38
	v_lshlrev_b32_e32 v38, 16, v39
	v_and_b32_e32 v39, 0xffff0000, v39
	v_pk_add_f32 v[36:37], v[32:33], v[36:37]
	v_pk_add_f32 v[42:43], v[30:31], v[42:43]
	v_pk_add_f32 v[38:39], v[28:29], v[38:39]
	v_pk_add_f32 v[44:45], v[26:27], v[44:45]
	v_cvt_pk_bf16_f32 v26, v42, v43
	v_cvt_pk_bf16_f32 v27, v36, v37
	v_mul_f32_e32 v43, v43, v43
	v_cvt_pk_bf16_f32 v28, v44, v45
	v_cvt_pk_bf16_f32 v29, v38, v39
	s_nop 0
	v_mul_f32_e32 v37, v37, v37
	v_mul_f32_e32 v45, v45, v45
	v_mul_f32_e32 v39, v39, v39
	v_fmac_f32_e32 v43, v42, v42
	v_fmac_f32_e32 v37, v36, v36
	v_fmac_f32_e32 v45, v44, v44
	v_fmac_f32_e32 v39, v38, v38
	v_add_f32_e32 v36, v43, v37
	v_add_f32_e32 v37, v45, v39
	v_add_f32_e32 v42, v36, v37
	global_store_dwordx4 v[40:41], v[26:29], off nt
	s_nop 1
	v_pk_mov_b32 v[30:31], v[194:195], v[194:195] op_sel:[0,1]
	v_pk_mov_b32 v[32:33], v[196:197], v[196:197] op_sel:[0,1]
	v_lshlrev_b32_e32 v36, 16, v30
	v_and_b32_e32 v37, 0xffff0000, v30
	v_lshlrev_b32_e32 v30, 16, v31
	v_and_b32_e32 v31, 0xffff0000, v31
	v_lshlrev_b32_e32 v38, 16, v32
	v_and_b32_e32 v39, 0xffff0000, v32
	v_lshlrev_b32_e32 v32, 16, v33
	v_and_b32_e32 v33, 0xffff0000, v33
	v_pk_add_f32 v[24:25], v[24:25], v[30:31]
	v_pk_add_f32 v[22:23], v[22:23], v[36:37]
	v_pk_add_f32 v[30:31], v[20:21], v[32:33]
	v_pk_add_f32 v[32:33], v[18:19], v[38:39]
	v_mul_f32_e32 v18, v23, v23
	v_mul_f32_e32 v19, v25, v25
	v_mul_f32_e32 v20, v33, v33
	v_mul_f32_e32 v21, v31, v31
	v_fmac_f32_e32 v18, v22, v22
	v_fmac_f32_e32 v19, v24, v24
	v_fmac_f32_e32 v20, v32, v32
	v_fmac_f32_e32 v21, v30, v30
	v_add_f32_e32 v18, v18, v19
	v_add_f32_e32 v19, v20, v21
	v_add_f32_e32 v18, v18, v19
	v_add_f32_e32 v18, v42, v18
	ds_bpermute_b32 v19, v122, v18
	v_cvt_pk_bf16_f32 v20, v22, v23
	v_cvt_pk_bf16_f32 v21, v24, v25
	v_cvt_pk_bf16_f32 v22, v32, v33
	v_cvt_pk_bf16_f32 v23, v30, v31
	s_waitcnt lgkmcnt(0)
	v_add_f32_e32 v18, v18, v19
	ds_bpermute_b32 v19, v116, v18
	global_store_dwordx4 v[40:41], v[20:23], off offset:256 nt
	s_and_saveexec_b64 s[20:21], s[4:5]
	s_cbranch_execz .LBB0_573
	s_waitcnt lgkmcnt(0)
	v_add_f32_e32 v18, v18, v19
	v_fma_f32 v18, v18, s42, 0.5
	v_trunc_f32_e32 v18, v18
	v_mul_f32_e32 v19, 0x2f800000, v18
	v_floor_f32_e32 v19, v19
	v_fmac_f32_e32 v18, 0xcf800000, v19
	v_cvt_u32_f32_e32 v18, v18
	v_cvt_u32_f32_e32 v19, v19
	v_lshl_add_u64 v[20:21], v[34:35], 3, s[12:13]
	global_atomic_add_x2 v[20:21], v[18:19], off
.LBB0_573:
	s_or_b64 exec, exec, s[20:21]
	v_add_u32_e32 v18, 0xb0, v150
	s_waitcnt lgkmcnt(0)
	v_ashrrev_i32_e32 v19, 31, v18
	v_lshlrev_b64 v[20:21], 12, v[18:19]
	v_lshl_add_u64 v[20:21], s[50:51], 0, v[20:21]
	v_lshl_add_u64 v[24:25], v[148:149], 1, v[20:21]
	s_nop 0
	s_waitcnt vmcnt(9)
	s_nop 1
	v_pk_mov_b32 v[20:21], v[198:199], v[198:199] op_sel:[0,1]
	v_pk_mov_b32 v[22:23], v[200:201], v[200:201] op_sel:[0,1]
	v_lshlrev_b32_e32 v26, 16, v20
	v_and_b32_e32 v27, 0xffff0000, v20
	v_lshlrev_b32_e32 v20, 16, v21
	v_and_b32_e32 v21, 0xffff0000, v21
	v_lshlrev_b32_e32 v28, 16, v22
	v_and_b32_e32 v29, 0xffff0000, v22
	v_lshlrev_b32_e32 v22, 16, v23
	v_and_b32_e32 v23, 0xffff0000, v23
	v_pk_add_f32 v[20:21], v[16:17], v[20:21]
	v_pk_add_f32 v[26:27], v[14:15], v[26:27]
	v_pk_add_f32 v[22:23], v[12:13], v[22:23]
	v_pk_add_f32 v[28:29], v[10:11], v[28:29]
	v_cvt_pk_bf16_f32 v10, v26, v27
	v_cvt_pk_bf16_f32 v11, v20, v21
	v_mul_f32_e32 v27, v27, v27
	v_cvt_pk_bf16_f32 v12, v28, v29
	v_cvt_pk_bf16_f32 v13, v22, v23
	s_nop 0
	v_mul_f32_e32 v21, v21, v21
	v_mul_f32_e32 v29, v29, v29
	v_mul_f32_e32 v23, v23, v23
	v_fmac_f32_e32 v27, v26, v26
	v_fmac_f32_e32 v21, v20, v20
	v_fmac_f32_e32 v29, v28, v28
	v_fmac_f32_e32 v23, v22, v22
	v_add_f32_e32 v20, v27, v21
	v_add_f32_e32 v21, v29, v23
	v_add_f32_e32 v26, v20, v21
	global_store_dwordx4 v[24:25], v[10:13], off nt
	s_nop 1
	v_pk_mov_b32 v[14:15], v[202:203], v[202:203] op_sel:[0,1]
	v_pk_mov_b32 v[16:17], v[204:205], v[204:205] op_sel:[0,1]
	v_lshlrev_b32_e32 v20, 16, v14
	v_and_b32_e32 v21, 0xffff0000, v14
	v_lshlrev_b32_e32 v14, 16, v15
	v_and_b32_e32 v15, 0xffff0000, v15
	v_lshlrev_b32_e32 v22, 16, v16
	v_and_b32_e32 v23, 0xffff0000, v16
	v_lshlrev_b32_e32 v16, 16, v17
	v_and_b32_e32 v17, 0xffff0000, v17
	v_pk_add_f32 v[8:9], v[8:9], v[14:15]
	v_pk_add_f32 v[6:7], v[6:7], v[20:21]
	v_pk_add_f32 v[14:15], v[4:5], v[16:17]
	v_pk_add_f32 v[16:17], v[2:3], v[22:23]
	v_mul_f32_e32 v2, v7, v7
	v_mul_f32_e32 v3, v9, v9
	v_mul_f32_e32 v4, v17, v17
	v_mul_f32_e32 v5, v15, v15
	v_fmac_f32_e32 v2, v6, v6
	v_fmac_f32_e32 v3, v8, v8
	v_fmac_f32_e32 v4, v16, v16
	v_fmac_f32_e32 v5, v14, v14
	v_add_f32_e32 v2, v2, v3
	v_add_f32_e32 v3, v4, v5
	v_add_f32_e32 v2, v2, v3
	v_add_f32_e32 v2, v26, v2
	ds_bpermute_b32 v3, v122, v2
	v_cvt_pk_bf16_f32 v4, v6, v7
	v_cvt_pk_bf16_f32 v5, v8, v9
	v_cvt_pk_bf16_f32 v6, v16, v17
	v_cvt_pk_bf16_f32 v7, v14, v15
	s_waitcnt lgkmcnt(0)
	v_add_f32_e32 v2, v2, v3
	ds_bpermute_b32 v3, v116, v2
	global_store_dwordx4 v[24:25], v[4:7], off offset:256 nt
	s_and_saveexec_b64 s[20:21], s[4:5]
	s_cbranch_execz .LBB0_575
	s_waitcnt lgkmcnt(0)
	v_add_f32_e32 v2, v2, v3
	v_fma_f32 v2, v2, s42, 0.5
	v_trunc_f32_e32 v2, v2
	v_mul_f32_e32 v3, 0x2f800000, v2
	v_floor_f32_e32 v3, v3
	v_fmac_f32_e32 v2, 0xcf800000, v3
	v_cvt_u32_f32_e32 v2, v2
	v_cvt_u32_f32_e32 v3, v3
	v_lshl_add_u64 v[4:5], v[18:19], 3, s[12:13]
	global_atomic_add_x2 v[4:5], v[2:3], off

.LBB0_654:
	v_lshl_add_u32 v152, s0, 8, v154
	v_ashrrev_i32_e32 v153, 31, v152
	v_lshl_add_u64 v[148:149], v[152:153], 3, s[12:13]
	global_load_dwordx2 v[150:151], v[148:149], off
	global_load_dwordx2 v[178:179], v[148:149], off offset:128
	global_load_dwordx2 v[180:181], v[148:149], off offset:256
	global_load_dwordx2 v[182:183], v[148:149], off offset:384
	global_load_dwordx2 v[184:185], v[148:149], off offset:1024
	global_load_dwordx2 v[186:187], v[148:149], off offset:1152
	global_load_dwordx2 v[188:189], v[148:149], off offset:1280
	global_load_dwordx2 v[190:191], v[148:149], off offset:1408
	v_lshlrev_b64 v[166:167], 14, v[152:153]
	v_lshl_or_b32 v162, s1, 8, v156
	v_ashrrev_i32_e32 v163, 31, v162
	v_or_b32_e32 v164, 16, v152
	v_lshlrev_b64 v[162:163], 1, v[162:163]
	v_ashrrev_i32_e32 v165, 31, v164
	s_mov_b64 s[0:1], 0x200000
	s_waitcnt vmcnt(7)
	v_ffbh_u32_e32 v153, v151
	v_min_u32_e32 v153, 32, v153
	v_lshlrev_b64 v[150:151], v153, v[150:151]
	v_min_u32_e32 v150, 1, v150
	v_or_b32_e32 v150, v151, v150
	v_cvt_f32_u32_e32 v150, v150
	v_sub_u32_e32 v151, 32, v153
	v_ldexp_f32 v150, v150, v151
	v_fmamk_f32 v150, v150, 0x30000000, v161
	v_rsq_f32_e32 v168, v150
	v_lshl_add_u64 v[150:151], s[10:11], 0, v[166:167]
	v_lshl_add_u64 v[150:151], v[150:151], 0, v[162:163]
	v_lshl_add_u64 v[166:167], v[164:165], 3, s[12:13]
	v_pk_mul_f32 v[128:129], v[128:129], v[168:169] op_sel_hi:[1,0]
	v_pk_mul_f32 v[126:127], v[126:127], v[168:169] op_sel_hi:[1,0]
	v_pk_mul_f32 v[124:125], v[124:125], v[168:169] op_sel_hi:[1,0]
	v_pk_mul_f32 v[122:123], v[122:123], v[168:169] op_sel_hi:[1,0]
	v_pk_mul_f32 v[120:121], v[120:121], v[168:169] op_sel_hi:[1,0]
	v_pk_mul_f32 v[118:119], v[118:119], v[168:169] op_sel_hi:[1,0]
	v_pk_mul_f32 v[170:171], v[116:117], v[168:169] op_sel_hi:[1,0]
	v_pk_mul_f32 v[168:169], v[114:115], v[168:169] op_sel_hi:[1,0]
	v_cvt_pk_bf16_f32 v114, v126, v127
	v_cvt_pk_bf16_f32 v115, v128, v129
	v_cvt_pk_bf16_f32 v116, v122, v123
	v_cvt_pk_bf16_f32 v117, v124, v125
	global_store_dwordx4 v[150:151], v[114:117], off nt
	s_nop 1
	v_cvt_pk_bf16_f32 v114, v118, v119
	v_cvt_pk_bf16_f32 v115, v120, v121
	v_cvt_pk_bf16_f32 v116, v168, v169
	v_cvt_pk_bf16_f32 v117, v170, v171
	global_store_dwordx4 v[150:151], v[114:117], off offset:256 nt
	s_nop 0
	s_nop 0
	v_or_b32_e32 v116, 32, v152
	s_waitcnt vmcnt(8)
	v_mov_b32_e32 v114, v178
	v_mov_b32_e32 v115, v179
	v_ffbh_u32_e32 v117, v115
	v_min_u32_e32 v118, 32, v117
	v_lshlrev_b64 v[114:115], v118, v[114:115]
	v_min_u32_e32 v114, 1, v114
	v_or_b32_e32 v114, v115, v114
	v_cvt_f32_u32_e32 v119, v114
	v_sub_u32_e32 v118, 32, v118
	v_lshlrev_b64 v[114:115], 14, v[164:165]
	v_lshl_add_u64 v[114:115], s[10:11], 0, v[114:115]
	v_ldexp_f32 v118, v119, v118
	v_fmamk_f32 v118, v118, 0x30000000, v161
	v_rsq_f32_e32 v118, v118
	v_ashrrev_i32_e32 v117, 31, v116
	v_lshl_add_u64 v[114:115], v[114:115], 0, v[162:163]
	v_lshl_add_u64 v[120:121], v[116:117], 3, s[12:13]
	v_pk_mul_f32 v[112:113], v[112:113], v[118:119] op_sel_hi:[1,0]
	v_pk_mul_f32 v[110:111], v[110:111], v[118:119] op_sel_hi:[1,0]
	v_pk_mul_f32 v[108:109], v[108:109], v[118:119] op_sel_hi:[1,0]
	v_pk_mul_f32 v[106:107], v[106:107], v[118:119] op_sel_hi:[1,0]
	v_pk_mul_f32 v[104:105], v[104:105], v[118:119] op_sel_hi:[1,0]
	v_pk_mul_f32 v[102:103], v[102:103], v[118:119] op_sel_hi:[1,0]
	v_pk_mul_f32 v[122:123], v[100:101], v[118:119] op_sel_hi:[1,0]
	v_pk_mul_f32 v[118:119], v[98:99], v[118:119] op_sel_hi:[1,0]
	v_cvt_pk_bf16_f32 v98, v110, v111
	v_cvt_pk_bf16_f32 v99, v112, v113
	v_cvt_pk_bf16_f32 v100, v106, v107
	v_cvt_pk_bf16_f32 v101, v108, v109
	global_store_dwordx4 v[114:115], v[98:101], off nt
	s_nop 1
	v_cvt_pk_bf16_f32 v98, v102, v103
	v_cvt_pk_bf16_f32 v99, v104, v105
	v_cvt_pk_bf16_f32 v100, v118, v119
	v_cvt_pk_bf16_f32 v101, v122, v123
	global_store_dwordx4 v[114:115], v[98:101], off offset:256 nt
	s_nop 0
	s_nop 0
	v_or_b32_e32 v100, 48, v152
	s_waitcnt vmcnt(9)
	v_mov_b32_e32 v98, v180
	v_mov_b32_e32 v99, v181
	v_ffbh_u32_e32 v101, v99
	v_min_u32_e32 v102, 32, v101
	v_lshlrev_b64 v[98:99], v102, v[98:99]
	v_min_u32_e32 v98, 1, v98
	v_or_b32_e32 v98, v99, v98
	v_cvt_f32_u32_e32 v103, v98
	v_sub_u32_e32 v102, 32, v102
	v_lshlrev_b64 v[98:99], 14, v[116:117]
	v_lshl_add_u64 v[98:99], s[10:11], 0, v[98:99]
	v_ldexp_f32 v102, v103, v102
	v_fmamk_f32 v102, v102, 0x30000000, v161
	v_rsq_f32_e32 v102, v102
	v_ashrrev_i32_e32 v101, 31, v100
	v_lshl_add_u64 v[98:99], v[98:99], 0, v[162:163]
	v_lshl_add_u64 v[104:105], v[100:101], 3, s[12:13]
	v_pk_mul_f32 v[96:97], v[96:97], v[102:103] op_sel_hi:[1,0]
	v_pk_mul_f32 v[94:95], v[94:95], v[102:103] op_sel_hi:[1,0]
	v_pk_mul_f32 v[92:93], v[92:93], v[102:103] op_sel_hi:[1,0]
	v_pk_mul_f32 v[90:91], v[90:91], v[102:103] op_sel_hi:[1,0]
	v_pk_mul_f32 v[88:89], v[88:89], v[102:103] op_sel_hi:[1,0]
	v_pk_mul_f32 v[86:87], v[86:87], v[102:103] op_sel_hi:[1,0]
	v_pk_mul_f32 v[106:107], v[84:85], v[102:103] op_sel_hi:[1,0]
	v_pk_mul_f32 v[102:103], v[82:83], v[102:103] op_sel_hi:[1,0]
	v_cvt_pk_bf16_f32 v82, v94, v95
	v_cvt_pk_bf16_f32 v83, v96, v97
	v_cvt_pk_bf16_f32 v84, v90, v91
	v_cvt_pk_bf16_f32 v85, v92, v93
	global_store_dwordx4 v[98:99], v[82:85], off nt
	s_nop 1
	v_cvt_pk_bf16_f32 v82, v86, v87
	v_cvt_pk_bf16_f32 v83, v88, v89
	v_cvt_pk_bf16_f32 v84, v102, v103
	v_cvt_pk_bf16_f32 v85, v106, v107
	global_store_dwordx4 v[98:99], v[82:85], off offset:256 nt
	s_nop 0
	s_waitcnt vmcnt(10)
	v_mov_b32_e32 v82, v182
	v_mov_b32_e32 v83, v183
	v_ffbh_u32_e32 v84, v83
	v_min_u32_e32 v84, 32, v84
	v_lshlrev_b64 v[82:83], v84, v[82:83]
	v_min_u32_e32 v82, 1, v82
	v_or_b32_e32 v82, v83, v82
	v_cvt_f32_u32_e32 v82, v82
	v_sub_u32_e32 v83, 32, v84
	v_lshlrev_b64 v[84:85], 14, v[100:101]
	v_lshl_add_u64 v[84:85], s[10:11], 0, v[84:85]
	v_ldexp_f32 v82, v82, v83
	v_fmamk_f32 v82, v82, 0x30000000, v161
	v_rsq_f32_e32 v82, v82
	v_lshl_add_u64 v[84:85], v[84:85], 0, v[162:163]
	v_pk_mul_f32 v[80:81], v[80:81], v[82:83] op_sel_hi:[1,0]
	v_pk_mul_f32 v[78:79], v[78:79], v[82:83] op_sel_hi:[1,0]
	v_pk_mul_f32 v[76:77], v[76:77], v[82:83] op_sel_hi:[1,0]
	v_pk_mul_f32 v[74:75], v[74:75], v[82:83] op_sel_hi:[1,0]
	v_pk_mul_f32 v[72:73], v[72:73], v[82:83] op_sel_hi:[1,0]
	v_pk_mul_f32 v[70:71], v[70:71], v[82:83] op_sel_hi:[1,0]
	v_pk_mul_f32 v[86:87], v[68:69], v[82:83] op_sel_hi:[1,0]
	v_pk_mul_f32 v[82:83], v[66:67], v[82:83] op_sel_hi:[1,0]
	v_cvt_pk_bf16_f32 v66, v78, v79
	v_cvt_pk_bf16_f32 v67, v80, v81
	v_cvt_pk_bf16_f32 v68, v74, v75
	v_cvt_pk_bf16_f32 v69, v76, v77
	global_store_dwordx4 v[84:85], v[66:69], off nt
	s_nop 1
	v_cvt_pk_bf16_f32 v66, v70, v71
	v_cvt_pk_bf16_f32 v67, v72, v73
	v_cvt_pk_bf16_f32 v68, v82, v83
	v_cvt_pk_bf16_f32 v69, v86, v87
	global_store_dwordx4 v[84:85], v[66:69], off offset:256 nt
	s_nop 0
	v_add_co_u32_e32 v70, vcc, s58, v150
	s_waitcnt vmcnt(11)
	v_mov_b32_e32 v66, v184
	v_mov_b32_e32 v67, v185
	v_ffbh_u32_e32 v68, v67
	v_min_u32_e32 v68, 32, v68
	v_lshlrev_b64 v[66:67], v68, v[66:67]
	v_min_u32_e32 v66, 1, v66
	v_or_b32_e32 v66, v67, v66
	v_cvt_f32_u32_e32 v69, v66
	v_sub_u32_e32 v68, 32, v68
	v_lshl_add_u64 v[66:67], v[150:151], 0, s[0:1]
	v_addc_co_u32_e32 v71, vcc, 0, v151, vcc
	v_ldexp_f32 v68, v69, v68
	v_fmamk_f32 v68, v68, 0x30000000, v161
	v_rsq_f32_e32 v68, v68
	s_nop 0
	v_pk_mul_f32 v[64:65], v[64:65], v[68:69] op_sel_hi:[1,0]
	v_pk_mul_f32 v[62:63], v[62:63], v[68:69] op_sel_hi:[1,0]
	v_pk_mul_f32 v[60:61], v[60:61], v[68:69] op_sel_hi:[1,0]
	v_pk_mul_f32 v[58:59], v[58:59], v[68:69] op_sel_hi:[1,0]
	v_pk_mul_f32 v[56:57], v[56:57], v[68:69] op_sel_hi:[1,0]
	v_pk_mul_f32 v[54:55], v[54:55], v[68:69] op_sel_hi:[1,0]
	v_pk_mul_f32 v[72:73], v[52:53], v[68:69] op_sel_hi:[1,0]
	v_pk_mul_f32 v[68:69], v[50:51], v[68:69] op_sel_hi:[1,0]
	v_cvt_pk_bf16_f32 v50, v62, v63
	v_cvt_pk_bf16_f32 v51, v64, v65
	v_cvt_pk_bf16_f32 v52, v58, v59
	v_cvt_pk_bf16_f32 v53, v60, v61
	global_store_dwordx4 v[70:71], v[50:53], off nt
	s_nop 1
	v_cvt_pk_bf16_f32 v50, v54, v55
	v_cvt_pk_bf16_f32 v51, v56, v57
	v_cvt_pk_bf16_f32 v52, v68, v69
	v_cvt_pk_bf16_f32 v53, v72, v73
	global_store_dwordx4 v[66:67], v[50:53], off offset:256 nt
	s_nop 0
	v_add_co_u32_e32 v54, vcc, s59, v150
	s_waitcnt vmcnt(12)
	v_mov_b32_e32 v50, v186
	v_mov_b32_e32 v51, v187
	v_ffbh_u32_e32 v52, v51
	v_min_u32_e32 v52, 32, v52
	v_lshlrev_b64 v[50:51], v52, v[50:51]
	v_min_u32_e32 v50, 1, v50
	v_or_b32_e32 v50, v51, v50
	v_cvt_f32_u32_e32 v53, v50
	v_sub_u32_e32 v52, 32, v52
	v_lshl_add_u64 v[50:51], v[150:151], 0, s[18:19]
	v_addc_co_u32_e32 v55, vcc, 0, v151, vcc
	v_ldexp_f32 v52, v53, v52
	v_fmamk_f32 v52, v52, 0x30000000, v161
	v_rsq_f32_e32 v52, v52
	s_nop 0
	v_pk_mul_f32 v[48:49], v[48:49], v[52:53] op_sel_hi:[1,0]
	v_pk_mul_f32 v[46:47], v[46:47], v[52:53] op_sel_hi:[1,0]
	v_pk_mul_f32 v[44:45], v[44:45], v[52:53] op_sel_hi:[1,0]
	v_pk_mul_f32 v[42:43], v[42:43], v[52:53] op_sel_hi:[1,0]
	v_pk_mul_f32 v[40:41], v[40:41], v[52:53] op_sel_hi:[1,0]
	v_pk_mul_f32 v[38:39], v[38:39], v[52:53] op_sel_hi:[1,0]
	v_pk_mul_f32 v[56:57], v[36:37], v[52:53] op_sel_hi:[1,0]
	v_pk_mul_f32 v[52:53], v[34:35], v[52:53] op_sel_hi:[1,0]
	v_cvt_pk_bf16_f32 v34, v46, v47
	v_cvt_pk_bf16_f32 v35, v48, v49
	v_cvt_pk_bf16_f32 v36, v42, v43
	v_cvt_pk_bf16_f32 v37, v44, v45
	global_store_dwordx4 v[54:55], v[34:37], off nt
	s_nop 1
	v_cvt_pk_bf16_f32 v34, v38, v39
	v_cvt_pk_bf16_f32 v35, v40, v41
	v_cvt_pk_bf16_f32 v36, v52, v53
	v_cvt_pk_bf16_f32 v37, v56, v57
	global_store_dwordx4 v[50:51], v[34:37], off offset:256 nt
	s_nop 0
	v_add_co_u32_e32 v38, vcc, s60, v150
	s_waitcnt vmcnt(13)
	v_mov_b32_e32 v34, v188
	v_mov_b32_e32 v35, v189
	v_ffbh_u32_e32 v36, v35
	v_min_u32_e32 v36, 32, v36
	v_lshlrev_b64 v[34:35], v36, v[34:35]
	v_min_u32_e32 v34, 1, v34
	v_or_b32_e32 v34, v35, v34
	v_cvt_f32_u32_e32 v37, v34
	v_sub_u32_e32 v36, 32, v36
	v_lshl_add_u64 v[34:35], v[150:151], 0, s[20:21]
	v_addc_co_u32_e32 v39, vcc, 0, v151, vcc
	v_ldexp_f32 v36, v37, v36
	v_fmamk_f32 v36, v36, 0x30000000, v161
	v_rsq_f32_e32 v36, v36
	s_andn2_b64 vcc, exec, s[4:5]
	v_pk_mul_f32 v[32:33], v[32:33], v[36:37] op_sel_hi:[1,0]
	v_pk_mul_f32 v[30:31], v[30:31], v[36:37] op_sel_hi:[1,0]
	v_pk_mul_f32 v[28:29], v[28:29], v[36:37] op_sel_hi:[1,0]
	v_pk_mul_f32 v[26:27], v[26:27], v[36:37] op_sel_hi:[1,0]
	v_pk_mul_f32 v[24:25], v[24:25], v[36:37] op_sel_hi:[1,0]
	v_pk_mul_f32 v[22:23], v[22:23], v[36:37] op_sel_hi:[1,0]
	v_pk_mul_f32 v[40:41], v[20:21], v[36:37] op_sel_hi:[1,0]
	v_pk_mul_f32 v[36:37], v[18:19], v[36:37] op_sel_hi:[1,0]
	v_cvt_pk_bf16_f32 v18, v30, v31
	v_cvt_pk_bf16_f32 v19, v32, v33
	v_cvt_pk_bf16_f32 v20, v26, v27
	v_cvt_pk_bf16_f32 v21, v28, v29
	global_store_dwordx4 v[38:39], v[18:21], off nt
	s_nop 1
	v_cvt_pk_bf16_f32 v18, v22, v23
	v_cvt_pk_bf16_f32 v19, v24, v25
	v_cvt_pk_bf16_f32 v20, v36, v37
	v_cvt_pk_bf16_f32 v21, v40, v41
	global_store_dwordx4 v[34:35], v[18:21], off offset:256 nt
	s_nop 0
	v_add_co_u32_e64 v22, s[0:1], s61, v150
	s_waitcnt vmcnt(14)
	v_mov_b32_e32 v18, v190
	v_mov_b32_e32 v19, v191
	v_ffbh_u32_e32 v20, v19
	v_min_u32_e32 v20, 32, v20
	v_lshlrev_b64 v[18:19], v20, v[18:19]
	v_min_u32_e32 v18, 1, v18
	v_or_b32_e32 v18, v19, v18
	v_cvt_f32_u32_e32 v21, v18
	v_sub_u32_e32 v20, 32, v20
	v_addc_co_u32_e64 v23, s[0:1], 0, v151, s[0:1]
	v_ldexp_f32 v20, v21, v20
	v_fmamk_f32 v20, v20, 0x30000000, v161
	v_rsq_f32_e32 v20, v20
	v_lshl_add_u64 v[18:19], v[150:151], 0, s[22:23]
	s_mov_b64 s[0:1], -1
	v_pk_mul_f32 v[16:17], v[16:17], v[20:21] op_sel_hi:[1,0]
	v_pk_mul_f32 v[14:15], v[14:15], v[20:21] op_sel_hi:[1,0]
	v_pk_mul_f32 v[12:13], v[12:13], v[20:21] op_sel_hi:[1,0]
	v_pk_mul_f32 v[10:11], v[10:11], v[20:21] op_sel_hi:[1,0]
	v_pk_mul_f32 v[8:9], v[8:9], v[20:21] op_sel_hi:[1,0]
	v_pk_mul_f32 v[6:7], v[6:7], v[20:21] op_sel_hi:[1,0]
	v_pk_mul_f32 v[24:25], v[4:5], v[20:21] op_sel_hi:[1,0]
	v_pk_mul_f32 v[20:21], v[2:3], v[20:21] op_sel_hi:[1,0]
	v_cvt_pk_bf16_f32 v2, v14, v15
	v_cvt_pk_bf16_f32 v3, v16, v17
	v_cvt_pk_bf16_f32 v4, v10, v11
	v_cvt_pk_bf16_f32 v5, v12, v13
	global_store_dwordx4 v[22:23], v[2:5], off nt
	s_nop 1
	v_cvt_pk_bf16_f32 v2, v6, v7
	v_cvt_pk_bf16_f32 v3, v8, v9
	v_cvt_pk_bf16_f32 v4, v20, v21
	v_cvt_pk_bf16_f32 v5, v24, v25
	global_store_dwordx4 v[18:19], v[2:5], off offset:256 nt
	s_cbranch_vccnz .LBB0_643
	s_andn2_b64 vcc, exec, s[8:9]
	s_cbranch_vccnz .LBB0_642
	s_barrier
	s_branch .LBB0_642

.LBB0_851:
	v_lshl_add_u32 v152, s30, 8, v154
	v_lshl_or_b32 v150, s57, 8, v156
	v_ashrrev_i32_e32 v153, 31, v152
	v_ashrrev_i32_e32 v151, 31, v150
	v_lshlrev_b64 v[148:149], 11, v[152:153]
	v_lshl_add_u64 v[148:149], v[148:149], 0, v[150:151]
	v_lshl_add_u64 v[166:167], v[148:149], 1, s[50:51]
	v_mov_b32_e32 v222, v166
	v_mov_b32_e32 v223, v167
	v_mov_b32_e32 v240, 0x10000
	v_mov_b32_e32 v241, 0
	global_load_dwordx4 v[174:177], v[222:223], off
	global_load_dwordx4 v[178:181], v[222:223], off offset:256
	v_lshl_add_u64 v[222:223], v[240:241], 0, v[222:223]
	global_load_dwordx4 v[182:185], v[222:223], off
	global_load_dwordx4 v[186:189], v[222:223], off offset:256
	v_lshl_add_u64 v[222:223], v[240:241], 0, v[222:223]
	global_load_dwordx4 v[190:193], v[222:223], off
	global_load_dwordx4 v[194:197], v[222:223], off offset:256
	v_lshl_add_u64 v[222:223], v[240:241], 0, v[222:223]
	global_load_dwordx4 v[198:201], v[222:223], off
	global_load_dwordx4 v[202:205], v[222:223], off offset:256
	v_lshl_add_u64 v[222:223], v[240:241], 2, v[222:223]
	v_lshl_add_u64 v[222:223], v[240:241], 0, v[222:223]
	global_load_dwordx4 v[206:209], v[222:223], off
	global_load_dwordx4 v[210:213], v[222:223], off offset:256
	v_lshl_add_u64 v[222:223], v[240:241], 0, v[222:223]
	global_load_dwordx4 v[214:217], v[222:223], off
	global_load_dwordx4 v[218:221], v[222:223], off offset:256
	s_nop 0
	v_lshl_add_u64 v[168:169], v[148:149], 2, s[28:29]
	s_andn2_b64 vcc, exec, s[4:5]
	s_mov_b64 s[4:5], -1
	s_waitcnt vmcnt(10)
	s_nop 1
	v_pk_mov_b32 v[162:163], v[174:175], v[174:175] op_sel:[0,1]
	v_pk_mov_b32 v[164:165], v[176:177], v[176:177] op_sel:[0,1]
	v_lshlrev_b32_e32 v170, 16, v162
	v_and_b32_e32 v171, 0xffff0000, v162
	v_lshlrev_b32_e32 v162, 16, v163
	v_and_b32_e32 v163, 0xffff0000, v163
	v_lshlrev_b32_e32 v172, 16, v164
	v_and_b32_e32 v173, 0xffff0000, v164
	v_lshlrev_b32_e32 v164, 16, v165
	v_and_b32_e32 v165, 0xffff0000, v165
	v_pk_add_f32 v[128:129], v[128:129], v[162:163]
	v_pk_add_f32 v[126:127], v[126:127], v[170:171]
	v_pk_add_f32 v[124:125], v[124:125], v[164:165]
	v_pk_add_f32 v[122:123], v[122:123], v[172:173]
	global_store_dwordx4 v[168:169], v[126:129], off nt
	global_store_dwordx4 v[168:169], v[122:125], off offset:16 nt
	s_nop 0
	v_or_b32_e32 v126, 16, v152
	v_ashrrev_i32_e32 v127, 31, v126
	v_lshlrev_b64 v[126:127], 11, v[126:127]
	v_lshl_add_u64 v[126:127], v[126:127], 0, v[150:151]
	v_lshl_add_u64 v[128:129], v[126:127], 1, s[50:51]
	s_nop 1
	v_pk_mov_b32 v[122:123], v[178:179], v[178:179] op_sel:[0,1]
	v_pk_mov_b32 v[124:125], v[180:181], v[180:181] op_sel:[0,1]
	v_lshl_add_u64 v[222:223], v[240:241], 0, v[222:223]
	global_load_dwordx4 v[174:177], v[222:223], off
	global_load_dwordx4 v[178:181], v[222:223], off offset:256
	v_lshlrev_b32_e32 v162, 16, v122
	v_and_b32_e32 v163, 0xffff0000, v122
	v_lshlrev_b32_e32 v122, 16, v123
	v_and_b32_e32 v123, 0xffff0000, v123
	v_lshlrev_b32_e32 v164, 16, v124
	v_and_b32_e32 v165, 0xffff0000, v124
	v_lshlrev_b32_e32 v124, 16, v125
	v_and_b32_e32 v125, 0xffff0000, v125
	v_pk_add_f32 v[120:121], v[120:121], v[122:123]
	v_pk_add_f32 v[118:119], v[118:119], v[162:163]
	v_pk_add_f32 v[116:117], v[116:117], v[124:125]
	v_pk_add_f32 v[114:115], v[114:115], v[164:165]
	global_store_dwordx4 v[168:169], v[118:121], off offset:512 nt
	global_store_dwordx4 v[168:169], v[114:117], off offset:528 nt
	s_nop 0
	v_lshl_add_u64 v[118:119], v[126:127], 2, s[28:29]
	s_waitcnt vmcnt(14)
	s_nop 1
	v_pk_mov_b32 v[114:115], v[182:183], v[182:183] op_sel:[0,1]
	v_pk_mov_b32 v[116:117], v[184:185], v[184:185] op_sel:[0,1]
	v_lshlrev_b32_e32 v120, 16, v114
	v_and_b32_e32 v121, 0xffff0000, v114
	v_lshlrev_b32_e32 v114, 16, v115
	v_and_b32_e32 v115, 0xffff0000, v115
	v_lshlrev_b32_e32 v122, 16, v116
	v_and_b32_e32 v123, 0xffff0000, v116
	v_lshlrev_b32_e32 v116, 16, v117
	v_and_b32_e32 v117, 0xffff0000, v117
	v_pk_add_f32 v[112:113], v[112:113], v[114:115]
	v_pk_add_f32 v[110:111], v[110:111], v[120:121]
	v_pk_add_f32 v[108:109], v[108:109], v[116:117]
	v_pk_add_f32 v[106:107], v[106:107], v[122:123]
	global_store_dwordx4 v[118:119], v[110:113], off nt
	global_store_dwordx4 v[118:119], v[106:109], off offset:16 nt
	s_nop 0
	v_or_b32_e32 v110, 32, v152
	v_ashrrev_i32_e32 v111, 31, v110
	v_lshlrev_b64 v[110:111], 11, v[110:111]
	v_lshl_add_u64 v[110:111], v[110:111], 0, v[150:151]
	v_lshl_add_u64 v[112:113], v[110:111], 1, s[50:51]
	s_nop 1
	v_pk_mov_b32 v[106:107], v[186:187], v[186:187] op_sel:[0,1]
	v_pk_mov_b32 v[108:109], v[188:189], v[188:189] op_sel:[0,1]
	v_lshl_add_u64 v[222:223], v[240:241], 0, v[222:223]
	global_load_dwordx4 v[182:185], v[222:223], off
	global_load_dwordx4 v[186:189], v[222:223], off offset:256
	v_lshlrev_b32_e32 v114, 16, v106
	v_and_b32_e32 v115, 0xffff0000, v106
	v_lshlrev_b32_e32 v106, 16, v107
	v_and_b32_e32 v107, 0xffff0000, v107
	v_lshlrev_b32_e32 v116, 16, v108
	v_and_b32_e32 v117, 0xffff0000, v108
	v_lshlrev_b32_e32 v108, 16, v109
	v_and_b32_e32 v109, 0xffff0000, v109
	v_pk_add_f32 v[104:105], v[104:105], v[106:107]
	v_pk_add_f32 v[102:103], v[102:103], v[114:115]
	v_pk_add_f32 v[100:101], v[100:101], v[108:109]
	v_pk_add_f32 v[98:99], v[98:99], v[116:117]
	global_store_dwordx4 v[118:119], v[102:105], off offset:512 nt
	global_store_dwordx4 v[118:119], v[98:101], off offset:528 nt
	s_nop 0
	v_lshl_add_u64 v[102:103], v[110:111], 2, s[28:29]
	s_waitcnt vmcnt(18)
	s_nop 1
	v_pk_mov_b32 v[98:99], v[190:191], v[190:191] op_sel:[0,1]
	v_pk_mov_b32 v[100:101], v[192:193], v[192:193] op_sel:[0,1]
	v_lshlrev_b32_e32 v104, 16, v98
	v_and_b32_e32 v105, 0xffff0000, v98
	v_lshlrev_b32_e32 v98, 16, v99
	v_and_b32_e32 v99, 0xffff0000, v99
	v_lshlrev_b32_e32 v106, 16, v100
	v_and_b32_e32 v107, 0xffff0000, v100
	v_lshlrev_b32_e32 v100, 16, v101
	v_and_b32_e32 v101, 0xffff0000, v101
	v_pk_add_f32 v[96:97], v[96:97], v[98:99]
	v_pk_add_f32 v[94:95], v[94:95], v[104:105]
	v_pk_add_f32 v[92:93], v[92:93], v[100:101]
	v_pk_add_f32 v[90:91], v[90:91], v[106:107]
	global_store_dwordx4 v[102:103], v[94:97], off nt
	global_store_dwordx4 v[102:103], v[90:93], off offset:16 nt
	s_nop 0
	v_or_b32_e32 v94, 48, v152
	v_ashrrev_i32_e32 v95, 31, v94
	v_lshlrev_b64 v[94:95], 11, v[94:95]
	v_lshl_add_u64 v[94:95], v[94:95], 0, v[150:151]
	v_lshl_add_u64 v[96:97], v[94:95], 1, s[50:51]
	s_nop 1
	v_pk_mov_b32 v[90:91], v[194:195], v[194:195] op_sel:[0,1]
	v_pk_mov_b32 v[92:93], v[196:197], v[196:197] op_sel:[0,1]
	v_lshlrev_b32_e32 v98, 16, v90
	v_and_b32_e32 v99, 0xffff0000, v90
	v_lshlrev_b32_e32 v90, 16, v91
	v_and_b32_e32 v91, 0xffff0000, v91
	v_lshlrev_b32_e32 v100, 16, v92
	v_and_b32_e32 v101, 0xffff0000, v92
	v_lshlrev_b32_e32 v92, 16, v93
	v_and_b32_e32 v93, 0xffff0000, v93
	v_pk_add_f32 v[88:89], v[88:89], v[90:91]
	v_pk_add_f32 v[86:87], v[86:87], v[98:99]
	v_pk_add_f32 v[84:85], v[84:85], v[92:93]
	v_pk_add_f32 v[82:83], v[82:83], v[100:101]
	global_store_dwordx4 v[102:103], v[86:89], off offset:512 nt
	global_store_dwordx4 v[102:103], v[82:85], off offset:528 nt
	s_nop 0
	v_lshl_add_u64 v[86:87], v[94:95], 2, s[28:29]
	s_waitcnt vmcnt(20)
	s_nop 1
	v_pk_mov_b32 v[82:83], v[198:199], v[198:199] op_sel:[0,1]
	v_pk_mov_b32 v[84:85], v[200:201], v[200:201] op_sel:[0,1]
	v_lshlrev_b32_e32 v88, 16, v82
	v_and_b32_e32 v89, 0xffff0000, v82
	v_lshlrev_b32_e32 v82, 16, v83
	v_and_b32_e32 v83, 0xffff0000, v83
	v_lshlrev_b32_e32 v90, 16, v84
	v_and_b32_e32 v91, 0xffff0000, v84
	v_lshlrev_b32_e32 v84, 16, v85
	v_and_b32_e32 v85, 0xffff0000, v85
	v_pk_add_f32 v[80:81], v[80:81], v[82:83]
	v_pk_add_f32 v[78:79], v[78:79], v[88:89]
	v_pk_add_f32 v[76:77], v[76:77], v[84:85]
	v_pk_add_f32 v[74:75], v[74:75], v[90:91]
	global_store_dwordx4 v[86:87], v[78:81], off nt
	global_store_dwordx4 v[86:87], v[74:77], off offset:16 nt
	s_nop 0
	v_lshl_add_u64 v[78:79], v[148:149], 0, s[12:13]
	v_lshl_add_u64 v[80:81], v[78:79], 1, s[50:51]
	s_nop 1
	v_pk_mov_b32 v[74:75], v[202:203], v[202:203] op_sel:[0,1]
	v_pk_mov_b32 v[76:77], v[204:205], v[204:205] op_sel:[0,1]
	v_lshlrev_b32_e32 v82, 16, v74
	v_and_b32_e32 v83, 0xffff0000, v74
	v_lshlrev_b32_e32 v74, 16, v75
	v_and_b32_e32 v75, 0xffff0000, v75
	v_lshlrev_b32_e32 v84, 16, v76
	v_and_b32_e32 v85, 0xffff0000, v76
	v_lshlrev_b32_e32 v76, 16, v77
	v_and_b32_e32 v77, 0xffff0000, v77
	v_pk_add_f32 v[72:73], v[72:73], v[74:75]
	v_pk_add_f32 v[70:71], v[70:71], v[82:83]
	v_pk_add_f32 v[68:69], v[68:69], v[76:77]
	v_pk_add_f32 v[66:67], v[66:67], v[84:85]
	global_store_dwordx4 v[86:87], v[70:73], off offset:512 nt
	global_store_dwordx4 v[86:87], v[66:69], off offset:528 nt
	s_nop 0
	v_lshl_add_u64 v[70:71], v[78:79], 2, s[28:29]
	s_waitcnt vmcnt(22)
	s_nop 1
	v_pk_mov_b32 v[66:67], v[206:207], v[206:207] op_sel:[0,1]
	v_pk_mov_b32 v[68:69], v[208:209], v[208:209] op_sel:[0,1]
	v_lshlrev_b32_e32 v72, 16, v66
	v_and_b32_e32 v73, 0xffff0000, v66
	v_lshlrev_b32_e32 v66, 16, v67
	v_and_b32_e32 v67, 0xffff0000, v67
	v_lshlrev_b32_e32 v74, 16, v68
	v_and_b32_e32 v75, 0xffff0000, v68
	v_lshlrev_b32_e32 v68, 16, v69
	v_and_b32_e32 v69, 0xffff0000, v69
	v_pk_add_f32 v[64:65], v[64:65], v[66:67]
	v_pk_add_f32 v[62:63], v[62:63], v[72:73]
	v_pk_add_f32 v[60:61], v[60:61], v[68:69]
	v_pk_add_f32 v[58:59], v[58:59], v[74:75]
	global_store_dwordx4 v[70:71], v[62:65], off nt
	global_store_dwordx4 v[70:71], v[58:61], off offset:16 nt
	s_nop 0
	v_lshl_add_u64 v[62:63], v[148:149], 0, s[14:15]
	v_lshl_add_u64 v[64:65], v[62:63], 1, s[50:51]
	s_nop 1
	v_pk_mov_b32 v[58:59], v[210:211], v[210:211] op_sel:[0,1]
	v_pk_mov_b32 v[60:61], v[212:213], v[212:213] op_sel:[0,1]
	v_lshlrev_b32_e32 v66, 16, v58
	v_and_b32_e32 v67, 0xffff0000, v58
	v_lshlrev_b32_e32 v58, 16, v59
	v_and_b32_e32 v59, 0xffff0000, v59
	v_lshlrev_b32_e32 v68, 16, v60
	v_and_b32_e32 v69, 0xffff0000, v60
	v_lshlrev_b32_e32 v60, 16, v61
	v_and_b32_e32 v61, 0xffff0000, v61
	v_pk_add_f32 v[56:57], v[56:57], v[58:59]
	v_pk_add_f32 v[54:55], v[54:55], v[66:67]
	v_pk_add_f32 v[52:53], v[52:53], v[60:61]
	v_pk_add_f32 v[50:51], v[50:51], v[68:69]
	global_store_dwordx4 v[70:71], v[54:57], off offset:512 nt
	global_store_dwordx4 v[70:71], v[50:53], off offset:528 nt
	s_nop 0
	v_lshl_add_u64 v[54:55], v[62:63], 2, s[28:29]
	s_waitcnt vmcnt(24)
	s_nop 1
	v_pk_mov_b32 v[50:51], v[214:215], v[214:215] op_sel:[0,1]
	v_pk_mov_b32 v[52:53], v[216:217], v[216:217] op_sel:[0,1]
	v_lshlrev_b32_e32 v56, 16, v50
	v_and_b32_e32 v57, 0xffff0000, v50
	v_lshlrev_b32_e32 v50, 16, v51
	v_and_b32_e32 v51, 0xffff0000, v51
	v_lshlrev_b32_e32 v58, 16, v52
	v_and_b32_e32 v59, 0xffff0000, v52
	v_lshlrev_b32_e32 v52, 16, v53
	v_and_b32_e32 v53, 0xffff0000, v53
	v_pk_add_f32 v[48:49], v[48:49], v[50:51]
	v_pk_add_f32 v[46:47], v[46:47], v[56:57]
	v_pk_add_f32 v[44:45], v[44:45], v[52:53]
	v_pk_add_f32 v[42:43], v[42:43], v[58:59]
	global_store_dwordx4 v[54:55], v[46:49], off nt
	global_store_dwordx4 v[54:55], v[42:45], off offset:16 nt
	s_nop 0
	v_lshl_add_u64 v[46:47], v[148:149], 0, s[16:17]
	v_lshl_add_u64 v[48:49], v[46:47], 1, s[50:51]
	s_nop 1
	v_pk_mov_b32 v[42:43], v[218:219], v[218:219] op_sel:[0,1]
	v_pk_mov_b32 v[44:45], v[220:221], v[220:221] op_sel:[0,1]
	v_lshlrev_b32_e32 v50, 16, v42
	v_and_b32_e32 v51, 0xffff0000, v42
	v_lshlrev_b32_e32 v42, 16, v43
	v_and_b32_e32 v43, 0xffff0000, v43
	v_lshlrev_b32_e32 v52, 16, v44
	v_and_b32_e32 v53, 0xffff0000, v44
	v_lshlrev_b32_e32 v44, 16, v45
	v_and_b32_e32 v45, 0xffff0000, v45
	v_pk_add_f32 v[40:41], v[40:41], v[42:43]
	v_pk_add_f32 v[38:39], v[38:39], v[50:51]
	v_pk_add_f32 v[36:37], v[36:37], v[44:45]
	v_pk_add_f32 v[34:35], v[34:35], v[52:53]
	global_store_dwordx4 v[54:55], v[38:41], off offset:512 nt
	global_store_dwordx4 v[54:55], v[34:37], off offset:528 nt
	s_nop 0
	v_lshl_add_u64 v[38:39], v[46:47], 2, s[28:29]
	s_waitcnt vmcnt(24)
	s_nop 1
	v_pk_mov_b32 v[34:35], v[174:175], v[174:175] op_sel:[0,1]
	v_pk_mov_b32 v[36:37], v[176:177], v[176:177] op_sel:[0,1]
	v_lshlrev_b32_e32 v40, 16, v34
	v_and_b32_e32 v41, 0xffff0000, v34
	v_lshlrev_b32_e32 v34, 16, v35
	v_and_b32_e32 v35, 0xffff0000, v35
	v_lshlrev_b32_e32 v42, 16, v36
	v_and_b32_e32 v43, 0xffff0000, v36
	v_lshlrev_b32_e32 v36, 16, v37
	v_and_b32_e32 v37, 0xffff0000, v37
	v_pk_add_f32 v[32:33], v[32:33], v[34:35]
	v_pk_add_f32 v[30:31], v[30:31], v[40:41]
	v_pk_add_f32 v[28:29], v[28:29], v[36:37]
	v_pk_add_f32 v[26:27], v[26:27], v[42:43]
	global_store_dwordx4 v[38:39], v[30:33], off nt
	global_store_dwordx4 v[38:39], v[26:29], off offset:16 nt
	s_nop 0
	v_lshl_add_u64 v[30:31], v[148:149], 0, s[18:19]
	v_lshl_add_u64 v[32:33], v[30:31], 1, s[50:51]
	s_nop 1
	v_pk_mov_b32 v[26:27], v[178:179], v[178:179] op_sel:[0,1]
	v_pk_mov_b32 v[28:29], v[180:181], v[180:181] op_sel:[0,1]
	v_lshlrev_b32_e32 v34, 16, v26
	v_and_b32_e32 v35, 0xffff0000, v26
	v_lshlrev_b32_e32 v26, 16, v27
	v_and_b32_e32 v27, 0xffff0000, v27
	v_lshlrev_b32_e32 v36, 16, v28
	v_and_b32_e32 v37, 0xffff0000, v28
	v_lshlrev_b32_e32 v28, 16, v29
	v_and_b32_e32 v29, 0xffff0000, v29
	v_pk_add_f32 v[24:25], v[24:25], v[26:27]
	v_pk_add_f32 v[22:23], v[22:23], v[34:35]
	v_pk_add_f32 v[20:21], v[20:21], v[28:29]
	v_pk_add_f32 v[18:19], v[18:19], v[36:37]
	global_store_dwordx4 v[38:39], v[22:25], off offset:512 nt
	global_store_dwordx4 v[38:39], v[18:21], off offset:528 nt
	s_nop 0
	v_lshl_add_u64 v[22:23], v[30:31], 2, s[28:29]
	s_waitcnt vmcnt(22)
	s_nop 1
	v_pk_mov_b32 v[18:19], v[182:183], v[182:183] op_sel:[0,1]
	v_pk_mov_b32 v[20:21], v[184:185], v[184:185] op_sel:[0,1]
	v_lshlrev_b32_e32 v24, 16, v18
	v_and_b32_e32 v25, 0xffff0000, v18
	v_lshlrev_b32_e32 v18, 16, v19
	v_and_b32_e32 v19, 0xffff0000, v19
	v_lshlrev_b32_e32 v26, 16, v20
	v_and_b32_e32 v27, 0xffff0000, v20
	v_lshlrev_b32_e32 v20, 16, v21
	v_and_b32_e32 v21, 0xffff0000, v21
	v_pk_add_f32 v[16:17], v[16:17], v[18:19]
	v_pk_add_f32 v[14:15], v[14:15], v[24:25]
	v_pk_add_f32 v[12:13], v[12:13], v[20:21]
	v_pk_add_f32 v[10:11], v[10:11], v[26:27]
	global_store_dwordx4 v[22:23], v[14:17], off nt
	global_store_dwordx4 v[22:23], v[10:13], off offset:16 nt
	s_nop 0
	s_nop 1
	v_pk_mov_b32 v[10:11], v[186:187], v[186:187] op_sel:[0,1]
	v_pk_mov_b32 v[12:13], v[188:189], v[188:189] op_sel:[0,1]
	v_lshlrev_b32_e32 v14, 16, v10
	v_and_b32_e32 v15, 0xffff0000, v10
	v_lshlrev_b32_e32 v10, 16, v11
	v_and_b32_e32 v11, 0xffff0000, v11
	v_lshlrev_b32_e32 v16, 16, v12
	v_and_b32_e32 v17, 0xffff0000, v12
	v_lshlrev_b32_e32 v12, 16, v13
	v_and_b32_e32 v13, 0xffff0000, v13
	v_pk_add_f32 v[8:9], v[8:9], v[10:11]
	v_pk_add_f32 v[6:7], v[6:7], v[14:15]
	v_pk_add_f32 v[4:5], v[4:5], v[12:13]
	v_pk_add_f32 v[2:3], v[2:3], v[16:17]
	global_store_dwordx4 v[22:23], v[6:9], off offset:512 nt
	global_store_dwordx4 v[22:23], v[2:5], off offset:528 nt
	s_cbranch_vccnz .LBB0_840
	s_andn2_b64 vcc, exec, s[6:7]
	s_cbranch_vccnz .LBB0_839
	s_barrier
	s_branch .LBB0_839

.LBB0_1087:
	v_pk_mul_f32 v[164:165], v[126:127], s[12:13] op_sel_hi:[1,0]
	v_pk_mul_f32 v[168:169], v[122:123], s[12:13] op_sel_hi:[1,0]
	v_exp_f32_e32 v164, v164
	v_exp_f32_e32 v165, v165
	v_exp_f32_e32 v168, v168
	v_exp_f32_e32 v169, v169
	v_pk_mul_f32 v[160:161], v[128:129], s[12:13] op_sel_hi:[1,0]
	v_pk_mul_f32 v[166:167], v[124:125], s[12:13] op_sel_hi:[1,0]
	v_pk_fma_f32 v[164:165], v[164:165], s[14:15], s[14:15] op_sel_hi:[1,0,0]
	v_exp_f32_e32 v160, v160
	v_exp_f32_e32 v161, v161
	v_exp_f32_e32 v166, v166
	v_exp_f32_e32 v167, v167
	v_rcp_f32_e32 v164, v164
	v_rcp_f32_e32 v165, v165
	v_pk_fma_f32 v[168:169], v[168:169], s[14:15], s[14:15] op_sel_hi:[1,0,0]
	v_pk_mul_f32 v[118:119], v[126:127], v[118:119]
	v_rcp_f32_e32 v168, v168
	v_rcp_f32_e32 v169, v169
	v_pk_fma_f32 v[160:161], v[160:161], s[14:15], s[14:15] op_sel_hi:[1,0,0]
	v_pk_fma_f32 v[166:167], v[166:167], s[14:15], s[14:15] op_sel_hi:[1,0,0]
	v_pk_mul_f32 v[118:119], v[118:119], v[164:165]
	v_pk_mul_f32 v[114:115], v[122:123], v[114:115]
	v_rcp_f32_e32 v160, v160
	v_rcp_f32_e32 v161, v161
	v_rcp_f32_e32 v166, v166
	v_rcp_f32_e32 v167, v167
	v_pk_mul_f32 v[114:115], v[114:115], v[168:169]
	v_med3_f32 v122, v118, s56, v157
	v_med3_f32 v119, v119, s56, v157
	v_mov_b32_e32 v118, 0
	v_cvt_pk_fp8_f32 v118, v122, v119
	v_med3_f32 v114, v114, s56, v157
	v_med3_f32 v115, v115, s56, v157
	v_mov_b32_e32 v119, 0
	v_cvt_pk_fp8_f32 v119, v114, v115
	v_pk_mul_f32 v[120:121], v[128:129], v[120:121]
	v_pk_mul_f32 v[116:117], v[124:125], v[116:117]
	v_pk_mul_f32 v[120:121], v[120:121], v[160:161]
	v_pk_mul_f32 v[116:117], v[116:117], v[166:167]
	v_med3_f32 v120, v120, s56, v157
	v_med3_f32 v121, v121, s56, v157
	v_med3_f32 v114, v116, s56, v157
	v_med3_f32 v115, v117, s56, v157
	v_pk_mul_f32 v[116:117], v[110:111], s[12:13] op_sel_hi:[1,0]
	v_cvt_pk_fp8_f32 v118, v120, v121 op_sel:[0,0,1]
	v_cvt_pk_fp8_f32 v119, v114, v115 op_sel:[0,0,1]
	v_exp_f32_e32 v116, v116
	v_exp_f32_e32 v117, v117
	v_pk_mul_f32 v[120:121], v[106:107], s[12:13] op_sel_hi:[1,0]
	v_lshl_add_u32 v158, s24, 8, v1
	v_lshl_or_b32 v148, s58, 7, v147
	v_mov_b64_e32 v[150:151], s[6:7]
	v_exp_f32_e32 v120, v120
	v_exp_f32_e32 v121, v121
	v_ashrrev_i32_e32 v149, 31, v148
	v_mad_i64_i32 v[114:115], s[26:27], v158, s55, v[150:151]
	v_lshl_add_u64 v[114:115], v[114:115], 0, v[148:149]
	global_store_dwordx2 v[114:115], v[118:119], off nt
	v_pk_mul_f32 v[114:115], v[112:113], s[12:13] op_sel_hi:[1,0]
	v_pk_mul_f32 v[118:119], v[108:109], s[12:13] op_sel_hi:[1,0]
	v_pk_fma_f32 v[116:117], v[116:117], s[14:15], s[14:15] op_sel_hi:[1,0,0]
	v_exp_f32_e32 v114, v114
	v_exp_f32_e32 v115, v115
	v_exp_f32_e32 v118, v118
	v_exp_f32_e32 v119, v119
	v_rcp_f32_e32 v116, v116
	v_rcp_f32_e32 v117, v117
	v_pk_fma_f32 v[120:121], v[120:121], s[14:15], s[14:15] op_sel_hi:[1,0,0]
	v_pk_mul_f32 v[102:103], v[110:111], v[102:103]
	v_rcp_f32_e32 v120, v120
	v_rcp_f32_e32 v121, v121
	v_pk_fma_f32 v[114:115], v[114:115], s[14:15], s[14:15] op_sel_hi:[1,0,0]
	v_pk_fma_f32 v[118:119], v[118:119], s[14:15], s[14:15] op_sel_hi:[1,0,0]
	v_pk_mul_f32 v[102:103], v[102:103], v[116:117]
	v_pk_mul_f32 v[98:99], v[106:107], v[98:99]
	v_rcp_f32_e32 v114, v114
	v_rcp_f32_e32 v115, v115
	v_rcp_f32_e32 v118, v118
	v_rcp_f32_e32 v119, v119
	v_pk_mul_f32 v[98:99], v[98:99], v[120:121]
	v_med3_f32 v106, v102, s56, v157
	v_med3_f32 v103, v103, s56, v157
	v_mov_b32_e32 v102, 0
	v_cvt_pk_fp8_f32 v102, v106, v103
	v_med3_f32 v98, v98, s56, v157
	v_med3_f32 v99, v99, s56, v157
	v_mov_b32_e32 v103, 0
	v_cvt_pk_fp8_f32 v103, v98, v99
	v_pk_mul_f32 v[104:105], v[112:113], v[104:105]
	v_pk_mul_f32 v[100:101], v[108:109], v[100:101]
	v_pk_mul_f32 v[104:105], v[104:105], v[114:115]
	v_pk_mul_f32 v[100:101], v[100:101], v[118:119]
	v_med3_f32 v104, v104, s56, v157
	v_med3_f32 v105, v105, s56, v157
	v_med3_f32 v98, v100, s56, v157
	v_med3_f32 v99, v101, s56, v157
	v_pk_mul_f32 v[100:101], v[94:95], s[12:13] op_sel_hi:[1,0]
	v_cvt_pk_fp8_f32 v102, v104, v105 op_sel:[0,0,1]
	v_cvt_pk_fp8_f32 v103, v98, v99 op_sel:[0,0,1]
	v_exp_f32_e32 v100, v100
	v_exp_f32_e32 v101, v101
	v_pk_mul_f32 v[104:105], v[90:91], s[12:13] op_sel_hi:[1,0]
	v_or_b32_e32 v122, 16, v158
	v_exp_f32_e32 v104, v104
	v_exp_f32_e32 v105, v105
	v_mad_i64_i32 v[98:99], s[26:27], v122, s55, v[150:151]
	v_lshl_add_u64 v[98:99], v[98:99], 0, v[148:149]
	global_store_dwordx2 v[98:99], v[102:103], off nt
	v_pk_mul_f32 v[98:99], v[96:97], s[12:13] op_sel_hi:[1,0]
	v_pk_mul_f32 v[102:103], v[92:93], s[12:13] op_sel_hi:[1,0]
	v_pk_fma_f32 v[100:101], v[100:101], s[14:15], s[14:15] op_sel_hi:[1,0,0]
	v_exp_f32_e32 v98, v98
	v_exp_f32_e32 v99, v99
	v_exp_f32_e32 v102, v102
	v_exp_f32_e32 v103, v103
	v_rcp_f32_e32 v100, v100
	v_rcp_f32_e32 v101, v101
	v_pk_fma_f32 v[104:105], v[104:105], s[14:15], s[14:15] op_sel_hi:[1,0,0]
	v_pk_mul_f32 v[86:87], v[94:95], v[86:87]
	v_rcp_f32_e32 v104, v104
	v_rcp_f32_e32 v105, v105
	v_pk_fma_f32 v[98:99], v[98:99], s[14:15], s[14:15] op_sel_hi:[1,0,0]
	v_pk_fma_f32 v[102:103], v[102:103], s[14:15], s[14:15] op_sel_hi:[1,0,0]
	v_pk_mul_f32 v[86:87], v[86:87], v[100:101]
	v_pk_mul_f32 v[82:83], v[90:91], v[82:83]
	v_rcp_f32_e32 v98, v98
	v_rcp_f32_e32 v99, v99
	v_rcp_f32_e32 v102, v102
	v_rcp_f32_e32 v103, v103
	v_pk_mul_f32 v[82:83], v[82:83], v[104:105]
	v_med3_f32 v90, v86, s56, v157
	v_med3_f32 v87, v87, s56, v157
	v_mov_b32_e32 v86, 0
	v_cvt_pk_fp8_f32 v86, v90, v87
	v_med3_f32 v82, v82, s56, v157
	v_med3_f32 v83, v83, s56, v157
	v_mov_b32_e32 v87, 0
	v_cvt_pk_fp8_f32 v87, v82, v83
	v_pk_mul_f32 v[88:89], v[96:97], v[88:89]
	v_pk_mul_f32 v[84:85], v[92:93], v[84:85]
	v_pk_mul_f32 v[88:89], v[88:89], v[98:99]
	v_pk_mul_f32 v[84:85], v[84:85], v[102:103]
	v_med3_f32 v88, v88, s56, v157
	v_med3_f32 v89, v89, s56, v157
	v_med3_f32 v82, v84, s56, v157
	v_med3_f32 v83, v85, s56, v157
	v_pk_mul_f32 v[84:85], v[78:79], s[12:13] op_sel_hi:[1,0]
	v_cvt_pk_fp8_f32 v86, v88, v89 op_sel:[0,0,1]
	v_cvt_pk_fp8_f32 v87, v82, v83 op_sel:[0,0,1]
	v_exp_f32_e32 v84, v84
	v_exp_f32_e32 v85, v85
	v_pk_mul_f32 v[88:89], v[74:75], s[12:13] op_sel_hi:[1,0]
	v_or_b32_e32 v106, 32, v158
	v_exp_f32_e32 v88, v88
	v_exp_f32_e32 v89, v89
	v_mad_i64_i32 v[82:83], s[26:27], v106, s55, v[150:151]
	v_lshl_add_u64 v[82:83], v[82:83], 0, v[148:149]
	global_store_dwordx2 v[82:83], v[86:87], off nt
	v_pk_mul_f32 v[82:83], v[80:81], s[12:13] op_sel_hi:[1,0]
	v_pk_mul_f32 v[86:87], v[76:77], s[12:13] op_sel_hi:[1,0]
	v_pk_fma_f32 v[84:85], v[84:85], s[14:15], s[14:15] op_sel_hi:[1,0,0]
	v_exp_f32_e32 v82, v82
	v_exp_f32_e32 v83, v83
	v_exp_f32_e32 v86, v86
	v_exp_f32_e32 v87, v87
	v_rcp_f32_e32 v84, v84
	v_rcp_f32_e32 v85, v85
	v_pk_fma_f32 v[88:89], v[88:89], s[14:15], s[14:15] op_sel_hi:[1,0,0]
	v_pk_mul_f32 v[70:71], v[78:79], v[70:71]
	v_rcp_f32_e32 v88, v88
	v_rcp_f32_e32 v89, v89
	v_pk_fma_f32 v[82:83], v[82:83], s[14:15], s[14:15] op_sel_hi:[1,0,0]
	v_pk_fma_f32 v[86:87], v[86:87], s[14:15], s[14:15] op_sel_hi:[1,0,0]
	v_pk_mul_f32 v[70:71], v[70:71], v[84:85]
	v_pk_mul_f32 v[66:67], v[74:75], v[66:67]
	v_rcp_f32_e32 v82, v82
	v_rcp_f32_e32 v83, v83
	v_rcp_f32_e32 v86, v86
	v_rcp_f32_e32 v87, v87
	v_pk_mul_f32 v[66:67], v[66:67], v[88:89]
	v_med3_f32 v74, v70, s56, v157
	v_med3_f32 v71, v71, s56, v157
	v_mov_b32_e32 v70, 0
	v_cvt_pk_fp8_f32 v70, v74, v71
	v_med3_f32 v66, v66, s56, v157
	v_med3_f32 v67, v67, s56, v157
	v_mov_b32_e32 v71, 0
	v_cvt_pk_fp8_f32 v71, v66, v67
	v_pk_mul_f32 v[72:73], v[80:81], v[72:73]
	v_pk_mul_f32 v[68:69], v[76:77], v[68:69]
	v_pk_mul_f32 v[72:73], v[72:73], v[82:83]
	v_pk_mul_f32 v[68:69], v[68:69], v[86:87]
	v_med3_f32 v72, v72, s56, v157
	v_med3_f32 v73, v73, s56, v157
	v_med3_f32 v66, v68, s56, v157
	v_med3_f32 v67, v69, s56, v157
	v_pk_mul_f32 v[68:69], v[62:63], s[12:13] op_sel_hi:[1,0]
	v_cvt_pk_fp8_f32 v70, v72, v73 op_sel:[0,0,1]
	v_cvt_pk_fp8_f32 v71, v66, v67 op_sel:[0,0,1]
	v_exp_f32_e32 v68, v68
	v_exp_f32_e32 v69, v69
	v_pk_mul_f32 v[72:73], v[58:59], s[12:13] op_sel_hi:[1,0]
	v_or_b32_e32 v90, 48, v158
	v_exp_f32_e32 v72, v72
	v_exp_f32_e32 v73, v73
	v_mad_i64_i32 v[66:67], s[26:27], v90, s55, v[150:151]
	v_lshl_add_u64 v[66:67], v[66:67], 0, v[148:149]
	global_store_dwordx2 v[66:67], v[70:71], off nt
	v_pk_mul_f32 v[66:67], v[64:65], s[12:13] op_sel_hi:[1,0]
	v_pk_mul_f32 v[70:71], v[60:61], s[12:13] op_sel_hi:[1,0]
	v_pk_fma_f32 v[68:69], v[68:69], s[14:15], s[14:15] op_sel_hi:[1,0,0]
	v_exp_f32_e32 v66, v66
	v_exp_f32_e32 v67, v67
	v_exp_f32_e32 v70, v70
	v_exp_f32_e32 v71, v71
	v_rcp_f32_e32 v68, v68
	v_rcp_f32_e32 v69, v69
	v_pk_fma_f32 v[72:73], v[72:73], s[14:15], s[14:15] op_sel_hi:[1,0,0]
	v_pk_mul_f32 v[54:55], v[62:63], v[54:55]
	v_rcp_f32_e32 v72, v72
	v_rcp_f32_e32 v73, v73
	v_pk_fma_f32 v[66:67], v[66:67], s[14:15], s[14:15] op_sel_hi:[1,0,0]
	v_pk_fma_f32 v[70:71], v[70:71], s[14:15], s[14:15] op_sel_hi:[1,0,0]
	v_pk_mul_f32 v[54:55], v[54:55], v[68:69]
	v_pk_mul_f32 v[50:51], v[58:59], v[50:51]
	v_rcp_f32_e32 v66, v66
	v_rcp_f32_e32 v67, v67
	v_rcp_f32_e32 v70, v70
	v_rcp_f32_e32 v71, v71
	v_pk_mul_f32 v[50:51], v[50:51], v[72:73]
	v_med3_f32 v58, v54, s56, v157
	v_med3_f32 v55, v55, s56, v157
	v_mov_b32_e32 v54, 0
	v_cvt_pk_fp8_f32 v54, v58, v55
	v_med3_f32 v50, v50, s56, v157
	v_med3_f32 v51, v51, s56, v157
	v_mov_b32_e32 v55, 0
	v_cvt_pk_fp8_f32 v55, v50, v51
	v_pk_mul_f32 v[56:57], v[64:65], v[56:57]
	v_pk_mul_f32 v[52:53], v[60:61], v[52:53]
	v_pk_mul_f32 v[56:57], v[56:57], v[66:67]
	v_pk_mul_f32 v[52:53], v[52:53], v[70:71]
	v_med3_f32 v56, v56, s56, v157
	v_med3_f32 v57, v57, s56, v157
	v_med3_f32 v50, v52, s56, v157
	v_med3_f32 v51, v53, s56, v157
	v_pk_mul_f32 v[52:53], v[46:47], s[12:13] op_sel_hi:[1,0]
	v_cvt_pk_fp8_f32 v54, v56, v57 op_sel:[0,0,1]
	v_cvt_pk_fp8_f32 v55, v50, v51 op_sel:[0,0,1]
	v_exp_f32_e32 v52, v52
	v_exp_f32_e32 v53, v53
	v_pk_mul_f32 v[56:57], v[42:43], s[12:13] op_sel_hi:[1,0]
	v_add_u32_e32 v74, 0x80, v158
	v_exp_f32_e32 v56, v56
	v_exp_f32_e32 v57, v57
	v_mad_i64_i32 v[50:51], s[26:27], v74, s55, v[150:151]
	v_lshl_add_u64 v[50:51], v[50:51], 0, v[148:149]
	global_store_dwordx2 v[50:51], v[54:55], off nt
	v_pk_mul_f32 v[50:51], v[48:49], s[12:13] op_sel_hi:[1,0]
	v_pk_mul_f32 v[54:55], v[44:45], s[12:13] op_sel_hi:[1,0]
	v_pk_fma_f32 v[52:53], v[52:53], s[14:15], s[14:15] op_sel_hi:[1,0,0]
	v_exp_f32_e32 v50, v50
	v_exp_f32_e32 v51, v51
	v_exp_f32_e32 v54, v54
	v_exp_f32_e32 v55, v55
	v_rcp_f32_e32 v52, v52
	v_rcp_f32_e32 v53, v53
	v_pk_fma_f32 v[56:57], v[56:57], s[14:15], s[14:15] op_sel_hi:[1,0,0]
	v_pk_mul_f32 v[38:39], v[46:47], v[38:39]
	v_rcp_f32_e32 v56, v56
	v_rcp_f32_e32 v57, v57
	v_pk_fma_f32 v[50:51], v[50:51], s[14:15], s[14:15] op_sel_hi:[1,0,0]
	v_pk_fma_f32 v[54:55], v[54:55], s[14:15], s[14:15] op_sel_hi:[1,0,0]
	v_pk_mul_f32 v[38:39], v[38:39], v[52:53]
	v_pk_mul_f32 v[34:35], v[42:43], v[34:35]
	v_rcp_f32_e32 v50, v50
	v_rcp_f32_e32 v51, v51
	v_rcp_f32_e32 v54, v54
	v_rcp_f32_e32 v55, v55
	v_pk_mul_f32 v[34:35], v[34:35], v[56:57]
	v_med3_f32 v42, v38, s56, v157
	v_med3_f32 v39, v39, s56, v157
	v_mov_b32_e32 v38, 0
	v_cvt_pk_fp8_f32 v38, v42, v39
	v_med3_f32 v34, v34, s56, v157
	v_med3_f32 v35, v35, s56, v157
	v_mov_b32_e32 v39, 0
	v_cvt_pk_fp8_f32 v39, v34, v35
	v_pk_mul_f32 v[40:41], v[48:49], v[40:41]
	v_pk_mul_f32 v[36:37], v[44:45], v[36:37]
	v_pk_mul_f32 v[40:41], v[40:41], v[50:51]
	v_pk_mul_f32 v[36:37], v[36:37], v[54:55]
	v_med3_f32 v40, v40, s56, v157
	v_med3_f32 v41, v41, s56, v157
	v_med3_f32 v34, v36, s56, v157
	v_med3_f32 v35, v37, s56, v157
	v_pk_mul_f32 v[36:37], v[30:31], s[12:13] op_sel_hi:[1,0]
	v_cvt_pk_fp8_f32 v38, v40, v41 op_sel:[0,0,1]
	v_cvt_pk_fp8_f32 v39, v34, v35 op_sel:[0,0,1]
	v_exp_f32_e32 v36, v36
	v_exp_f32_e32 v37, v37
	v_pk_mul_f32 v[40:41], v[26:27], s[12:13] op_sel_hi:[1,0]
	v_add_u32_e32 v58, 0x90, v158
	v_exp_f32_e32 v40, v40
	v_exp_f32_e32 v41, v41
	v_mad_i64_i32 v[34:35], s[26:27], v58, s55, v[150:151]
	v_lshl_add_u64 v[34:35], v[34:35], 0, v[148:149]
	global_store_dwordx2 v[34:35], v[38:39], off nt
	v_pk_mul_f32 v[34:35], v[32:33], s[12:13] op_sel_hi:[1,0]
	v_pk_mul_f32 v[38:39], v[28:29], s[12:13] op_sel_hi:[1,0]
	v_pk_fma_f32 v[36:37], v[36:37], s[14:15], s[14:15] op_sel_hi:[1,0,0]
	v_exp_f32_e32 v34, v34
	v_exp_f32_e32 v35, v35
	v_exp_f32_e32 v38, v38
	v_exp_f32_e32 v39, v39
	v_rcp_f32_e32 v36, v36
	v_rcp_f32_e32 v37, v37
	v_pk_fma_f32 v[40:41], v[40:41], s[14:15], s[14:15] op_sel_hi:[1,0,0]
	v_pk_mul_f32 v[22:23], v[30:31], v[22:23]
	v_rcp_f32_e32 v40, v40
	v_rcp_f32_e32 v41, v41
	v_pk_fma_f32 v[34:35], v[34:35], s[14:15], s[14:15] op_sel_hi:[1,0,0]
	v_pk_fma_f32 v[38:39], v[38:39], s[14:15], s[14:15] op_sel_hi:[1,0,0]
	v_pk_mul_f32 v[22:23], v[22:23], v[36:37]
	v_pk_mul_f32 v[18:19], v[26:27], v[18:19]
	v_rcp_f32_e32 v34, v34
	v_rcp_f32_e32 v35, v35
	v_rcp_f32_e32 v38, v38
	v_rcp_f32_e32 v39, v39
	v_pk_mul_f32 v[18:19], v[18:19], v[40:41]
	v_med3_f32 v26, v22, s56, v157
	v_med3_f32 v23, v23, s56, v157
	v_mov_b32_e32 v22, 0
	v_cvt_pk_fp8_f32 v22, v26, v23
	v_med3_f32 v18, v18, s56, v157
	v_med3_f32 v19, v19, s56, v157
	v_mov_b32_e32 v23, 0
	v_cvt_pk_fp8_f32 v23, v18, v19
	v_pk_mul_f32 v[24:25], v[32:33], v[24:25]
	v_pk_mul_f32 v[20:21], v[28:29], v[20:21]
	v_pk_mul_f32 v[24:25], v[24:25], v[34:35]
	v_pk_mul_f32 v[20:21], v[20:21], v[38:39]
	v_med3_f32 v24, v24, s56, v157
	v_med3_f32 v25, v25, s56, v157
	v_med3_f32 v18, v20, s56, v157
	v_med3_f32 v19, v21, s56, v157
	v_pk_mul_f32 v[20:21], v[14:15], s[12:13] op_sel_hi:[1,0]
	v_cvt_pk_fp8_f32 v22, v24, v25 op_sel:[0,0,1]
	v_cvt_pk_fp8_f32 v23, v18, v19 op_sel:[0,0,1]
	v_exp_f32_e32 v20, v20
	v_exp_f32_e32 v21, v21
	v_pk_mul_f32 v[24:25], v[10:11], s[12:13] op_sel_hi:[1,0]
	v_add_u32_e32 v42, 0xa0, v158
	v_exp_f32_e32 v24, v24
	v_exp_f32_e32 v25, v25
	v_mad_i64_i32 v[18:19], s[26:27], v42, s55, v[150:151]
	v_lshl_add_u64 v[18:19], v[18:19], 0, v[148:149]
	global_store_dwordx2 v[18:19], v[22:23], off nt
	v_pk_mul_f32 v[18:19], v[16:17], s[12:13] op_sel_hi:[1,0]
	v_pk_mul_f32 v[22:23], v[12:13], s[12:13] op_sel_hi:[1,0]
	v_pk_fma_f32 v[20:21], v[20:21], s[14:15], s[14:15] op_sel_hi:[1,0,0]
	v_exp_f32_e32 v18, v18
	v_exp_f32_e32 v19, v19
	v_exp_f32_e32 v22, v22
	v_exp_f32_e32 v23, v23
	v_rcp_f32_e32 v20, v20
	v_rcp_f32_e32 v21, v21
	v_pk_fma_f32 v[24:25], v[24:25], s[14:15], s[14:15] op_sel_hi:[1,0,0]
	v_pk_mul_f32 v[6:7], v[14:15], v[6:7]
	v_rcp_f32_e32 v24, v24
	v_rcp_f32_e32 v25, v25
	v_pk_fma_f32 v[18:19], v[18:19], s[14:15], s[14:15] op_sel_hi:[1,0,0]
	v_pk_fma_f32 v[22:23], v[22:23], s[14:15], s[14:15] op_sel_hi:[1,0,0]
	v_pk_mul_f32 v[6:7], v[6:7], v[20:21]
	v_pk_mul_f32 v[2:3], v[10:11], v[2:3]
	v_rcp_f32_e32 v18, v18
	v_rcp_f32_e32 v19, v19
	v_rcp_f32_e32 v22, v22
	v_rcp_f32_e32 v23, v23
	v_pk_mul_f32 v[2:3], v[2:3], v[24:25]
	v_med3_f32 v10, v6, s56, v157
	v_med3_f32 v7, v7, s56, v157
	v_mov_b32_e32 v6, 0
	v_cvt_pk_fp8_f32 v6, v10, v7
	v_med3_f32 v2, v2, s56, v157
	v_med3_f32 v3, v3, s56, v157
	v_mov_b32_e32 v7, 0
	v_cvt_pk_fp8_f32 v7, v2, v3
	v_pk_mul_f32 v[8:9], v[16:17], v[8:9]
	v_pk_mul_f32 v[4:5], v[12:13], v[4:5]
	v_pk_mul_f32 v[8:9], v[8:9], v[18:19]
	v_pk_mul_f32 v[4:5], v[4:5], v[22:23]
	v_med3_f32 v8, v8, s56, v157
	v_med3_f32 v9, v9, s56, v157
	v_med3_f32 v2, v4, s56, v157
	v_med3_f32 v3, v5, s56, v157
	v_cvt_pk_fp8_f32 v6, v8, v9 op_sel:[0,0,1]
	v_cvt_pk_fp8_f32 v7, v2, v3 op_sel:[0,0,1]
	v_add_u32_e32 v26, 0xb0, v158
	v_mad_i64_i32 v[2:3], s[26:27], v26, s55, v[150:151]
	v_lshl_add_u64 v[2:3], v[2:3], 0, v[148:149]
	s_andn2_b64 vcc, exec, s[2:3]
	s_mov_b64 s[2:3], -1
	global_store_dwordx2 v[2:3], v[6:7], off nt
	s_cbranch_vccnz .LBB0_1078
	s_andn2_b64 vcc, exec, s[4:5]
	s_cbranch_vccnz .LBB0_1077
	s_barrier
	s_branch .LBB0_1077

.LBB0_1162:
	v_lshl_add_u32 v166, s0, 8, v157
	v_ashrrev_i32_e32 v167, 31, v166
	v_lshl_add_u64 v[144:145], v[166:167], 2, s[6:7]
	global_load_dword v168, v[144:145], off
	global_load_dword v178, v[144:145], off offset:64
	global_load_dword v179, v[144:145], off offset:128
	global_load_dword v180, v[144:145], off offset:192
	global_load_dword v181, v[144:145], off offset:512
	global_load_dword v182, v[144:145], off offset:576
	global_load_dword v183, v[144:145], off offset:640
	global_load_dword v184, v[144:145], off offset:704
	v_lshl_or_b32 v148, s67, 8, v159
	v_ashrrev_i32_e32 v149, 31, v148
	v_lshlrev_b64 v[172:173], 12, v[166:167]
	v_or_b32_e32 v170, 16, v166
	v_lshlrev_b64 v[174:175], 1, v[148:149]
	v_lshl_add_u64 v[148:149], s[12:13], 0, v[172:173]
	v_ashrrev_i32_e32 v171, 31, v170
	v_lshl_add_u64 v[148:149], v[148:149], 0, v[174:175]
	v_lshl_add_u64 v[172:173], v[170:171], 2, s[6:7]
	s_waitcnt vmcnt(7)
	v_pk_mul_f32 v[128:129], v[128:129], v[168:169] op_sel_hi:[1,0]
	v_pk_mul_f32 v[126:127], v[126:127], v[168:169] op_sel_hi:[1,0]
	v_pk_mul_f32 v[124:125], v[124:125], v[168:169] op_sel_hi:[1,0]
	v_pk_mul_f32 v[122:123], v[122:123], v[168:169] op_sel_hi:[1,0]
	v_pk_mul_f32 v[120:121], v[120:121], v[168:169] op_sel_hi:[1,0]
	v_pk_mul_f32 v[118:119], v[118:119], v[168:169] op_sel_hi:[1,0]
	v_pk_mul_f32 v[176:177], v[116:117], v[168:169] op_sel_hi:[1,0]
	v_pk_mul_f32 v[168:169], v[114:115], v[168:169] op_sel_hi:[1,0]
	v_cvt_pk_bf16_f32 v114, v126, v127
	v_cvt_pk_bf16_f32 v115, v128, v129
	v_cvt_pk_bf16_f32 v116, v122, v123
	v_cvt_pk_bf16_f32 v117, v124, v125
	global_store_dwordx4 v[148:149], v[114:117], off nt
	s_nop 1
	v_cvt_pk_bf16_f32 v114, v118, v119
	v_cvt_pk_bf16_f32 v115, v120, v121
	v_cvt_pk_bf16_f32 v116, v168, v169
	v_cvt_pk_bf16_f32 v117, v176, v177
	global_store_dwordx4 v[148:149], v[114:117], off offset:256 nt
	s_nop 0
	v_lshlrev_b64 v[118:119], 12, v[170:171]
	v_or_b32_e32 v116, 32, v166
	v_lshl_add_u64 v[118:119], s[12:13], 0, v[118:119]
	v_ashrrev_i32_e32 v117, 31, v116
	v_lshl_add_u64 v[118:119], v[118:119], 0, v[174:175]
	v_lshl_add_u64 v[120:121], v[116:117], 2, s[6:7]
	s_waitcnt vmcnt(8)
	v_mov_b32_e32 v114, v178
	v_pk_mul_f32 v[112:113], v[112:113], v[114:115] op_sel_hi:[1,0]
	v_pk_mul_f32 v[110:111], v[110:111], v[114:115] op_sel_hi:[1,0]
	v_pk_mul_f32 v[108:109], v[108:109], v[114:115] op_sel_hi:[1,0]
	v_pk_mul_f32 v[106:107], v[106:107], v[114:115] op_sel_hi:[1,0]
	v_pk_mul_f32 v[104:105], v[104:105], v[114:115] op_sel_hi:[1,0]
	v_pk_mul_f32 v[102:103], v[102:103], v[114:115] op_sel_hi:[1,0]
	v_pk_mul_f32 v[122:123], v[100:101], v[114:115] op_sel_hi:[1,0]
	v_pk_mul_f32 v[114:115], v[98:99], v[114:115] op_sel_hi:[1,0]
	v_cvt_pk_bf16_f32 v98, v110, v111
	v_cvt_pk_bf16_f32 v99, v112, v113
	v_cvt_pk_bf16_f32 v100, v106, v107
	v_cvt_pk_bf16_f32 v101, v108, v109
	global_store_dwordx4 v[118:119], v[98:101], off nt
	s_nop 1
	v_cvt_pk_bf16_f32 v98, v102, v103
	v_cvt_pk_bf16_f32 v99, v104, v105
	v_cvt_pk_bf16_f32 v100, v114, v115
	v_cvt_pk_bf16_f32 v101, v122, v123
	global_store_dwordx4 v[118:119], v[98:101], off offset:256 nt
	s_nop 0
	v_lshlrev_b64 v[102:103], 12, v[116:117]
	v_or_b32_e32 v100, 48, v166
	v_lshl_add_u64 v[102:103], s[12:13], 0, v[102:103]
	v_ashrrev_i32_e32 v101, 31, v100
	v_lshl_add_u64 v[102:103], v[102:103], 0, v[174:175]
	v_lshl_add_u64 v[104:105], v[100:101], 2, s[6:7]
	s_waitcnt vmcnt(9)
	v_mov_b32_e32 v98, v179
	v_pk_mul_f32 v[96:97], v[96:97], v[98:99] op_sel_hi:[1,0]
	v_pk_mul_f32 v[94:95], v[94:95], v[98:99] op_sel_hi:[1,0]
	v_pk_mul_f32 v[92:93], v[92:93], v[98:99] op_sel_hi:[1,0]
	v_pk_mul_f32 v[90:91], v[90:91], v[98:99] op_sel_hi:[1,0]
	v_pk_mul_f32 v[84:85], v[84:85], v[98:99] op_sel_hi:[1,0]
	v_pk_mul_f32 v[82:83], v[82:83], v[98:99] op_sel_hi:[1,0]
	v_pk_mul_f32 v[106:107], v[76:77], v[98:99] op_sel_hi:[1,0]
	v_pk_mul_f32 v[98:99], v[74:75], v[98:99] op_sel_hi:[1,0]
	v_cvt_pk_bf16_f32 v74, v94, v95
	v_cvt_pk_bf16_f32 v75, v96, v97
	v_cvt_pk_bf16_f32 v76, v90, v91
	v_cvt_pk_bf16_f32 v77, v92, v93
	global_store_dwordx4 v[102:103], v[74:77], off nt
	s_nop 1
	v_cvt_pk_bf16_f32 v74, v82, v83
	v_cvt_pk_bf16_f32 v75, v84, v85
	v_cvt_pk_bf16_f32 v76, v98, v99
	v_cvt_pk_bf16_f32 v77, v106, v107
	global_store_dwordx4 v[102:103], v[74:77], off offset:256 nt
	s_nop 0
	s_waitcnt vmcnt(10)
	v_mov_b32_e32 v74, v180
	v_pk_mul_f32 v[82:83], v[88:89], v[74:75] op_sel_hi:[1,0]
	v_lshlrev_b64 v[76:77], 12, v[100:101]
	v_lshl_add_u64 v[76:77], s[12:13], 0, v[76:77]
	v_lshl_add_u64 v[76:77], v[76:77], 0, v[174:175]
	v_pk_mul_f32 v[84:85], v[86:87], v[74:75] op_sel_hi:[1,0]
	v_pk_mul_f32 v[80:81], v[80:81], v[74:75] op_sel_hi:[1,0]
	v_pk_mul_f32 v[78:79], v[78:79], v[74:75] op_sel_hi:[1,0]
	v_pk_mul_f32 v[72:73], v[72:73], v[74:75] op_sel_hi:[1,0]
	v_pk_mul_f32 v[70:71], v[70:71], v[74:75] op_sel_hi:[1,0]
	v_pk_mul_f32 v[86:87], v[68:69], v[74:75] op_sel_hi:[1,0]
	v_pk_mul_f32 v[74:75], v[66:67], v[74:75] op_sel_hi:[1,0]
	v_cvt_pk_bf16_f32 v66, v84, v85
	v_cvt_pk_bf16_f32 v67, v82, v83
	v_cvt_pk_bf16_f32 v68, v78, v79
	v_cvt_pk_bf16_f32 v69, v80, v81
	global_store_dwordx4 v[76:77], v[66:69], off nt
	s_nop 1
	v_cvt_pk_bf16_f32 v66, v70, v71
	v_cvt_pk_bf16_f32 v67, v72, v73
	v_cvt_pk_bf16_f32 v68, v74, v75
	v_cvt_pk_bf16_f32 v69, v86, v87
	global_store_dwordx4 v[76:77], v[66:69], off offset:256 nt
	s_nop 0
	v_add_co_u32_e32 v70, vcc, s60, v148
	v_lshl_add_u64 v[68:69], v[148:149], 0, s[18:19]
	s_nop 0
	v_addc_co_u32_e32 v71, vcc, 0, v149, vcc
	s_waitcnt vmcnt(11)
	v_mov_b32_e32 v66, v181
	v_pk_mul_f32 v[64:65], v[64:65], v[66:67] op_sel_hi:[1,0]
	v_pk_mul_f32 v[62:63], v[62:63], v[66:67] op_sel_hi:[1,0]
	v_pk_mul_f32 v[60:61], v[60:61], v[66:67] op_sel_hi:[1,0]
	v_pk_mul_f32 v[58:59], v[58:59], v[66:67] op_sel_hi:[1,0]
	v_pk_mul_f32 v[56:57], v[56:57], v[66:67] op_sel_hi:[1,0]
	v_pk_mul_f32 v[54:55], v[54:55], v[66:67] op_sel_hi:[1,0]
	v_pk_mul_f32 v[72:73], v[52:53], v[66:67] op_sel_hi:[1,0]
	v_pk_mul_f32 v[66:67], v[50:51], v[66:67] op_sel_hi:[1,0]
	v_cvt_pk_bf16_f32 v50, v62, v63
	v_cvt_pk_bf16_f32 v51, v64, v65
	v_cvt_pk_bf16_f32 v52, v58, v59
	v_cvt_pk_bf16_f32 v53, v60, v61
	global_store_dwordx4 v[70:71], v[50:53], off nt
	s_nop 1
	v_cvt_pk_bf16_f32 v50, v54, v55
	v_cvt_pk_bf16_f32 v51, v56, v57
	v_cvt_pk_bf16_f32 v52, v66, v67
	v_cvt_pk_bf16_f32 v53, v72, v73
	global_store_dwordx4 v[68:69], v[50:53], off offset:256 nt
	s_nop 0
	v_add_co_u32_e32 v54, vcc, s61, v148
	v_lshl_add_u64 v[52:53], v[148:149], 0, s[20:21]
	s_nop 0
	v_addc_co_u32_e32 v55, vcc, 0, v149, vcc
	s_waitcnt vmcnt(12)
	v_mov_b32_e32 v50, v182
	v_pk_mul_f32 v[48:49], v[48:49], v[50:51] op_sel_hi:[1,0]
	v_pk_mul_f32 v[46:47], v[46:47], v[50:51] op_sel_hi:[1,0]
	v_pk_mul_f32 v[44:45], v[44:45], v[50:51] op_sel_hi:[1,0]
	v_pk_mul_f32 v[42:43], v[42:43], v[50:51] op_sel_hi:[1,0]
	v_pk_mul_f32 v[40:41], v[40:41], v[50:51] op_sel_hi:[1,0]
	v_pk_mul_f32 v[38:39], v[38:39], v[50:51] op_sel_hi:[1,0]
	v_pk_mul_f32 v[56:57], v[36:37], v[50:51] op_sel_hi:[1,0]
	v_pk_mul_f32 v[50:51], v[34:35], v[50:51] op_sel_hi:[1,0]
	v_cvt_pk_bf16_f32 v34, v46, v47
	v_cvt_pk_bf16_f32 v35, v48, v49
	v_cvt_pk_bf16_f32 v36, v42, v43
	v_cvt_pk_bf16_f32 v37, v44, v45
	global_store_dwordx4 v[54:55], v[34:37], off nt
	s_nop 1
	v_cvt_pk_bf16_f32 v34, v38, v39
	v_cvt_pk_bf16_f32 v35, v40, v41
	v_cvt_pk_bf16_f32 v36, v50, v51
	v_cvt_pk_bf16_f32 v37, v56, v57
	global_store_dwordx4 v[52:53], v[34:37], off offset:256 nt
	s_nop 0
	v_add_co_u32_e32 v38, vcc, s62, v148
	v_lshl_add_u64 v[36:37], v[148:149], 0, s[22:23]
	s_nop 0
	v_addc_co_u32_e32 v39, vcc, 0, v149, vcc
	s_and_b64 vcc, exec, s[2:3]
	s_waitcnt vmcnt(13)
	v_mov_b32_e32 v34, v183
	v_pk_mul_f32 v[32:33], v[32:33], v[34:35] op_sel_hi:[1,0]
	v_pk_mul_f32 v[30:31], v[30:31], v[34:35] op_sel_hi:[1,0]
	v_pk_mul_f32 v[28:29], v[28:29], v[34:35] op_sel_hi:[1,0]
	v_pk_mul_f32 v[26:27], v[26:27], v[34:35] op_sel_hi:[1,0]
	v_pk_mul_f32 v[24:25], v[24:25], v[34:35] op_sel_hi:[1,0]
	v_pk_mul_f32 v[22:23], v[22:23], v[34:35] op_sel_hi:[1,0]
	v_pk_mul_f32 v[40:41], v[20:21], v[34:35] op_sel_hi:[1,0]
	v_pk_mul_f32 v[34:35], v[18:19], v[34:35] op_sel_hi:[1,0]
	v_cvt_pk_bf16_f32 v18, v30, v31
	v_cvt_pk_bf16_f32 v19, v32, v33
	v_cvt_pk_bf16_f32 v20, v26, v27
	v_cvt_pk_bf16_f32 v21, v28, v29
	global_store_dwordx4 v[38:39], v[18:21], off nt
	s_nop 1
	v_cvt_pk_bf16_f32 v18, v22, v23
	v_cvt_pk_bf16_f32 v19, v24, v25
	v_cvt_pk_bf16_f32 v20, v34, v35
	v_cvt_pk_bf16_f32 v21, v40, v41
	global_store_dwordx4 v[36:37], v[18:21], off offset:256 nt
	s_nop 0
	v_add_co_u32_e64 v22, s[0:1], s63, v148
	v_lshl_add_u64 v[20:21], v[148:149], 0, s[24:25]
	s_nop 0
	v_addc_co_u32_e64 v23, s[0:1], 0, v149, s[0:1]
	s_mov_b64 s[0:1], -1
	s_waitcnt vmcnt(14)
	v_mov_b32_e32 v18, v184
	v_pk_mul_f32 v[16:17], v[16:17], v[18:19] op_sel_hi:[1,0]
	v_pk_mul_f32 v[14:15], v[14:15], v[18:19] op_sel_hi:[1,0]
	v_pk_mul_f32 v[12:13], v[12:13], v[18:19] op_sel_hi:[1,0]
	v_pk_mul_f32 v[10:11], v[10:11], v[18:19] op_sel_hi:[1,0]
	v_pk_mul_f32 v[8:9], v[8:9], v[18:19] op_sel_hi:[1,0]
	v_pk_mul_f32 v[6:7], v[6:7], v[18:19] op_sel_hi:[1,0]
	v_pk_mul_f32 v[24:25], v[4:5], v[18:19] op_sel_hi:[1,0]
	v_pk_mul_f32 v[18:19], v[2:3], v[18:19] op_sel_hi:[1,0]
	v_cvt_pk_bf16_f32 v2, v14, v15
	v_cvt_pk_bf16_f32 v3, v16, v17
	v_cvt_pk_bf16_f32 v4, v10, v11
	v_cvt_pk_bf16_f32 v5, v12, v13
	global_store_dwordx4 v[22:23], v[2:5], off nt
	s_nop 1
	v_cvt_pk_bf16_f32 v2, v6, v7
	v_cvt_pk_bf16_f32 v3, v8, v9
	v_cvt_pk_bf16_f32 v4, v18, v19
	v_cvt_pk_bf16_f32 v5, v24, v25
	global_store_dwordx4 v[20:21], v[2:5], off offset:256 nt
	s_cbranch_vccnz .LBB0_1151
	s_andn2_b64 vcc, exec, s[10:11]
	s_cbranch_vccnz .LBB0_1150
	s_barrier
	s_branch .LBB0_1150

.LBB0_1183:
	v_lshl_add_u32 v148, s20, 8, v147
	v_ashrrev_i32_e32 v149, 31, v148
	v_lshl_add_u64 v[140:141], v[148:149], 2, s[6:7]
	global_load_dword v158, v[140:141], off
	global_load_dword v178, v[140:141], off offset:64
	global_load_dword v179, v[140:141], off offset:128
	global_load_dword v180, v[140:141], off offset:192
	global_load_dword v181, v[140:141], off offset:512
	global_load_dword v182, v[140:141], off offset:576
	global_load_dword v183, v[140:141], off offset:640
	global_load_dword v184, v[140:141], off offset:704
	s_abs_i32 s22, s67
	s_mul_hi_u32 s23, s22, s61
	s_mul_i32 s24, s23, s59
	s_ashr_i32 s20, s67, 31
	s_sub_i32 s22, s22, s24
	s_xor_b32 s20, s20, s60
	s_add_i32 s25, s23, 1
	s_sub_i32 s24, s22, s59
	s_cmp_ge_u32 s22, s59
	s_cselect_b32 s23, s25, s23
	s_cselect_b32 s22, s24, s22
	s_add_i32 s24, s23, 1
	s_cmp_ge_u32 s22, s59
	s_cselect_b32 s22, s24, s23
	s_xor_b32 s22, s22, s20
	s_sub_i32 s20, s22, s20
	s_mul_hi_i32 s23, s53, s20
	s_mul_i32 s22, s53, s20
	s_lshl_b64 s[22:23], s[22:23], 1
	v_lshl_or_b32 v144, s66, 8, v151
	v_subrev_u32_e32 v142, s52, v148
	s_add_u32 s22, s50, s22
	v_ashrrev_i32_e32 v145, 31, v144
	v_ashrrev_i32_e32 v143, 31, v142
	s_addc_u32 s23, s51, s23
	v_or_b32_e32 v160, 16, v148
	v_lshlrev_b64 v[162:163], 12, v[142:143]
	v_lshl_add_u64 v[144:145], v[144:145], 1, s[22:23]
	v_ashrrev_i32_e32 v161, 31, v160
	v_lshl_add_u64 v[162:163], v[144:145], 0, v[162:163]
	v_lshl_add_u64 v[164:165], v[160:161], 2, s[6:7]
	s_and_b64 vcc, exec, s[2:3]
	s_mov_b64 s[2:3], -1
	s_waitcnt vmcnt(7)
	v_pk_mul_f32 v[122:123], v[122:123], v[158:159] op_sel_hi:[1,0]
	v_pk_mul_f32 v[120:121], v[120:121], v[158:159] op_sel_hi:[1,0]
	v_pk_mul_f32 v[126:127], v[126:127], v[158:159] op_sel_hi:[1,0]
	v_pk_mul_f32 v[124:125], v[124:125], v[158:159] op_sel_hi:[1,0]
	v_pk_mul_f32 v[118:119], v[118:119], v[158:159] op_sel_hi:[1,0]
	v_pk_mul_f32 v[116:117], v[116:117], v[158:159] op_sel_hi:[1,0]
	v_pk_mul_f32 v[166:167], v[114:115], v[158:159] op_sel_hi:[1,0]
	v_pk_mul_f32 v[158:159], v[112:113], v[158:159] op_sel_hi:[1,0]
	v_cvt_pk_bf16_f32 v112, v120, v121
	v_cvt_pk_bf16_f32 v113, v122, v123
	v_cvt_pk_bf16_f32 v114, v124, v125
	v_cvt_pk_bf16_f32 v115, v126, v127
	global_store_dwordx4 v[162:163], v[112:115], off nt
	s_nop 1
	v_cvt_pk_bf16_f32 v112, v116, v117
	v_cvt_pk_bf16_f32 v113, v118, v119
	v_cvt_pk_bf16_f32 v114, v158, v159
	v_cvt_pk_bf16_f32 v115, v166, v167
	global_store_dwordx4 v[162:163], v[112:115], off offset:256 nt
	s_nop 0
	v_subrev_u32_e32 v116, s52, v160
	v_ashrrev_i32_e32 v117, 31, v116
	v_or_b32_e32 v114, 32, v148
	v_lshlrev_b64 v[116:117], 12, v[116:117]
	v_ashrrev_i32_e32 v115, 31, v114
	v_lshl_add_u64 v[116:117], v[144:145], 0, v[116:117]
	v_lshl_add_u64 v[118:119], v[114:115], 2, s[6:7]
	s_waitcnt vmcnt(8)
	v_mov_b32_e32 v112, v178
	v_pk_mul_f32 v[110:111], v[110:111], v[112:113] op_sel_hi:[1,0]
	v_pk_mul_f32 v[108:109], v[108:109], v[112:113] op_sel_hi:[1,0]
	v_pk_mul_f32 v[106:107], v[106:107], v[112:113] op_sel_hi:[1,0]
	v_pk_mul_f32 v[104:105], v[104:105], v[112:113] op_sel_hi:[1,0]
	v_pk_mul_f32 v[102:103], v[102:103], v[112:113] op_sel_hi:[1,0]
	v_pk_mul_f32 v[100:101], v[100:101], v[112:113] op_sel_hi:[1,0]
	v_pk_mul_f32 v[120:121], v[98:99], v[112:113] op_sel_hi:[1,0]
	v_pk_mul_f32 v[112:113], v[96:97], v[112:113] op_sel_hi:[1,0]
	v_cvt_pk_bf16_f32 v96, v108, v109
	v_cvt_pk_bf16_f32 v97, v110, v111
	v_cvt_pk_bf16_f32 v98, v104, v105
	v_cvt_pk_bf16_f32 v99, v106, v107
	global_store_dwordx4 v[116:117], v[96:99], off nt
	s_nop 1
	v_cvt_pk_bf16_f32 v96, v100, v101
	v_cvt_pk_bf16_f32 v97, v102, v103
	v_cvt_pk_bf16_f32 v98, v112, v113
	v_cvt_pk_bf16_f32 v99, v120, v121
	global_store_dwordx4 v[116:117], v[96:99], off offset:256 nt
	s_nop 0
	v_subrev_u32_e32 v100, s52, v114
	v_ashrrev_i32_e32 v101, 31, v100
	v_or_b32_e32 v98, 48, v148
	v_lshlrev_b64 v[100:101], 12, v[100:101]
	v_ashrrev_i32_e32 v99, 31, v98
	v_lshl_add_u64 v[100:101], v[144:145], 0, v[100:101]
	v_lshl_add_u64 v[102:103], v[98:99], 2, s[6:7]
	s_waitcnt vmcnt(9)
	v_mov_b32_e32 v96, v179
	v_pk_mul_f32 v[94:95], v[94:95], v[96:97] op_sel_hi:[1,0]
	v_pk_mul_f32 v[92:93], v[92:93], v[96:97] op_sel_hi:[1,0]
	v_pk_mul_f32 v[90:91], v[90:91], v[96:97] op_sel_hi:[1,0]
	v_pk_mul_f32 v[88:89], v[88:89], v[96:97] op_sel_hi:[1,0]
	v_pk_mul_f32 v[86:87], v[86:87], v[96:97] op_sel_hi:[1,0]
	v_pk_mul_f32 v[84:85], v[84:85], v[96:97] op_sel_hi:[1,0]
	v_pk_mul_f32 v[104:105], v[82:83], v[96:97] op_sel_hi:[1,0]
	v_pk_mul_f32 v[96:97], v[80:81], v[96:97] op_sel_hi:[1,0]
	v_cvt_pk_bf16_f32 v80, v92, v93
	v_cvt_pk_bf16_f32 v81, v94, v95
	v_cvt_pk_bf16_f32 v82, v88, v89
	v_cvt_pk_bf16_f32 v83, v90, v91
	global_store_dwordx4 v[100:101], v[80:83], off nt
	s_nop 1
	v_cvt_pk_bf16_f32 v80, v84, v85
	v_cvt_pk_bf16_f32 v81, v86, v87
	v_cvt_pk_bf16_f32 v82, v96, v97
	v_cvt_pk_bf16_f32 v83, v104, v105
	global_store_dwordx4 v[100:101], v[80:83], off offset:256 nt
	s_nop 0
	s_waitcnt vmcnt(10)
	v_mov_b32_e32 v80, v180
	v_pk_mul_f32 v[78:79], v[78:79], v[80:81] op_sel_hi:[1,0]
	v_subrev_u32_e32 v82, s52, v98
	v_ashrrev_i32_e32 v83, 31, v82
	v_lshlrev_b64 v[82:83], 12, v[82:83]
	v_lshl_add_u64 v[82:83], v[144:145], 0, v[82:83]
	v_pk_mul_f32 v[76:77], v[76:77], v[80:81] op_sel_hi:[1,0]
	v_pk_mul_f32 v[74:75], v[74:75], v[80:81] op_sel_hi:[1,0]
	v_pk_mul_f32 v[72:73], v[72:73], v[80:81] op_sel_hi:[1,0]
	v_pk_mul_f32 v[70:71], v[70:71], v[80:81] op_sel_hi:[1,0]
	v_pk_mul_f32 v[68:69], v[68:69], v[80:81] op_sel_hi:[1,0]
	v_pk_mul_f32 v[84:85], v[66:67], v[80:81] op_sel_hi:[1,0]
	v_pk_mul_f32 v[80:81], v[64:65], v[80:81] op_sel_hi:[1,0]
	v_cvt_pk_bf16_f32 v64, v76, v77
	v_cvt_pk_bf16_f32 v65, v78, v79
	v_cvt_pk_bf16_f32 v66, v72, v73
	v_cvt_pk_bf16_f32 v67, v74, v75
	global_store_dwordx4 v[82:83], v[64:67], off nt
	s_nop 1
	v_cvt_pk_bf16_f32 v64, v68, v69
	v_cvt_pk_bf16_f32 v65, v70, v71
	v_cvt_pk_bf16_f32 v66, v80, v81
	v_cvt_pk_bf16_f32 v67, v84, v85
	global_store_dwordx4 v[82:83], v[64:67], off offset:256 nt
	s_nop 0
	s_waitcnt vmcnt(11)
	v_mov_b32_e32 v64, v181
	v_pk_mul_f32 v[62:63], v[62:63], v[64:65] op_sel_hi:[1,0]
	v_add_u32_e32 v66, 0x80, v142
	v_ashrrev_i32_e32 v67, 31, v66
	v_lshlrev_b64 v[66:67], 12, v[66:67]
	v_lshl_add_u64 v[66:67], v[144:145], 0, v[66:67]
	v_pk_mul_f32 v[60:61], v[60:61], v[64:65] op_sel_hi:[1,0]
	v_pk_mul_f32 v[58:59], v[58:59], v[64:65] op_sel_hi:[1,0]
	v_pk_mul_f32 v[56:57], v[56:57], v[64:65] op_sel_hi:[1,0]
	v_pk_mul_f32 v[54:55], v[54:55], v[64:65] op_sel_hi:[1,0]
	v_pk_mul_f32 v[52:53], v[52:53], v[64:65] op_sel_hi:[1,0]
	v_pk_mul_f32 v[68:69], v[50:51], v[64:65] op_sel_hi:[1,0]
	v_pk_mul_f32 v[64:65], v[48:49], v[64:65] op_sel_hi:[1,0]
	v_cvt_pk_bf16_f32 v48, v60, v61
	v_cvt_pk_bf16_f32 v49, v62, v63
	v_cvt_pk_bf16_f32 v50, v56, v57
	v_cvt_pk_bf16_f32 v51, v58, v59
	global_store_dwordx4 v[66:67], v[48:51], off nt
	s_nop 1
	v_cvt_pk_bf16_f32 v48, v52, v53
	v_cvt_pk_bf16_f32 v49, v54, v55
	v_cvt_pk_bf16_f32 v50, v64, v65
	v_cvt_pk_bf16_f32 v51, v68, v69
	global_store_dwordx4 v[66:67], v[48:51], off offset:256 nt
	s_nop 0
	s_waitcnt vmcnt(12)
	v_mov_b32_e32 v48, v182
	v_pk_mul_f32 v[46:47], v[46:47], v[48:49] op_sel_hi:[1,0]
	v_add_u32_e32 v50, 0x90, v142
	v_ashrrev_i32_e32 v51, 31, v50
	v_lshlrev_b64 v[50:51], 12, v[50:51]
	v_lshl_add_u64 v[50:51], v[144:145], 0, v[50:51]
	v_pk_mul_f32 v[44:45], v[44:45], v[48:49] op_sel_hi:[1,0]
	v_pk_mul_f32 v[42:43], v[42:43], v[48:49] op_sel_hi:[1,0]
	v_pk_mul_f32 v[40:41], v[40:41], v[48:49] op_sel_hi:[1,0]
	v_pk_mul_f32 v[38:39], v[38:39], v[48:49] op_sel_hi:[1,0]
	v_pk_mul_f32 v[36:37], v[36:37], v[48:49] op_sel_hi:[1,0]
	v_pk_mul_f32 v[52:53], v[34:35], v[48:49] op_sel_hi:[1,0]
	v_pk_mul_f32 v[48:49], v[32:33], v[48:49] op_sel_hi:[1,0]
	v_cvt_pk_bf16_f32 v32, v44, v45
	v_cvt_pk_bf16_f32 v33, v46, v47
	v_cvt_pk_bf16_f32 v34, v40, v41
	v_cvt_pk_bf16_f32 v35, v42, v43
	global_store_dwordx4 v[50:51], v[32:35], off nt
	s_nop 1
	v_cvt_pk_bf16_f32 v32, v36, v37
	v_cvt_pk_bf16_f32 v33, v38, v39
	v_cvt_pk_bf16_f32 v34, v48, v49
	v_cvt_pk_bf16_f32 v35, v52, v53
	global_store_dwordx4 v[50:51], v[32:35], off offset:256 nt
	s_nop 0
	s_waitcnt vmcnt(13)
	v_mov_b32_e32 v32, v183
	v_pk_mul_f32 v[30:31], v[30:31], v[32:33] op_sel_hi:[1,0]
	v_add_u32_e32 v34, 0xa0, v142
	v_ashrrev_i32_e32 v35, 31, v34
	v_lshlrev_b64 v[34:35], 12, v[34:35]
	v_lshl_add_u64 v[34:35], v[144:145], 0, v[34:35]
	v_pk_mul_f32 v[28:29], v[28:29], v[32:33] op_sel_hi:[1,0]
	v_pk_mul_f32 v[26:27], v[26:27], v[32:33] op_sel_hi:[1,0]
	v_pk_mul_f32 v[24:25], v[24:25], v[32:33] op_sel_hi:[1,0]
	v_pk_mul_f32 v[22:23], v[22:23], v[32:33] op_sel_hi:[1,0]
	v_pk_mul_f32 v[20:21], v[20:21], v[32:33] op_sel_hi:[1,0]
	v_pk_mul_f32 v[36:37], v[18:19], v[32:33] op_sel_hi:[1,0]
	v_pk_mul_f32 v[32:33], v[16:17], v[32:33] op_sel_hi:[1,0]
	v_cvt_pk_bf16_f32 v16, v28, v29
	v_cvt_pk_bf16_f32 v17, v30, v31
	v_cvt_pk_bf16_f32 v18, v24, v25
	v_cvt_pk_bf16_f32 v19, v26, v27
	global_store_dwordx4 v[34:35], v[16:19], off nt
	s_nop 1
	v_cvt_pk_bf16_f32 v16, v20, v21
	v_cvt_pk_bf16_f32 v17, v22, v23
	v_cvt_pk_bf16_f32 v18, v32, v33
	v_cvt_pk_bf16_f32 v19, v36, v37
	global_store_dwordx4 v[34:35], v[16:19], off offset:256 nt
	s_nop 0
	s_waitcnt vmcnt(14)
	v_mov_b32_e32 v16, v184
	v_pk_mul_f32 v[14:15], v[14:15], v[16:17] op_sel_hi:[1,0]
	v_add_u32_e32 v18, 0xb0, v142
	v_ashrrev_i32_e32 v19, 31, v18
	v_lshlrev_b64 v[18:19], 12, v[18:19]
	v_lshl_add_u64 v[18:19], v[144:145], 0, v[18:19]
	v_pk_mul_f32 v[12:13], v[12:13], v[16:17] op_sel_hi:[1,0]
	v_pk_mul_f32 v[10:11], v[10:11], v[16:17] op_sel_hi:[1,0]
	v_pk_mul_f32 v[8:9], v[8:9], v[16:17] op_sel_hi:[1,0]
	v_pk_mul_f32 v[6:7], v[6:7], v[16:17] op_sel_hi:[1,0]
	v_pk_mul_f32 v[4:5], v[4:5], v[16:17] op_sel_hi:[1,0]
	v_pk_mul_f32 v[20:21], v[2:3], v[16:17] op_sel_hi:[1,0]
	v_pk_mul_f32 v[16:17], v[0:1], v[16:17] op_sel_hi:[1,0]
	v_cvt_pk_bf16_f32 v0, v12, v13
	v_cvt_pk_bf16_f32 v1, v14, v15
	v_cvt_pk_bf16_f32 v2, v8, v9
	v_cvt_pk_bf16_f32 v3, v10, v11
	global_store_dwordx4 v[18:19], v[0:3], off nt
	s_nop 1
	v_cvt_pk_bf16_f32 v0, v4, v5
	v_cvt_pk_bf16_f32 v1, v6, v7
	v_cvt_pk_bf16_f32 v2, v16, v17
	v_cvt_pk_bf16_f32 v3, v20, v21
	global_store_dwordx4 v[18:19], v[0:3], off offset:256 nt
	s_cbranch_vccnz .LBB0_1171
	s_andn2_b64 vcc, exec, s[0:1]
	s_cbranch_vccnz .LBB0_1170
	s_barrier
	s_branch .LBB0_1170
